# mix phase: wave_sum hops via DPP quad_perm/row mirrors + permlane16/32 swap instead of ds_bpermute round trips (bit-identical sums); skew 0; flat-release barrier
# speedup vs baseline: 1.0080x; 1.0066x over previous
; __global__ void __launch_bounds__(512, 2) mega_fwd(Args args) {
;     ...
;             { const unsigned long long t0_ = __builtin_amdgcn_s_memrealtime(); const unsigned long long d_ = (unsigned long long)(PROJ_SKEW_GRP) * (unsigned long long)(PROJ_SKEW_T);
;               while (__builtin_amdgcn_s_memrealtime() - t0_ < d_) __builtin_amdgcn_s_sleep(8); }
.LBB0_211:
	s_memrealtime s[2:3]
	s_memrealtime s[10:11]
	s_bfe_u32 s5, s42, 0x20006
	s_mul_i32 s30, s5, 0x0
	v_mov_b64_e32 v[0:1], s[30:31]
	s_waitcnt lgkmcnt(0)
	s_sub_u32 s10, s10, s2
	s_subb_u32 s11, s11, s3
	v_cmp_ge_u64_e32 vcc, s[10:11], v[0:1]
	s_cbranch_vccnz .LBB0_213

; #define GAS __attribute__((address_space(1)))
; __device__ __forceinline__ float bflo(unsigned w) { return __uint_as_float(w << 16); }
; __device__ __forceinline__ float bfhi(unsigned w) { return __uint_as_float(w & 0xffff0000u); }
; template <bool F8> __device__ __forceinline__ void mix_phase(const Ctx& C, const bf16* YCONV, const bf16* YSWA, const bf16* ODIFF, const float* conv_g, const float* swa_g, const float* lq1, const float* lk1, const float* lq2, const float* lk2, ...
;     bf16* MIX = (bf16*)MIX8; constexpr float SMX_ = F8 ? SMX : 1.0f;
;     const float lam = __expf(wave_sum(lq1[C.lane] * lk1[C.lane])) - __expf(wave_sum(lq2[C.lane] * lk2[C.lane])) + lambda_init;
;     const float osc = 1.0f - lambda_init;
;     const int l = C.lane;
;     const int vh = l >> 5, dd = 2 * (l & 31); const float gA = sub_g[2 * l] * (osc * SMX_), gB = sub_g[2 * l + 1] * (osc * SMX_);
;     const f32x4 cg0 = *(const GAS f32x4*)(conv_g + 8 * l) * SMX_, cg1 = *(const GAS f32x4*)(conv_g + 8 * l + 4) * SMX_;
;     const f32x4 sg0 = *(const GAS f32x4*)(swa_g + 8 * l) * SMX_, sg1 = *(const GAS f32x4*)(swa_g + 8 * l + 4) * SMX_, sg2 = *(const GAS f32x4*)(swa_g + 512 + 4 * l) * SMX_;
;     constexpr int NR = 2;
;     for (int m0 = C.gw; m0 < T; m0 += NR * C.NGW) {
;         v4u yc[NR], ys[NR]; v2u ys2[NR]; unsigned oa[NR][6], ob[NR][6];
; #pragma unroll
;         for (int q = 0; q < NR; ++q) { const int m = m0 + q * C.NGW;
;             yc[q] = *(const GAS v4u*)(YCONV + (size_t)m * 512 + 8 * l); ys[q] = *(const GAS v4u*)(YSWA + (size_t)m * 768 + 8 * l); ys2[q] = *(const GAS v2u*)(YSWA + (size_t)m * 768 + 512 + 4 * l);
; #pragma unroll
;             for (int h = 0; h < 6; ++h) { const bf16* op = ODIFF + (size_t)m * 1536 + 64 * (4 * h + vh) + dd; oa[q][h] = *(const GAS unsigned*)op; ob[q][h] = *(const GAS unsigned*)(op + 128); } }
; #pragma unroll
;         for (int q = 0; q < NR; ++q) { const int m = m0 + q * C.NGW;
;             { const v4u y = yc[q];
;               float f[8] = {bflo(y.x), bfhi(y.x), bflo(y.y), bfhi(y.y), bflo(y.z), bfhi(y.z), bflo(y.w), bfhi(y.w)}; float ss = 0.f;
; #pragma unroll
;               for (int i = 0; i < 8; ++i) ss += f[i] * f[i];
;               const float r = 1.0f / sqrtf(wave_sum(ss) * (1.0f / 512.0f) + RMS_EPS);
.LBB0_718:
	v_lshl_add_u64 v[24:25], v[62:63], 0, s[10:11]
	v_add_co_u32_e32 v24, vcc, s19, v24
	v_lshl_add_u64 v[86:87], v[62:63], 0, v[64:65]
	s_nop 0
	v_addc_co_u32_e32 v25, vcc, -1, v25, vcc
	global_load_dwordx4 v[36:39], v[24:25], off offset:-2048
	v_lshl_add_u64 v[24:25], v[62:63], 0, s[6:7]
	v_add_co_u32_e32 v24, vcc, s20, v24
	v_lshl_add_u64 v[96:97], s[12:13], 0, v[48:49]
	s_nop 0
	v_addc_co_u32_e32 v25, vcc, -1, v25, vcc
	global_load_dwordx4 v[32:35], v[24:25], off offset:-2048
	v_lshl_add_u64 v[24:25], v[62:63], 0, v[84:85]
	v_add_co_u32_e32 v24, vcc, s20, v24
	s_addk_i32 s16, 0x1000
	s_nop 0
	v_addc_co_u32_e32 v25, vcc, -1, v25, vcc
	global_load_dwordx2 v[88:89], v[24:25], off offset:-1024
	v_lshl_add_u64 v[24:25], s[12:13], 0, v[72:73]
	v_add_co_u32_e32 v24, vcc, s21, v24
	v_lshl_add_u64 v[48:49], v[48:49], 0, s[26:27]
	s_nop 0
	v_addc_co_u32_e32 v25, vcc, 0, v25, vcc
	global_load_dword v117, v[24:25], off
	global_load_dword v118, v[24:25], off offset:256
	v_lshl_add_u64 v[24:25], s[12:13], 0, v[74:75]
	v_add_co_u32_e32 v24, vcc, s21, v24
	v_lshl_add_u64 v[64:65], v[64:65], 0, s[28:29]
	s_nop 0
	v_addc_co_u32_e32 v25, vcc, 0, v25, vcc
	global_load_dword v115, v[24:25], off
	global_load_dword v116, v[24:25], off offset:256
	v_lshl_add_u64 v[24:25], s[12:13], 0, v[76:77]
	v_add_co_u32_e32 v24, vcc, s21, v24
	v_lshl_add_u64 v[72:73], v[72:73], 0, s[26:27]
	s_nop 0
	v_addc_co_u32_e32 v25, vcc, 0, v25, vcc
	global_load_dword v113, v[24:25], off
	global_load_dword v114, v[24:25], off offset:256
	v_lshl_add_u64 v[24:25], s[12:13], 0, v[78:79]
	v_add_co_u32_e32 v24, vcc, s21, v24
	v_lshl_add_u64 v[74:75], v[74:75], 0, s[26:27]
	s_nop 0
	v_addc_co_u32_e32 v25, vcc, 0, v25, vcc
	global_load_dword v111, v[24:25], off
	global_load_dword v112, v[24:25], off offset:256
	v_lshl_add_u64 v[24:25], s[12:13], 0, v[80:81]
	v_add_co_u32_e32 v24, vcc, s21, v24
	v_lshl_add_u64 v[76:77], v[76:77], 0, s[26:27]
	s_nop 0
	v_addc_co_u32_e32 v25, vcc, 0, v25, vcc
	global_load_dword v109, v[24:25], off
	global_load_dword v110, v[24:25], off offset:256
	v_lshl_add_u64 v[24:25], s[12:13], 0, v[82:83]
	v_add_co_u32_e32 v24, vcc, s21, v24
	v_lshl_add_u64 v[78:79], v[78:79], 0, s[26:27]
	s_nop 0
	v_addc_co_u32_e32 v25, vcc, 0, v25, vcc
	global_load_dword v107, v[24:25], off
	global_load_dword v108, v[24:25], off offset:256
	v_lshl_add_u64 v[24:25], v[62:63], 0, s[8:9]
	v_add_co_u32_e32 v24, vcc, s19, v24
	v_lshl_add_u64 v[80:81], v[80:81], 0, s[26:27]
	s_nop 0
	v_addc_co_u32_e32 v25, vcc, -1, v25, vcc
	global_load_dwordx4 v[28:31], v[24:25], off offset:-2048
	v_lshl_add_u64 v[24:25], v[62:63], 0, s[4:5]
	v_add_co_u32_e32 v24, vcc, s20, v24
	s_add_u32 s4, s4, 0x600000
	s_nop 0
	v_addc_co_u32_e32 v25, vcc, -1, v25, vcc
	v_add_co_u32_e32 v86, vcc, s20, v86
	global_load_dwordx4 v[24:27], v[24:25], off offset:-2048
	s_nop 0
	v_addc_co_u32_e32 v87, vcc, -1, v87, vcc
	v_add_co_u32_e32 v96, vcc, s21, v96
	global_load_dwordx2 v[86:87], v[86:87], off offset:-1024
	s_nop 0
	v_addc_co_u32_e32 v97, vcc, 0, v97, vcc
	global_load_dword v105, v[96:97], off
	global_load_dword v106, v[96:97], off offset:256
	v_lshl_add_u64 v[96:97], s[12:13], 0, v[50:51]
	v_add_co_u32_e32 v96, vcc, s21, v96
	s_waitcnt vmcnt(19)
	v_lshlrev_b32_e32 v130, 16, v36
	v_addc_co_u32_e32 v97, vcc, 0, v97, vcc
	global_load_dword v103, v[96:97], off
	global_load_dword v104, v[96:97], off offset:256
	v_lshl_add_u64 v[96:97], s[12:13], 0, v[52:53]
	v_add_co_u32_e32 v96, vcc, s21, v96
	v_and_b32_e32 v131, 0xffff0000, v36
	s_nop 0
	v_addc_co_u32_e32 v97, vcc, 0, v97, vcc
	global_load_dword v101, v[96:97], off
	global_load_dword v102, v[96:97], off offset:256
	v_lshl_add_u64 v[96:97], s[12:13], 0, v[54:55]
	v_add_co_u32_e32 v96, vcc, s21, v96
	v_lshlrev_b32_e32 v126, 16, v37
	s_nop 0
	v_addc_co_u32_e32 v97, vcc, 0, v97, vcc
	global_load_dword v99, v[96:97], off
	global_load_dword v100, v[96:97], off offset:256
	v_lshl_add_u64 v[96:97], s[12:13], 0, v[56:57]
	v_add_co_u32_e32 v120, vcc, s21, v96
	v_and_b32_e32 v127, 0xffff0000, v37
	s_nop 0
	v_addc_co_u32_e32 v121, vcc, 0, v97, vcc
	global_load_dword v97, v[120:121], off
	global_load_dword v98, v[120:121], off offset:256
	v_lshl_add_u64 v[120:121], s[12:13], 0, v[60:61]
	v_pk_mul_f32 v[36:37], v[130:131], v[130:131]
	v_add_co_u32_e32 v120, vcc, s21, v120
	v_pk_mul_f32 v[128:129], v[126:127], v[126:127]
	v_add_f32_e32 v36, v36, v37
	v_addc_co_u32_e32 v121, vcc, 0, v121, vcc
	v_lshlrev_b32_e32 v124, 16, v38
	v_and_b32_e32 v125, 0xffff0000, v38
	v_add_f32_e32 v36, v128, v36
	global_load_dword v95, v[120:121], off
	global_load_dword v96, v[120:121], off offset:256
	v_lshlrev_b32_e32 v120, 16, v39
	v_and_b32_e32 v121, 0xffff0000, v39
	v_pk_mul_f32 v[38:39], v[124:125], v[124:125]
	v_add_f32_e32 v36, v129, v36
	v_add_f32_e32 v36, v38, v36
	v_pk_mul_f32 v[122:123], v[120:121], v[120:121]
	v_add_f32_e32 v36, v39, v36
	v_add_f32_e32 v36, v122, v36
	v_add_f32_e32 v36, v123, v36
	s_nop 1
	v_mov_b32_dpp v37, v36 quad_perm:[1,0,3,2] row_mask:0xf bank_mask:0xf
	s_waitcnt vmcnt(28)
	v_lshlrev_b32_e32 v134, 16, v32
	v_and_b32_e32 v135, 0xffff0000, v32
	v_lshlrev_b32_e32 v128, 16, v34
	v_and_b32_e32 v129, 0xffff0000, v34
	s_waitcnt lgkmcnt(0)
	v_add_f32_e32 v36, v36, v37
	s_nop 1
	v_mov_b32_dpp v37, v36 quad_perm:[2,3,0,1] row_mask:0xf bank_mask:0xf
	s_addc_u32 s5, s5, 0
	s_add_u32 s8, s8, 0x400000
	s_addc_u32 s9, s9, 0
	s_add_u32 s6, s6, 0x600000
	s_waitcnt lgkmcnt(0)
	v_add_f32_e32 v36, v36, v37
	s_nop 1
	v_mov_b32_dpp v37, v36 row_half_mirror row_mask:0xf bank_mask:0xf
	s_addc_u32 s7, s7, 0
	s_add_u32 s10, s10, 0x400000
	s_addc_u32 s11, s11, 0
	v_lshl_add_u64 v[50:51], v[50:51], 0, s[26:27]
	s_waitcnt lgkmcnt(0)
; template <bool F8> __device__ __forceinline__ void mix_phase(const Ctx& C, const bf16* YCONV, const bf16* YSWA, const bf16* ODIFF, const float* conv_g, const float* swa_g, const float* lq1, const float* lk1, const float* lq2, const float* lk2, ...
;     ...
;             { const v4u y = yc[q];
;               float f[8] = {bflo(y.x), bfhi(y.x), bflo(y.y), bfhi(y.y), bflo(y.z), bfhi(y.z), bflo(y.w), bfhi(y.w)}; float ss = 0.f;
; #pragma unroll
;               for (int i = 0; i < 8; ++i) ss += f[i] * f[i];
;               const float r = 1.0f / sqrtf(wave_sum(ss) * (1.0f / 512.0f) + RMS_EPS);
;               if constexpr (F8) { v2u o; o.x = pk4_fp8m(f[0] * r * cg0.x, f[1] * r * cg0.y, f[2] * r * cg0.z, f[3] * r * cg0.w); o.y = pk4_fp8m(f[4] * r * cg1.x, f[5] * r * cg1.y, f[6] * r * cg1.z, f[7] * r * cg1.w);
;                 *(GAS v2u*)(MIX8 + (size_t)m * DM + 8 * l) = o; }
;               else { v4u o; o.x = pk2(f[0] * r * cg0.x, f[1] * r * cg0.y); o.y = pk2(f[2] * r * cg0.z, f[3] * r * cg0.w); o.z = pk2(f[4] * r * cg1.x, f[5] * r * cg1.y); o.w = pk2(f[6] * r * cg1.z, f[7] * r * cg1.w);
;                 *(GAS v4u*)(MIX + (size_t)m * DM + 8 * l) = o; } }
;             { const v4u y = ys[q]; const v2u y2 = ys2[q];
;               float f[12] = {bflo(y.x), bfhi(y.x), bflo(y.y), bfhi(y.y), bflo(y.z), bfhi(y.z), bflo(y.w), bfhi(y.w), bflo(y2.x), bfhi(y2.x), bflo(y2.y), bfhi(y2.y)}; float ss = 0.f;
; #pragma unroll
;               for (int i = 0; i < 12; ++i) ss += f[i] * f[i];
;               const float r = 1.0f / sqrtf(wave_sum(ss) * (1.0f / 768.0f) + RMS_EPS);
;               if constexpr (F8) { v2u o; o.x = pk4_fp8m(f[0] * r * sg0.x, f[1] * r * sg0.y, f[2] * r * sg0.z, f[3] * r * sg0.w); o.y = pk4_fp8m(f[4] * r * sg1.x, f[5] * r * sg1.y, f[6] * r * sg1.z, f[7] * r * sg1.w);
;                 const unsigned o2 = pk4_fp8m(f[8] * r * sg2.x, f[9] * r * sg2.y, f[10] * r * sg2.z, f[11] * r * sg2.w);
;                 *(GAS v2u*)(MIX8 + (size_t)m * DM + 512 + 8 * l) = o; *(GAS unsigned*)(MIX8 + (size_t)m * DM + 1024 + 4 * l) = o2; }
;               else { v4u o; o.x = pk2(f[0] * r * sg0.x, f[1] * r * sg0.y); o.y = pk2(f[2] * r * sg0.z, f[3] * r * sg0.w); o.z = pk2(f[4] * r * sg1.x, f[5] * r * sg1.y); o.w = pk2(f[6] * r * sg1.z, f[7] * r * sg1.w);
;                 v2u o2; o2.x = pk2(f[8] * r * sg2.x, f[9] * r * sg2.y); o2.y = pk2(f[10] * r * sg2.z, f[11] * r * sg2.w);
	v_add_f32_e32 v36, v36, v37
	s_nop 1
	v_mov_b32_dpp v37, v36 row_mirror row_mask:0xf bank_mask:0xf
	v_lshl_add_u64 v[52:53], v[52:53], 0, s[26:27]
	v_lshl_add_u64 v[54:55], v[54:55], 0, s[26:27]
	v_lshl_add_u64 v[56:57], v[56:57], 0, s[26:27]
	v_lshl_add_u64 v[60:61], v[60:61], 0, s[26:27]
	s_waitcnt lgkmcnt(0)
	v_add_f32_e32 v36, v36, v37
	v_mov_b32_e32 v37, v36
	s_nop 1
	v_permlane16_swap_b32_e32 v36, v37
	v_lshl_add_u64 v[82:83], v[82:83], 0, s[26:27]
	v_lshl_add_u64 v[84:85], v[84:85], 0, s[28:29]
	s_cmpk_lt_i32 s16, 0x3000
	s_waitcnt lgkmcnt(0)
	v_add_f32_e32 v36, v36, v37
	v_mov_b32_e32 v37, v36
	s_nop 1
	v_permlane32_swap_b32_e32 v36, v37
	s_waitcnt lgkmcnt(0)
	v_add_f32_e32 v36, v36, v37
	v_fmamk_f32 v36, v36, 0x3b000000, v212
	v_cmp_gt_f32_e32 vcc, s18, v36
	v_mul_f32_e32 v37, 0x4f800000, v36
	s_nop 0
	v_cndmask_b32_e32 v36, v36, v37, vcc
	v_sqrt_f32_e32 v37, v36
	s_nop 0
	v_add_u32_e32 v38, -1, v37
	v_fma_f32 v39, -v38, v37, v36
	v_cmp_ge_f32_e64 s[2:3], 0, v39
	v_add_u32_e32 v39, 1, v37
	s_nop 0
	v_cndmask_b32_e64 v38, v37, v38, s[2:3]
	v_fma_f32 v37, -v39, v37, v36
	v_cmp_lt_f32_e64 s[2:3], 0, v37
	s_nop 1
	v_cndmask_b32_e64 v37, v38, v39, s[2:3]
	v_mul_f32_e32 v38, 0x37800000, v37
	v_cndmask_b32_e32 v37, v37, v38, vcc
	v_cmp_class_f32_e32 vcc, v36, v211
	s_nop 1
	v_cndmask_b32_e32 v36, v37, v36, vcc
	v_div_scale_f32 v37, s[2:3], v36, v36, 1.0
	v_rcp_f32_e32 v38, v37
	s_nop 0
	v_fma_f32 v39, -v37, v38, 1.0
	v_fmac_f32_e32 v38, v39, v38
	v_div_scale_f32 v39, vcc, 1.0, v36, 1.0
	v_mul_f32_e32 v119, v39, v38
	v_fma_f32 v122, -v37, v119, v39
	v_fmac_f32_e32 v119, v122, v38
	v_fma_f32 v37, -v37, v119, v39
	v_div_fmas_f32 v37, v37, v38, v119
	v_div_fixup_f32 v122, v37, v36, 1.0
	v_pk_mul_f32 v[36:37], v[122:123], v[130:131] op_sel_hi:[0,1]
	v_pk_mul_f32 v[38:39], v[122:123], v[126:127] op_sel_hi:[0,1]
	v_lshlrev_b32_e32 v130, 16, v33
	v_and_b32_e32 v131, 0xffff0000, v33
	v_pk_mul_f32 v[32:33], v[134:135], v[134:135]
	v_pk_mul_f32 v[36:37], v[16:17], v[36:37]
	v_pk_mul_f32 v[38:39], v[18:19], v[38:39]
	v_pk_mul_f32 v[132:133], v[130:131], v[130:131]
	v_add_f32_e32 v32, v32, v33
	v_cvt_pk_bf16_f32 v36, v36, v37
	v_cvt_pk_bf16_f32 v37, v38, v39
	v_pk_mul_f32 v[38:39], v[122:123], v[124:125] op_sel_hi:[0,1]
	v_pk_mul_f32 v[120:121], v[122:123], v[120:121] op_sel_hi:[0,1]
	v_add_f32_e32 v32, v132, v32
	v_pk_mul_f32 v[38:39], v[20:21], v[38:39]
	v_pk_mul_f32 v[120:121], v[22:23], v[120:121]
	v_lshlrev_b32_e32 v124, 16, v35
	v_and_b32_e32 v125, 0xffff0000, v35
	v_pk_mul_f32 v[34:35], v[128:129], v[128:129]
	v_add_f32_e32 v32, v133, v32
	v_cvt_pk_bf16_f32 v38, v38, v39
	v_cvt_pk_bf16_f32 v39, v120, v121
	v_lshl_add_u64 v[120:121], s[12:13], 0, v[70:71]
	v_add_f32_e32 v32, v34, v32
	v_add_co_u32_e32 v120, vcc, s22, v120
	v_pk_mul_f32 v[126:127], v[124:125], v[124:125]
	v_add_f32_e32 v32, v35, v32
	v_addc_co_u32_e32 v121, vcc, 0, v121, vcc
	s_waitcnt vmcnt(27)
	v_lshlrev_b32_e32 v122, 16, v88
	v_and_b32_e32 v123, 0xffff0000, v88
	v_add_f32_e32 v32, v126, v32
	global_store_dwordx4 v[120:121], v[36:39], off
	v_add_f32_e32 v32, v127, v32
	v_lshl_add_u64 v[70:71], v[70:71], 0, s[24:25]
	v_lshlrev_b32_e32 v38, 16, v89
	v_and_b32_e32 v39, 0xffff0000, v89
	v_pk_mul_f32 v[88:89], v[122:123], v[122:123]
	v_pk_mul_f32 v[36:37], v[38:39], v[38:39]
	v_add_f32_e32 v32, v88, v32
	v_add_f32_e32 v32, v89, v32
	v_add_f32_e32 v32, v36, v32
	v_add_f32_e32 v32, v37, v32
	s_nop 1
	v_mov_b32_dpp v33, v32 quad_perm:[1,0,3,2] row_mask:0xf bank_mask:0xf
	s_waitcnt lgkmcnt(0)
	v_add_f32_e32 v32, v32, v33
	s_nop 1
	v_mov_b32_dpp v33, v32 quad_perm:[2,3,0,1] row_mask:0xf bank_mask:0xf
	s_waitcnt lgkmcnt(0)
	v_add_f32_e32 v32, v32, v33
	s_nop 1
	v_mov_b32_dpp v33, v32 row_half_mirror row_mask:0xf bank_mask:0xf
	s_waitcnt lgkmcnt(0)
	v_add_f32_e32 v32, v32, v33
	s_nop 1
	v_mov_b32_dpp v33, v32 row_mirror row_mask:0xf bank_mask:0xf
	s_waitcnt lgkmcnt(0)
	v_add_f32_e32 v32, v32, v33
	v_mov_b32_e32 v33, v32
	s_nop 1
	v_permlane16_swap_b32_e32 v32, v33
	s_waitcnt lgkmcnt(0)
	v_add_f32_e32 v32, v32, v33
	v_mov_b32_e32 v33, v32
	s_nop 1
	v_permlane32_swap_b32_e32 v32, v33
	s_waitcnt lgkmcnt(0)
	v_add_f32_e32 v32, v32, v33
	v_fmamk_f32 v32, v32, 0x3aaaaaab, v212
	v_cmp_gt_f32_e32 vcc, s18, v32
	v_mul_f32_e32 v33, 0x4f800000, v32
	s_nop 0
	v_cndmask_b32_e32 v32, v32, v33, vcc
	v_sqrt_f32_e32 v33, v32
	s_nop 0
	v_add_u32_e32 v34, -1, v33
	v_fma_f32 v35, -v34, v33, v32
	v_cmp_ge_f32_e64 s[2:3], 0, v35
	v_add_u32_e32 v35, 1, v33
	s_nop 0
	v_cndmask_b32_e64 v34, v33, v34, s[2:3]
	v_fma_f32 v33, -v35, v33, v32
	v_cmp_lt_f32_e64 s[2:3], 0, v33
	s_nop 1
	v_cndmask_b32_e64 v33, v34, v35, s[2:3]
	v_mul_f32_e32 v34, 0x37800000, v33
	v_cndmask_b32_e32 v33, v33, v34, vcc
	v_cmp_class_f32_e32 vcc, v32, v211
	s_nop 1
	v_cndmask_b32_e32 v32, v33, v32, vcc
	v_div_scale_f32 v33, s[2:3], v32, v32, 1.0
	v_rcp_f32_e32 v34, v33
	s_nop 0
	v_fma_f32 v35, -v33, v34, 1.0
	v_fmac_f32_e32 v34, v35, v34
	v_div_scale_f32 v35, vcc, 1.0, v32, 1.0
	v_mul_f32_e32 v36, v35, v34
	v_fma_f32 v37, -v33, v36, v35
	v_fmac_f32_e32 v36, v37, v34
	v_fma_f32 v33, -v33, v36, v35
	v_div_fmas_f32 v33, v33, v34, v36
	v_div_fixup_f32 v88, v33, v32, 1.0
	v_pk_mul_f32 v[32:33], v[88:89], v[134:135] op_sel_hi:[0,1]
	v_pk_mul_f32 v[32:33], v[8:9], v[32:33]
	v_pk_mul_f32 v[38:39], v[88:89], v[38:39] op_sel_hi:[0,1]
	v_cvt_pk_bf16_f32 v34, v32, v33
	v_pk_mul_f32 v[32:33], v[88:89], v[130:131] op_sel_hi:[0,1]
	v_pk_mul_f32 v[32:33], v[10:11], v[32:33]
	v_pk_mul_f32 v[38:39], v[6:7], v[38:39]
	v_cvt_pk_bf16_f32 v35, v32, v33
	v_pk_mul_f32 v[32:33], v[88:89], v[128:129] op_sel_hi:[0,1]
	v_pk_mul_f32 v[32:33], v[12:13], v[32:33]
	s_nop 0
	v_cvt_pk_bf16_f32 v36, v32, v33
	v_pk_mul_f32 v[32:33], v[88:89], v[124:125] op_sel_hi:[0,1]
	v_pk_mul_f32 v[32:33], v[14:15], v[32:33]
	s_nop 0
	v_cvt_pk_bf16_f32 v37, v32, v33
	v_pk_mul_f32 v[32:33], v[88:89], v[122:123] op_sel_hi:[0,1]
	v_pk_mul_f32 v[32:33], v[4:5], v[32:33]
	global_store_dwordx4 v[120:121], v[34:37], off offset:1024
	v_cvt_pk_bf16_f32 v32, v32, v33
	v_cvt_pk_bf16_f32 v33, v38, v39
	v_lshl_add_u64 v[34:35], s[12:13], 0, v[68:69]
	global_store_dwordx2 v[34:35], v[32:33], off
	s_waitcnt vmcnt(29)
; #define GAS __attribute__((address_space(1)))
; __device__ __forceinline__ unsigned pk2(float lo, float hi) { f32x2_m v = {lo, hi}; bf16x2_m b = __builtin_convertvector(v, bf16x2_m); return __builtin_bit_cast(unsigned, b); }
; __device__ __forceinline__ float bflo(unsigned w) { return __uint_as_float(w << 16); }
; __device__ __forceinline__ float bfhi(unsigned w) { return __uint_as_float(w & 0xffff0000u); }
; template <bool F8> __device__ __forceinline__ void mix_phase(const Ctx& C, const bf16* YCONV, const bf16* YSWA, const bf16* ODIFF, const float* conv_g, const float* swa_g, const float* lq1, const float* lk1, const float* lq2, const float* lk2, ...
;     ...
; #pragma unroll
;             for (int h = 0; h < 6; ++h) { const unsigned a = oa[q][h], bq = ob[q][h];
;                 const float v0 = bflo(a) - lam * bflo(bq), v1 = bfhi(a) - lam * bfhi(bq);
;                 const float r = 1.0f / sqrtf(wave_sum(v0 * v0 + v1 * v1) * (1.0f / 128.0f) + LN_EPS);
;                 if constexpr (F8) *(GAS unsigned short*)(MIX8 + (size_t)m * DM + 1280 + 128 * h + 2 * l) = (unsigned short)pk4_fp8m(v0 * r * gA, v1 * r * gB, 0.f, 0.f);
;                 else *(GAS unsigned*)(MIX + (size_t)m * DM + 1280 + 128 * h + 2 * l) = pk2(v0 * r * gA, v1 * r * gB); } }
	v_lshlrev_b32_e32 v34, 16, v117
	s_waitcnt vmcnt(28)
	v_lshlrev_b32_e32 v36, 16, v118
	v_and_b32_e32 v35, 0xffff0000, v117
	v_and_b32_e32 v37, 0xffff0000, v118
	v_pk_fma_f32 v[34:35], v[40:41], v[36:37], v[34:35] neg_lo:[1,0,0] neg_hi:[1,0,0]
	v_lshl_add_u64 v[32:33], s[12:13], 0, v[66:67]
	v_pk_mul_f32 v[36:37], v[34:35], v[34:35]
	v_lshl_add_u64 v[66:67], v[66:67], 0, s[24:25]
	v_add_f32_e32 v36, v36, v37
	s_nop 1
	v_mov_b32_dpp v37, v36 quad_perm:[1,0,3,2] row_mask:0xf bank_mask:0xf
	v_lshl_add_u64 v[68:69], v[68:69], 0, s[24:25]
	s_waitcnt lgkmcnt(0)
	v_add_f32_e32 v36, v36, v37
	s_nop 1
	v_mov_b32_dpp v37, v36 quad_perm:[2,3,0,1] row_mask:0xf bank_mask:0xf
	s_waitcnt lgkmcnt(0)
	v_add_f32_e32 v36, v36, v37
	s_nop 1
	v_mov_b32_dpp v37, v36 row_half_mirror row_mask:0xf bank_mask:0xf
	s_waitcnt lgkmcnt(0)
	v_add_f32_e32 v36, v36, v37
	s_nop 1
	v_mov_b32_dpp v37, v36 row_mirror row_mask:0xf bank_mask:0xf
	s_waitcnt lgkmcnt(0)
	v_add_f32_e32 v36, v36, v37
	v_mov_b32_e32 v37, v36
	s_nop 1
	v_permlane16_swap_b32_e32 v36, v37
	s_waitcnt lgkmcnt(0)
	v_add_f32_e32 v36, v36, v37
	v_mov_b32_e32 v37, v36
	s_nop 1
	v_permlane32_swap_b32_e32 v36, v37
	s_waitcnt lgkmcnt(0)
	v_add_f32_e32 v36, v36, v37
	v_fmamk_f32 v36, v36, 0x3c000000, v210
	v_cmp_gt_f32_e32 vcc, s18, v36
	v_mul_f32_e32 v37, 0x4f800000, v36
	s_nop 0
	v_cndmask_b32_e32 v36, v36, v37, vcc
	v_sqrt_f32_e32 v37, v36
	s_nop 0
	v_add_u32_e32 v38, -1, v37
	v_fma_f32 v39, -v38, v37, v36
	v_cmp_ge_f32_e64 s[2:3], 0, v39
	v_add_u32_e32 v39, 1, v37
	s_nop 0
	v_cndmask_b32_e64 v38, v37, v38, s[2:3]
	v_fma_f32 v37, -v39, v37, v36
	v_cmp_lt_f32_e64 s[2:3], 0, v37
	s_nop 1
	v_cndmask_b32_e64 v37, v38, v39, s[2:3]
	v_mul_f32_e32 v38, 0x37800000, v37
	v_cndmask_b32_e32 v37, v37, v38, vcc
	v_cmp_class_f32_e32 vcc, v36, v211
	s_nop 1
	v_cndmask_b32_e32 v36, v37, v36, vcc
	v_div_scale_f32 v37, s[2:3], v36, v36, 1.0
	v_rcp_f32_e32 v38, v37
	s_nop 0
	v_fma_f32 v39, -v37, v38, 1.0
	v_fmac_f32_e32 v38, v39, v38
	v_div_scale_f32 v39, vcc, 1.0, v36, 1.0
	v_mul_f32_e32 v88, v39, v38
	v_fma_f32 v89, -v37, v88, v39
	v_fmac_f32_e32 v88, v89, v38
	v_fma_f32 v37, -v37, v88, v39
	v_div_fmas_f32 v37, v37, v38, v88
	v_div_fixup_f32 v36, v37, v36, 1.0
	v_pk_mul_f32 v[34:35], v[34:35], v[36:37] op_sel_hi:[1,0]
	v_add_co_u32_e32 v32, vcc, s22, v32
	v_pk_mul_f32 v[34:35], v[58:59], v[34:35]
	s_nop 0
	v_addc_co_u32_e32 v33, vcc, 0, v33, vcc
	v_cvt_pk_bf16_f32 v34, v34, v35
	global_store_dword v[32:33], v34, off offset:2560
	s_waitcnt vmcnt(28)
	v_lshlrev_b32_e32 v34, 16, v115
	s_waitcnt vmcnt(27)
	v_lshlrev_b32_e32 v36, 16, v116
	v_and_b32_e32 v35, 0xffff0000, v115
	v_and_b32_e32 v37, 0xffff0000, v116
	v_pk_fma_f32 v[34:35], v[40:41], v[36:37], v[34:35] neg_lo:[1,0,0] neg_hi:[1,0,0]
	s_nop 0
	v_pk_mul_f32 v[36:37], v[34:35], v[34:35]
	s_nop 0
	v_add_f32_e32 v36, v36, v37
	s_nop 1
	v_mov_b32_dpp v37, v36 quad_perm:[1,0,3,2] row_mask:0xf bank_mask:0xf
	s_waitcnt lgkmcnt(0)
	v_add_f32_e32 v36, v36, v37
	s_nop 1
	v_mov_b32_dpp v37, v36 quad_perm:[2,3,0,1] row_mask:0xf bank_mask:0xf
	s_waitcnt lgkmcnt(0)
	v_add_f32_e32 v36, v36, v37
	s_nop 1
	v_mov_b32_dpp v37, v36 row_half_mirror row_mask:0xf bank_mask:0xf
	s_waitcnt lgkmcnt(0)
	v_add_f32_e32 v36, v36, v37
	s_nop 1
	v_mov_b32_dpp v37, v36 row_mirror row_mask:0xf bank_mask:0xf
	s_waitcnt lgkmcnt(0)
	v_add_f32_e32 v36, v36, v37
	v_mov_b32_e32 v37, v36
	s_nop 1
	v_permlane16_swap_b32_e32 v36, v37
	s_waitcnt lgkmcnt(0)
	v_add_f32_e32 v36, v36, v37
	v_mov_b32_e32 v37, v36
	s_nop 1
	v_permlane32_swap_b32_e32 v36, v37
	s_waitcnt lgkmcnt(0)
	v_add_f32_e32 v36, v36, v37
	v_fmamk_f32 v36, v36, 0x3c000000, v210
	v_cmp_gt_f32_e32 vcc, s18, v36
	v_mul_f32_e32 v37, 0x4f800000, v36
	s_nop 0
	v_cndmask_b32_e32 v36, v36, v37, vcc
	v_sqrt_f32_e32 v37, v36
	s_nop 0
	v_add_u32_e32 v38, -1, v37
	v_fma_f32 v39, -v38, v37, v36
	v_cmp_ge_f32_e64 s[2:3], 0, v39
	v_add_u32_e32 v39, 1, v37
	s_nop 0
	v_cndmask_b32_e64 v38, v37, v38, s[2:3]
	v_fma_f32 v37, -v39, v37, v36
	v_cmp_lt_f32_e64 s[2:3], 0, v37
	s_nop 1
	v_cndmask_b32_e64 v37, v38, v39, s[2:3]
	v_mul_f32_e32 v38, 0x37800000, v37
	v_cndmask_b32_e32 v37, v37, v38, vcc
	v_cmp_class_f32_e32 vcc, v36, v211
	s_nop 1
	v_cndmask_b32_e32 v36, v37, v36, vcc
	v_div_scale_f32 v37, s[2:3], v36, v36, 1.0
	v_rcp_f32_e32 v38, v37
	s_nop 0
	v_fma_f32 v39, -v37, v38, 1.0
	v_fmac_f32_e32 v38, v39, v38
	v_div_scale_f32 v39, vcc, 1.0, v36, 1.0
	v_mul_f32_e32 v88, v39, v38
	v_fma_f32 v89, -v37, v88, v39
	v_fmac_f32_e32 v88, v89, v38
	v_fma_f32 v37, -v37, v88, v39
	v_div_fmas_f32 v37, v37, v38, v88
	v_div_fixup_f32 v36, v37, v36, 1.0
	v_pk_mul_f32 v[34:35], v[34:35], v[36:37] op_sel_hi:[1,0]
	s_waitcnt vmcnt(25)
	v_lshlrev_b32_e32 v36, 16, v114
	v_pk_mul_f32 v[34:35], v[58:59], v[34:35]
	v_and_b32_e32 v37, 0xffff0000, v114
	v_cvt_pk_bf16_f32 v34, v34, v35
	global_store_dword v[32:33], v34, off offset:2816
	v_lshlrev_b32_e32 v34, 16, v113
	v_and_b32_e32 v35, 0xffff0000, v113
	v_pk_fma_f32 v[34:35], v[40:41], v[36:37], v[34:35] neg_lo:[1,0,0] neg_hi:[1,0,0]
	s_waitcnt vmcnt(18)
	v_and_b32_e32 v113, 0xffff0000, v24
	v_pk_mul_f32 v[36:37], v[34:35], v[34:35]
	s_nop 0
	v_add_f32_e32 v36, v36, v37
	s_nop 1
	v_mov_b32_dpp v37, v36 quad_perm:[1,0,3,2] row_mask:0xf bank_mask:0xf
	s_waitcnt lgkmcnt(0)
	v_add_f32_e32 v36, v36, v37
	s_nop 1
	v_mov_b32_dpp v37, v36 quad_perm:[2,3,0,1] row_mask:0xf bank_mask:0xf
	s_waitcnt lgkmcnt(0)
	v_add_f32_e32 v36, v36, v37
	s_nop 1
	v_mov_b32_dpp v37, v36 row_half_mirror row_mask:0xf bank_mask:0xf
	s_waitcnt lgkmcnt(0)
	v_add_f32_e32 v36, v36, v37
	s_nop 1
	v_mov_b32_dpp v37, v36 row_mirror row_mask:0xf bank_mask:0xf
	s_waitcnt lgkmcnt(0)
; #define GAS __attribute__((address_space(1)))
; __device__ __forceinline__ unsigned pk2(float lo, float hi) { f32x2_m v = {lo, hi}; bf16x2_m b = __builtin_convertvector(v, bf16x2_m); return __builtin_bit_cast(unsigned, b); }
; __device__ __forceinline__ float bflo(unsigned w) { return __uint_as_float(w << 16); }
; __device__ __forceinline__ float bfhi(unsigned w) { return __uint_as_float(w & 0xffff0000u); }
; template <bool F8> __device__ __forceinline__ void mix_phase(const Ctx& C, const bf16* YCONV, const bf16* YSWA, const bf16* ODIFF, const float* conv_g, const float* swa_g, const float* lq1, const float* lk1, const float* lq2, const float* lk2, ...
;     ...
; #pragma unroll
;             for (int h = 0; h < 6; ++h) { const unsigned a = oa[q][h], bq = ob[q][h];
;                 const float v0 = bflo(a) - lam * bflo(bq), v1 = bfhi(a) - lam * bfhi(bq);
;                 const float r = 1.0f / sqrtf(wave_sum(v0 * v0 + v1 * v1) * (1.0f / 128.0f) + LN_EPS);
;                 if constexpr (F8) *(GAS unsigned short*)(MIX8 + (size_t)m * DM + 1280 + 128 * h + 2 * l) = (unsigned short)pk4_fp8m(v0 * r * gA, v1 * r * gB, 0.f, 0.f);
;                 else *(GAS unsigned*)(MIX + (size_t)m * DM + 1280 + 128 * h + 2 * l) = pk2(v0 * r * gA, v1 * r * gB); } }
	v_add_f32_e32 v36, v36, v37
	v_mov_b32_e32 v37, v36
	s_nop 1
	v_permlane16_swap_b32_e32 v36, v37
	s_waitcnt lgkmcnt(0)
	v_add_f32_e32 v36, v36, v37
	v_mov_b32_e32 v37, v36
	s_nop 1
	v_permlane32_swap_b32_e32 v36, v37
	s_waitcnt lgkmcnt(0)
	v_add_f32_e32 v36, v36, v37
	v_fmamk_f32 v36, v36, 0x3c000000, v210
	v_cmp_gt_f32_e32 vcc, s18, v36
	v_mul_f32_e32 v37, 0x4f800000, v36
	s_nop 0
	v_cndmask_b32_e32 v36, v36, v37, vcc
	v_sqrt_f32_e32 v37, v36
	s_nop 0
	v_add_u32_e32 v38, -1, v37
	v_fma_f32 v39, -v38, v37, v36
	v_cmp_ge_f32_e64 s[2:3], 0, v39
	v_add_u32_e32 v39, 1, v37
	s_nop 0
	v_cndmask_b32_e64 v38, v37, v38, s[2:3]
	v_fma_f32 v37, -v39, v37, v36
	v_cmp_lt_f32_e64 s[2:3], 0, v37
	s_nop 1
	v_cndmask_b32_e64 v37, v38, v39, s[2:3]
	v_mul_f32_e32 v38, 0x37800000, v37
	v_cndmask_b32_e32 v37, v37, v38, vcc
	v_cmp_class_f32_e32 vcc, v36, v211
	s_nop 1
	v_cndmask_b32_e32 v36, v37, v36, vcc
	v_div_scale_f32 v37, s[2:3], v36, v36, 1.0
	v_rcp_f32_e32 v38, v37
	s_nop 0
	v_fma_f32 v39, -v37, v38, 1.0
	v_fmac_f32_e32 v38, v39, v38
	v_div_scale_f32 v39, vcc, 1.0, v36, 1.0
	v_mul_f32_e32 v88, v39, v38
	v_fma_f32 v89, -v37, v88, v39
	v_fmac_f32_e32 v88, v89, v38
	v_fma_f32 v37, -v37, v88, v39
	v_div_fmas_f32 v37, v37, v38, v88
	v_div_fixup_f32 v36, v37, v36, 1.0
	v_pk_mul_f32 v[34:35], v[34:35], v[36:37] op_sel_hi:[1,0]
	v_lshlrev_b32_e32 v36, 16, v112
	v_pk_mul_f32 v[34:35], v[58:59], v[34:35]
	v_and_b32_e32 v37, 0xffff0000, v112
	v_cvt_pk_bf16_f32 v34, v34, v35
	global_store_dword v[32:33], v34, off offset:3072
	v_lshlrev_b32_e32 v34, 16, v111
	v_and_b32_e32 v35, 0xffff0000, v111
	v_pk_fma_f32 v[34:35], v[40:41], v[36:37], v[34:35] neg_lo:[1,0,0] neg_hi:[1,0,0]
	v_lshlrev_b32_e32 v112, 16, v24
	v_pk_mul_f32 v[36:37], v[34:35], v[34:35]
	s_nop 0
	v_add_f32_e32 v36, v36, v37
	s_nop 1
	v_mov_b32_dpp v37, v36 quad_perm:[1,0,3,2] row_mask:0xf bank_mask:0xf
	s_waitcnt lgkmcnt(0)
	v_add_f32_e32 v36, v36, v37
	s_nop 1
	v_mov_b32_dpp v37, v36 quad_perm:[2,3,0,1] row_mask:0xf bank_mask:0xf
	s_waitcnt lgkmcnt(0)
	v_add_f32_e32 v36, v36, v37
	s_nop 1
	v_mov_b32_dpp v37, v36 row_half_mirror row_mask:0xf bank_mask:0xf
	s_waitcnt lgkmcnt(0)
	v_add_f32_e32 v36, v36, v37
	s_nop 1
	v_mov_b32_dpp v37, v36 row_mirror row_mask:0xf bank_mask:0xf
	s_waitcnt lgkmcnt(0)
	v_add_f32_e32 v36, v36, v37
	v_mov_b32_e32 v37, v36
	s_nop 1
	v_permlane16_swap_b32_e32 v36, v37
	s_waitcnt lgkmcnt(0)
	v_add_f32_e32 v36, v36, v37
	v_mov_b32_e32 v37, v36
	s_nop 1
	v_permlane32_swap_b32_e32 v36, v37
	s_waitcnt lgkmcnt(0)
	v_add_f32_e32 v36, v36, v37
	v_fmamk_f32 v36, v36, 0x3c000000, v210
	v_cmp_gt_f32_e32 vcc, s18, v36
	v_mul_f32_e32 v37, 0x4f800000, v36
	s_nop 0
	v_cndmask_b32_e32 v36, v36, v37, vcc
	v_sqrt_f32_e32 v37, v36
	s_nop 0
	v_add_u32_e32 v38, -1, v37
	v_fma_f32 v39, -v38, v37, v36
	v_cmp_ge_f32_e64 s[2:3], 0, v39
	v_add_u32_e32 v39, 1, v37
	s_nop 0
	v_cndmask_b32_e64 v38, v37, v38, s[2:3]
	v_fma_f32 v37, -v39, v37, v36
	v_cmp_lt_f32_e64 s[2:3], 0, v37
	s_nop 1
	v_cndmask_b32_e64 v37, v38, v39, s[2:3]
	v_mul_f32_e32 v38, 0x37800000, v37
	v_cndmask_b32_e32 v37, v37, v38, vcc
	v_cmp_class_f32_e32 vcc, v36, v211
	s_nop 1
	v_cndmask_b32_e32 v36, v37, v36, vcc
	v_div_scale_f32 v37, s[2:3], v36, v36, 1.0
	v_rcp_f32_e32 v38, v37
	s_nop 0
	v_fma_f32 v39, -v37, v38, 1.0
	v_fmac_f32_e32 v38, v39, v38
	v_div_scale_f32 v39, vcc, 1.0, v36, 1.0
	v_mul_f32_e32 v88, v39, v38
	v_fma_f32 v89, -v37, v88, v39
	v_fmac_f32_e32 v88, v89, v38
	v_fma_f32 v37, -v37, v88, v39
	v_div_fmas_f32 v37, v37, v38, v88
	v_div_fixup_f32 v36, v37, v36, 1.0
	v_pk_mul_f32 v[34:35], v[34:35], v[36:37] op_sel_hi:[1,0]
	v_lshlrev_b32_e32 v36, 16, v110
	v_pk_mul_f32 v[34:35], v[58:59], v[34:35]
	v_and_b32_e32 v37, 0xffff0000, v110
	v_cvt_pk_bf16_f32 v34, v34, v35
	global_store_dword v[32:33], v34, off offset:3328
	v_lshlrev_b32_e32 v34, 16, v109
	v_and_b32_e32 v35, 0xffff0000, v109
	v_pk_fma_f32 v[34:35], v[40:41], v[36:37], v[34:35] neg_lo:[1,0,0] neg_hi:[1,0,0]
	v_and_b32_e32 v109, 0xffff0000, v28
	v_pk_mul_f32 v[36:37], v[34:35], v[34:35]
	s_nop 0
	v_add_f32_e32 v36, v36, v37
	s_nop 1
	v_mov_b32_dpp v37, v36 quad_perm:[1,0,3,2] row_mask:0xf bank_mask:0xf
	s_waitcnt lgkmcnt(0)
	v_add_f32_e32 v36, v36, v37
	s_nop 1
	v_mov_b32_dpp v37, v36 quad_perm:[2,3,0,1] row_mask:0xf bank_mask:0xf
	s_waitcnt lgkmcnt(0)
	v_add_f32_e32 v36, v36, v37
	s_nop 1
	v_mov_b32_dpp v37, v36 row_half_mirror row_mask:0xf bank_mask:0xf
	s_waitcnt lgkmcnt(0)
	v_add_f32_e32 v36, v36, v37
	s_nop 1
	v_mov_b32_dpp v37, v36 row_mirror row_mask:0xf bank_mask:0xf
	s_waitcnt lgkmcnt(0)
	v_add_f32_e32 v36, v36, v37
	v_mov_b32_e32 v37, v36
	s_nop 1
	v_permlane16_swap_b32_e32 v36, v37
	s_waitcnt lgkmcnt(0)
	v_add_f32_e32 v36, v36, v37
	v_mov_b32_e32 v37, v36
	s_nop 1
	v_permlane32_swap_b32_e32 v36, v37
	s_waitcnt lgkmcnt(0)
	v_add_f32_e32 v36, v36, v37
	v_fmamk_f32 v36, v36, 0x3c000000, v210
	v_cmp_gt_f32_e32 vcc, s18, v36
	v_mul_f32_e32 v37, 0x4f800000, v36
	s_nop 0
	v_cndmask_b32_e32 v36, v36, v37, vcc
	v_sqrt_f32_e32 v37, v36
	s_nop 0
	v_add_u32_e32 v38, -1, v37
	v_fma_f32 v39, -v38, v37, v36
	v_cmp_ge_f32_e64 s[2:3], 0, v39
	v_add_u32_e32 v39, 1, v37
	s_nop 0
	v_cndmask_b32_e64 v38, v37, v38, s[2:3]
	v_fma_f32 v37, -v39, v37, v36
	v_cmp_lt_f32_e64 s[2:3], 0, v37
	s_nop 1
	v_cndmask_b32_e64 v37, v38, v39, s[2:3]
	v_mul_f32_e32 v38, 0x37800000, v37
	v_cndmask_b32_e32 v37, v37, v38, vcc
	v_cmp_class_f32_e32 vcc, v36, v211
	s_nop 1
	v_cndmask_b32_e32 v36, v37, v36, vcc
	v_div_scale_f32 v37, s[2:3], v36, v36, 1.0
	v_rcp_f32_e32 v38, v37
	s_nop 0
	v_fma_f32 v39, -v37, v38, 1.0
	v_fmac_f32_e32 v38, v39, v38
	v_div_scale_f32 v39, vcc, 1.0, v36, 1.0
	v_mul_f32_e32 v88, v39, v38
	v_fma_f32 v89, -v37, v88, v39
	v_fmac_f32_e32 v88, v89, v38
	v_fma_f32 v37, -v37, v88, v39
	v_div_fmas_f32 v37, v37, v38, v88
	v_div_fixup_f32 v36, v37, v36, 1.0
	v_pk_mul_f32 v[34:35], v[34:35], v[36:37] op_sel_hi:[1,0]
	v_lshlrev_b32_e32 v36, 16, v108
	v_pk_mul_f32 v[34:35], v[58:59], v[34:35]
	v_and_b32_e32 v37, 0xffff0000, v108
	v_cvt_pk_bf16_f32 v34, v34, v35
	global_store_dword v[32:33], v34, off offset:3584
	v_lshlrev_b32_e32 v34, 16, v107
	v_and_b32_e32 v35, 0xffff0000, v107
	v_pk_fma_f32 v[34:35], v[40:41], v[36:37], v[34:35] neg_lo:[1,0,0] neg_hi:[1,0,0]
	v_lshlrev_b32_e32 v108, 16, v28
	v_pk_mul_f32 v[36:37], v[34:35], v[34:35]
	s_nop 0
	v_add_f32_e32 v36, v36, v37
	s_nop 1
	v_mov_b32_dpp v37, v36 quad_perm:[1,0,3,2] row_mask:0xf bank_mask:0xf
	s_waitcnt lgkmcnt(0)
; template <bool F8> __device__ __forceinline__ void mix_phase(const Ctx& C, const bf16* YCONV, const bf16* YSWA, const bf16* ODIFF, const float* conv_g, const float* swa_g, const float* lq1, const float* lk1, const float* lq2, const float* lk2, ...
;     ...
;             { const v4u y = yc[q];
;               float f[8] = {bflo(y.x), bfhi(y.x), bflo(y.y), bfhi(y.y), bflo(y.z), bfhi(y.z), bflo(y.w), bfhi(y.w)}; float ss = 0.f;
; #pragma unroll
;               for (int i = 0; i < 8; ++i) ss += f[i] * f[i];
;               const float r = 1.0f / sqrtf(wave_sum(ss) * (1.0f / 512.0f) + RMS_EPS);
;               if constexpr (F8) { v2u o; o.x = pk4_fp8m(f[0] * r * cg0.x, f[1] * r * cg0.y, f[2] * r * cg0.z, f[3] * r * cg0.w); o.y = pk4_fp8m(f[4] * r * cg1.x, f[5] * r * cg1.y, f[6] * r * cg1.z, f[7] * r * cg1.w);
;                 *(GAS v2u*)(MIX8 + (size_t)m * DM + 8 * l) = o; }
;               else { v4u o; o.x = pk2(f[0] * r * cg0.x, f[1] * r * cg0.y); o.y = pk2(f[2] * r * cg0.z, f[3] * r * cg0.w); o.z = pk2(f[4] * r * cg1.x, f[5] * r * cg1.y); o.w = pk2(f[6] * r * cg1.z, f[7] * r * cg1.w);
;                 *(GAS v4u*)(MIX + (size_t)m * DM + 8 * l) = o; } }
;             { const v4u y = ys[q]; const v2u y2 = ys2[q];
;               float f[12] = {bflo(y.x), bfhi(y.x), bflo(y.y), bfhi(y.y), bflo(y.z), bfhi(y.z), bflo(y.w), bfhi(y.w), bflo(y2.x), bfhi(y2.x), bflo(y2.y), bfhi(y2.y)}; float ss = 0.f;
; #pragma unroll
;               for (int i = 0; i < 12; ++i) ss += f[i] * f[i];
;               const float r = 1.0f / sqrtf(wave_sum(ss) * (1.0f / 768.0f) + RMS_EPS);
;               if constexpr (F8) { v2u o; o.x = pk4_fp8m(f[0] * r * sg0.x, f[1] * r * sg0.y, f[2] * r * sg0.z, f[3] * r * sg0.w); o.y = pk4_fp8m(f[4] * r * sg1.x, f[5] * r * sg1.y, f[6] * r * sg1.z, f[7] * r * sg1.w);
;                 const unsigned o2 = pk4_fp8m(f[8] * r * sg2.x, f[9] * r * sg2.y, f[10] * r * sg2.z, f[11] * r * sg2.w);
;                 *(GAS v2u*)(MIX8 + (size_t)m * DM + 512 + 8 * l) = o; *(GAS unsigned*)(MIX8 + (size_t)m * DM + 1024 + 4 * l) = o2; }
;               else { v4u o; o.x = pk2(f[0] * r * sg0.x, f[1] * r * sg0.y); o.y = pk2(f[2] * r * sg0.z, f[3] * r * sg0.w); o.z = pk2(f[4] * r * sg1.x, f[5] * r * sg1.y); o.w = pk2(f[6] * r * sg1.z, f[7] * r * sg1.w);
;                 v2u o2; o2.x = pk2(f[8] * r * sg2.x, f[9] * r * sg2.y); o2.y = pk2(f[10] * r * sg2.z, f[11] * r * sg2.w);
	v_add_f32_e32 v36, v36, v37
	s_nop 1
	v_mov_b32_dpp v37, v36 quad_perm:[2,3,0,1] row_mask:0xf bank_mask:0xf
	s_waitcnt lgkmcnt(0)
	v_add_f32_e32 v36, v36, v37
	s_nop 1
	v_mov_b32_dpp v37, v36 row_half_mirror row_mask:0xf bank_mask:0xf
	s_waitcnt lgkmcnt(0)
	v_add_f32_e32 v36, v36, v37
	s_nop 1
	v_mov_b32_dpp v37, v36 row_mirror row_mask:0xf bank_mask:0xf
	s_waitcnt lgkmcnt(0)
	v_add_f32_e32 v36, v36, v37
	v_mov_b32_e32 v37, v36
	s_nop 1
	v_permlane16_swap_b32_e32 v36, v37
	s_waitcnt lgkmcnt(0)
	v_add_f32_e32 v36, v36, v37
	v_mov_b32_e32 v37, v36
	s_nop 1
	v_permlane32_swap_b32_e32 v36, v37
	s_waitcnt lgkmcnt(0)
	v_add_f32_e32 v36, v36, v37
	v_fmamk_f32 v36, v36, 0x3c000000, v210
	v_cmp_gt_f32_e32 vcc, s18, v36
	v_mul_f32_e32 v37, 0x4f800000, v36
	s_nop 0
	v_cndmask_b32_e32 v36, v36, v37, vcc
	v_sqrt_f32_e32 v37, v36
	s_nop 0
	v_add_u32_e32 v38, -1, v37
	v_fma_f32 v39, -v38, v37, v36
	v_cmp_ge_f32_e64 s[2:3], 0, v39
	v_add_u32_e32 v39, 1, v37
	s_nop 0
	v_cndmask_b32_e64 v38, v37, v38, s[2:3]
	v_fma_f32 v37, -v39, v37, v36
	v_cmp_lt_f32_e64 s[2:3], 0, v37
	s_nop 1
	v_cndmask_b32_e64 v37, v38, v39, s[2:3]
	v_mul_f32_e32 v38, 0x37800000, v37
	v_cndmask_b32_e32 v37, v37, v38, vcc
	v_cmp_class_f32_e32 vcc, v36, v211
	s_nop 1
	v_cndmask_b32_e32 v36, v37, v36, vcc
	v_div_scale_f32 v37, s[2:3], v36, v36, 1.0
	v_rcp_f32_e32 v38, v37
	s_nop 0
	v_fma_f32 v39, -v37, v38, 1.0
	v_fmac_f32_e32 v38, v39, v38
	v_div_scale_f32 v39, vcc, 1.0, v36, 1.0
	v_mul_f32_e32 v88, v39, v38
	v_fma_f32 v89, -v37, v88, v39
	v_fmac_f32_e32 v88, v89, v38
	v_fma_f32 v37, -v37, v88, v39
	v_div_fmas_f32 v37, v37, v38, v88
	v_div_fixup_f32 v36, v37, v36, 1.0
	v_pk_mul_f32 v[34:35], v[34:35], v[36:37] op_sel_hi:[1,0]
	v_lshlrev_b32_e32 v38, 16, v29
	v_and_b32_e32 v39, 0xffff0000, v29
	v_pk_mul_f32 v[28:29], v[108:109], v[108:109]
	v_pk_mul_f32 v[34:35], v[58:59], v[34:35]
	v_pk_mul_f32 v[88:89], v[38:39], v[38:39]
	v_add_f32_e32 v28, v28, v29
	v_cvt_pk_bf16_f32 v34, v34, v35
	v_lshlrev_b32_e32 v36, 16, v30
	v_and_b32_e32 v37, 0xffff0000, v30
	v_add_f32_e32 v28, v88, v28
	global_store_dword v[32:33], v34, off offset:3840
	v_lshlrev_b32_e32 v32, 16, v31
	v_and_b32_e32 v33, 0xffff0000, v31
	v_pk_mul_f32 v[30:31], v[36:37], v[36:37]
	v_add_f32_e32 v28, v89, v28
	v_add_f32_e32 v28, v30, v28
	v_pk_mul_f32 v[34:35], v[32:33], v[32:33]
	v_add_f32_e32 v28, v31, v28
	v_add_f32_e32 v28, v34, v28
	v_add_f32_e32 v28, v35, v28
	s_nop 1
	v_mov_b32_dpp v29, v28 quad_perm:[1,0,3,2] row_mask:0xf bank_mask:0xf
	v_lshlrev_b32_e32 v88, 16, v26
	v_and_b32_e32 v89, 0xffff0000, v26
	s_waitcnt lgkmcnt(0)
	v_add_f32_e32 v28, v28, v29
	s_nop 1
	v_mov_b32_dpp v29, v28 quad_perm:[2,3,0,1] row_mask:0xf bank_mask:0xf
	s_waitcnt lgkmcnt(0)
	v_add_f32_e32 v28, v28, v29
	s_nop 1
	v_mov_b32_dpp v29, v28 row_half_mirror row_mask:0xf bank_mask:0xf
	s_waitcnt lgkmcnt(0)
	v_add_f32_e32 v28, v28, v29
	s_nop 1
	v_mov_b32_dpp v29, v28 row_mirror row_mask:0xf bank_mask:0xf
	s_waitcnt lgkmcnt(0)
	v_add_f32_e32 v28, v28, v29
	v_mov_b32_e32 v29, v28
	s_nop 1
	v_permlane16_swap_b32_e32 v28, v29
	s_waitcnt lgkmcnt(0)
	v_add_f32_e32 v28, v28, v29
	v_mov_b32_e32 v29, v28
	s_nop 1
	v_permlane32_swap_b32_e32 v28, v29
	s_waitcnt lgkmcnt(0)
	v_add_f32_e32 v28, v28, v29
	v_fmamk_f32 v28, v28, 0x3b000000, v212
	v_cmp_gt_f32_e32 vcc, s18, v28
	v_mul_f32_e32 v29, 0x4f800000, v28
	s_nop 0
	v_cndmask_b32_e32 v28, v28, v29, vcc
	v_sqrt_f32_e32 v29, v28
	s_nop 0
	v_add_u32_e32 v30, -1, v29
	v_fma_f32 v31, -v30, v29, v28
	v_cmp_ge_f32_e64 s[2:3], 0, v31
	v_add_u32_e32 v31, 1, v29
	s_nop 0
	v_cndmask_b32_e64 v30, v29, v30, s[2:3]
	v_fma_f32 v29, -v31, v29, v28
	v_cmp_lt_f32_e64 s[2:3], 0, v29
	s_nop 1
	v_cndmask_b32_e64 v29, v30, v31, s[2:3]
	v_mul_f32_e32 v30, 0x37800000, v29
	v_cndmask_b32_e32 v29, v29, v30, vcc
	v_cmp_class_f32_e32 vcc, v28, v211
	s_nop 1
	v_cndmask_b32_e32 v28, v29, v28, vcc
	v_div_scale_f32 v29, s[2:3], v28, v28, 1.0
	v_rcp_f32_e32 v30, v29
	s_nop 0
	v_fma_f32 v31, -v29, v30, 1.0
	v_fmac_f32_e32 v30, v31, v30
	v_div_scale_f32 v31, vcc, 1.0, v28, 1.0
	v_mul_f32_e32 v34, v31, v30
	v_fma_f32 v35, -v29, v34, v31
	v_fmac_f32_e32 v34, v35, v30
	v_fma_f32 v29, -v29, v34, v31
	v_div_fmas_f32 v29, v29, v30, v34
	v_div_fixup_f32 v34, v29, v28, 1.0
	v_pk_mul_f32 v[28:29], v[34:35], v[108:109] op_sel_hi:[0,1]
	v_pk_mul_f32 v[30:31], v[34:35], v[38:39] op_sel_hi:[0,1]
	v_pk_mul_f32 v[28:29], v[16:17], v[28:29]
	v_pk_mul_f32 v[30:31], v[18:19], v[30:31]
	v_cvt_pk_bf16_f32 v28, v28, v29
	v_cvt_pk_bf16_f32 v29, v30, v31
	v_pk_mul_f32 v[30:31], v[34:35], v[36:37] op_sel_hi:[0,1]
	v_pk_mul_f32 v[32:33], v[34:35], v[32:33] op_sel_hi:[0,1]
	v_lshlrev_b32_e32 v108, 16, v25
	v_and_b32_e32 v109, 0xffff0000, v25
	v_pk_mul_f32 v[24:25], v[112:113], v[112:113]
	v_pk_mul_f32 v[30:31], v[20:21], v[30:31]
	v_pk_mul_f32 v[32:33], v[22:23], v[32:33]
	v_pk_mul_f32 v[110:111], v[108:109], v[108:109]
	v_add_f32_e32 v24, v24, v25
	v_cvt_pk_bf16_f32 v30, v30, v31
	v_cvt_pk_bf16_f32 v31, v32, v33
	v_lshl_add_u64 v[32:33], s[12:13], 0, v[44:45]
	v_add_f32_e32 v24, v110, v24
	v_add_co_u32_e32 v32, vcc, s22, v32
	v_lshlrev_b32_e32 v38, 16, v27
	v_and_b32_e32 v39, 0xffff0000, v27
	v_pk_mul_f32 v[26:27], v[88:89], v[88:89]
	v_add_f32_e32 v24, v111, v24
	v_addc_co_u32_e32 v33, vcc, 0, v33, vcc
	v_add_f32_e32 v24, v26, v24
	global_store_dwordx4 v[32:33], v[28:31], off
	s_waitcnt vmcnt(22)
; #define GAS __attribute__((address_space(1)))
; __device__ __forceinline__ float bflo(unsigned w) { return __uint_as_float(w << 16); }
; template <bool F8> __device__ __forceinline__ void mix_phase(const Ctx& C, const bf16* YCONV, const bf16* YSWA, const bf16* ODIFF, const float* conv_g, const float* swa_g, const float* lq1, const float* lk1, const float* lq2, const float* lk2, ...
;     ...
;             { const v4u y = ys[q]; const v2u y2 = ys2[q];
;               float f[12] = {bflo(y.x), bfhi(y.x), bflo(y.y), bfhi(y.y), bflo(y.z), bfhi(y.z), bflo(y.w), bfhi(y.w), bflo(y2.x), bfhi(y2.x), bflo(y2.y), bfhi(y2.y)}; float ss = 0.f;
; #pragma unroll
;               for (int i = 0; i < 12; ++i) ss += f[i] * f[i];
;               const float r = 1.0f / sqrtf(wave_sum(ss) * (1.0f / 768.0f) + RMS_EPS);
;               if constexpr (F8) { v2u o; o.x = pk4_fp8m(f[0] * r * sg0.x, f[1] * r * sg0.y, f[2] * r * sg0.z, f[3] * r * sg0.w); o.y = pk4_fp8m(f[4] * r * sg1.x, f[5] * r * sg1.y, f[6] * r * sg1.z, f[7] * r * sg1.w);
;                 const unsigned o2 = pk4_fp8m(f[8] * r * sg2.x, f[9] * r * sg2.y, f[10] * r * sg2.z, f[11] * r * sg2.w);
;                 *(GAS v2u*)(MIX8 + (size_t)m * DM + 512 + 8 * l) = o; *(GAS unsigned*)(MIX8 + (size_t)m * DM + 1024 + 4 * l) = o2; }
;               else { v4u o; o.x = pk2(f[0] * r * sg0.x, f[1] * r * sg0.y); o.y = pk2(f[2] * r * sg0.z, f[3] * r * sg0.w); o.z = pk2(f[4] * r * sg1.x, f[5] * r * sg1.y); o.w = pk2(f[6] * r * sg1.z, f[7] * r * sg1.w);
;                 v2u o2; o2.x = pk2(f[8] * r * sg2.x, f[9] * r * sg2.y); o2.y = pk2(f[10] * r * sg2.z, f[11] * r * sg2.w);
;                 *(GAS v4u*)(MIX + (size_t)m * DM + 512 + 8 * l) = o; *(GAS v2u*)(MIX + (size_t)m * DM + 1024 + 4 * l) = o2; } }
; #pragma unroll
;             for (int h = 0; h < 6; ++h) { const unsigned a = oa[q][h], bq = ob[q][h];
;                 const float v0 = bflo(a) - lam * bflo(bq), v1 = bfhi(a) - lam * bfhi(bq);
;                 const float r = 1.0f / sqrtf(wave_sum(v0 * v0 + v1 * v1) * (1.0f / 128.0f) + LN_EPS);
;                 if constexpr (F8) *(GAS unsigned short*)(MIX8 + (size_t)m * DM + 1280 + 128 * h + 2 * l) = (unsigned short)pk4_fp8m(v0 * r * gA, v1 * r * gB, 0.f, 0.f);
;                 else *(GAS unsigned*)(MIX + (size_t)m * DM + 1280 + 128 * h + 2 * l) = pk2(v0 * r * gA, v1 * r * gB); } }
	v_lshlrev_b32_e32 v34, 16, v86
	v_and_b32_e32 v35, 0xffff0000, v86
	v_lshlrev_b32_e32 v30, 16, v87
	v_and_b32_e32 v31, 0xffff0000, v87
	v_pk_mul_f32 v[86:87], v[38:39], v[38:39]
	v_add_f32_e32 v24, v27, v24
	v_add_f32_e32 v24, v86, v24
	v_pk_mul_f32 v[36:37], v[34:35], v[34:35]
	v_add_f32_e32 v24, v87, v24
	v_add_f32_e32 v24, v36, v24
	v_pk_mul_f32 v[28:29], v[30:31], v[30:31]
	v_add_f32_e32 v24, v37, v24
	v_add_f32_e32 v24, v28, v24
	v_add_f32_e32 v24, v29, v24
	s_nop 1
	v_mov_b32_dpp v25, v24 quad_perm:[1,0,3,2] row_mask:0xf bank_mask:0xf
	v_lshl_add_u64 v[44:45], v[44:45], 0, s[24:25]
	s_waitcnt lgkmcnt(0)
	v_add_f32_e32 v24, v24, v25
	s_nop 1
	v_mov_b32_dpp v25, v24 quad_perm:[2,3,0,1] row_mask:0xf bank_mask:0xf
	s_waitcnt lgkmcnt(0)
	v_add_f32_e32 v24, v24, v25
	s_nop 1
	v_mov_b32_dpp v25, v24 row_half_mirror row_mask:0xf bank_mask:0xf
	s_waitcnt lgkmcnt(0)
	v_add_f32_e32 v24, v24, v25
	s_nop 1
	v_mov_b32_dpp v25, v24 row_mirror row_mask:0xf bank_mask:0xf
	s_waitcnt lgkmcnt(0)
	v_add_f32_e32 v24, v24, v25
	v_mov_b32_e32 v25, v24
	s_nop 1
	v_permlane16_swap_b32_e32 v24, v25
	s_waitcnt lgkmcnt(0)
	v_add_f32_e32 v24, v24, v25
	v_mov_b32_e32 v25, v24
	s_nop 1
	v_permlane32_swap_b32_e32 v24, v25
	s_waitcnt lgkmcnt(0)
	v_add_f32_e32 v24, v24, v25
	v_fmamk_f32 v24, v24, 0x3aaaaaab, v212
	v_cmp_gt_f32_e32 vcc, s18, v24
	v_mul_f32_e32 v25, 0x4f800000, v24
	s_nop 0
	v_cndmask_b32_e32 v24, v24, v25, vcc
	v_sqrt_f32_e32 v25, v24
	s_nop 0
	v_add_u32_e32 v26, -1, v25
	v_fma_f32 v27, -v26, v25, v24
	v_cmp_ge_f32_e64 s[2:3], 0, v27
	v_add_u32_e32 v27, 1, v25
	s_nop 0
	v_cndmask_b32_e64 v26, v25, v26, s[2:3]
	v_fma_f32 v25, -v27, v25, v24
	v_cmp_lt_f32_e64 s[2:3], 0, v25
	s_nop 1
	v_cndmask_b32_e64 v25, v26, v27, s[2:3]
	v_mul_f32_e32 v26, 0x37800000, v25
	v_cndmask_b32_e32 v25, v25, v26, vcc
	v_cmp_class_f32_e32 vcc, v24, v211
	s_nop 1
	v_cndmask_b32_e32 v24, v25, v24, vcc
	v_div_scale_f32 v25, s[2:3], v24, v24, 1.0
	v_rcp_f32_e32 v26, v25
	s_nop 0
	v_fma_f32 v27, -v25, v26, 1.0
	v_fmac_f32_e32 v26, v27, v26
	v_div_scale_f32 v27, vcc, 1.0, v24, 1.0
	v_mul_f32_e32 v28, v27, v26
	v_fma_f32 v29, -v25, v28, v27
	v_fmac_f32_e32 v28, v29, v26
	v_fma_f32 v25, -v25, v28, v27
	v_div_fmas_f32 v25, v25, v26, v28
	v_div_fixup_f32 v36, v25, v24, 1.0
	v_pk_mul_f32 v[24:25], v[36:37], v[112:113] op_sel_hi:[0,1]
	v_pk_mul_f32 v[24:25], v[8:9], v[24:25]
	v_pk_mul_f32 v[30:31], v[36:37], v[30:31] op_sel_hi:[0,1]
	v_cvt_pk_bf16_f32 v26, v24, v25
	v_pk_mul_f32 v[24:25], v[36:37], v[108:109] op_sel_hi:[0,1]
	v_pk_mul_f32 v[24:25], v[10:11], v[24:25]
	v_pk_mul_f32 v[30:31], v[6:7], v[30:31]
	v_cvt_pk_bf16_f32 v27, v24, v25
	v_pk_mul_f32 v[24:25], v[36:37], v[88:89] op_sel_hi:[0,1]
	v_pk_mul_f32 v[24:25], v[12:13], v[24:25]
	s_nop 0
	v_cvt_pk_bf16_f32 v28, v24, v25
	v_pk_mul_f32 v[24:25], v[36:37], v[38:39] op_sel_hi:[0,1]
	v_pk_mul_f32 v[24:25], v[14:15], v[24:25]
	s_nop 0
	v_cvt_pk_bf16_f32 v29, v24, v25
	v_pk_mul_f32 v[24:25], v[36:37], v[34:35] op_sel_hi:[0,1]
	v_pk_mul_f32 v[24:25], v[4:5], v[24:25]
	global_store_dwordx4 v[32:33], v[26:29], off offset:1024
	v_cvt_pk_bf16_f32 v24, v24, v25
	v_cvt_pk_bf16_f32 v25, v30, v31
	v_lshl_add_u64 v[26:27], s[12:13], 0, v[46:47]
	global_store_dwordx2 v[26:27], v[24:25], off
	s_waitcnt vmcnt(23)
	v_lshlrev_b32_e32 v26, 16, v105
	s_waitcnt vmcnt(22)
	v_lshlrev_b32_e32 v28, 16, v106
	v_and_b32_e32 v27, 0xffff0000, v105
	v_and_b32_e32 v29, 0xffff0000, v106
	v_pk_fma_f32 v[26:27], v[40:41], v[28:29], v[26:27] neg_lo:[1,0,0] neg_hi:[1,0,0]
	v_lshl_add_u64 v[24:25], s[12:13], 0, v[42:43]
	v_pk_mul_f32 v[28:29], v[26:27], v[26:27]
	v_lshl_add_u64 v[42:43], v[42:43], 0, s[24:25]
	v_add_f32_e32 v28, v28, v29
	s_nop 1
	v_mov_b32_dpp v29, v28 quad_perm:[1,0,3,2] row_mask:0xf bank_mask:0xf
	v_lshl_add_u64 v[46:47], v[46:47], 0, s[24:25]
	s_waitcnt lgkmcnt(0)
	v_add_f32_e32 v28, v28, v29
	s_nop 1
	v_mov_b32_dpp v29, v28 quad_perm:[2,3,0,1] row_mask:0xf bank_mask:0xf
	s_waitcnt lgkmcnt(0)
	v_add_f32_e32 v28, v28, v29
	s_nop 1
	v_mov_b32_dpp v29, v28 row_half_mirror row_mask:0xf bank_mask:0xf
	s_waitcnt lgkmcnt(0)
	v_add_f32_e32 v28, v28, v29
	s_nop 1
	v_mov_b32_dpp v29, v28 row_mirror row_mask:0xf bank_mask:0xf
	s_waitcnt lgkmcnt(0)
	v_add_f32_e32 v28, v28, v29
	v_mov_b32_e32 v29, v28
	s_nop 1
	v_permlane16_swap_b32_e32 v28, v29
	s_waitcnt lgkmcnt(0)
	v_add_f32_e32 v28, v28, v29
	v_mov_b32_e32 v29, v28
	s_nop 1
	v_permlane32_swap_b32_e32 v28, v29
	s_waitcnt lgkmcnt(0)
	v_add_f32_e32 v28, v28, v29
	v_fmamk_f32 v28, v28, 0x3c000000, v210
	v_cmp_gt_f32_e32 vcc, s18, v28
	v_mul_f32_e32 v29, 0x4f800000, v28
	s_nop 0
	v_cndmask_b32_e32 v28, v28, v29, vcc
	v_sqrt_f32_e32 v29, v28
	s_nop 0
	v_add_u32_e32 v30, -1, v29
	v_fma_f32 v31, -v30, v29, v28
	v_cmp_ge_f32_e64 s[2:3], 0, v31
	v_add_u32_e32 v31, 1, v29
	s_nop 0
	v_cndmask_b32_e64 v30, v29, v30, s[2:3]
	v_fma_f32 v29, -v31, v29, v28
	v_cmp_lt_f32_e64 s[2:3], 0, v29
	s_nop 1
	v_cndmask_b32_e64 v29, v30, v31, s[2:3]
	v_mul_f32_e32 v30, 0x37800000, v29
	v_cndmask_b32_e32 v29, v29, v30, vcc
	v_cmp_class_f32_e32 vcc, v28, v211
	s_nop 1
	v_cndmask_b32_e32 v28, v29, v28, vcc
	v_div_scale_f32 v29, s[2:3], v28, v28, 1.0
	v_rcp_f32_e32 v30, v29
	s_nop 0
	v_fma_f32 v31, -v29, v30, 1.0
	v_fmac_f32_e32 v30, v31, v30
	v_div_scale_f32 v31, vcc, 1.0, v28, 1.0
	v_mul_f32_e32 v32, v31, v30
	v_fma_f32 v33, -v29, v32, v31
	v_fmac_f32_e32 v32, v33, v30
	v_fma_f32 v29, -v29, v32, v31
	v_div_fmas_f32 v29, v29, v30, v32
	v_div_fixup_f32 v28, v29, v28, 1.0
	v_pk_mul_f32 v[26:27], v[26:27], v[28:29] op_sel_hi:[1,0]
	v_add_co_u32_e32 v24, vcc, s22, v24
	v_pk_mul_f32 v[26:27], v[58:59], v[26:27]
	s_nop 0
	v_addc_co_u32_e32 v25, vcc, 0, v25, vcc
	v_cvt_pk_bf16_f32 v26, v26, v27
	global_store_dword v[24:25], v26, off offset:2560
	s_waitcnt vmcnt(22)
; #define GAS __attribute__((address_space(1)))
; __device__ __forceinline__ unsigned pk2(float lo, float hi) { f32x2_m v = {lo, hi}; bf16x2_m b = __builtin_convertvector(v, bf16x2_m); return __builtin_bit_cast(unsigned, b); }
; __device__ __forceinline__ float bflo(unsigned w) { return __uint_as_float(w << 16); }
; __device__ __forceinline__ float bfhi(unsigned w) { return __uint_as_float(w & 0xffff0000u); }
; template <bool F8> __device__ __forceinline__ void mix_phase(const Ctx& C, const bf16* YCONV, const bf16* YSWA, const bf16* ODIFF, const float* conv_g, const float* swa_g, const float* lq1, const float* lk1, const float* lq2, const float* lk2, ...
;     ...
; #pragma unroll
;             for (int h = 0; h < 6; ++h) { const unsigned a = oa[q][h], bq = ob[q][h];
;                 const float v0 = bflo(a) - lam * bflo(bq), v1 = bfhi(a) - lam * bfhi(bq);
;                 const float r = 1.0f / sqrtf(wave_sum(v0 * v0 + v1 * v1) * (1.0f / 128.0f) + LN_EPS);
;                 if constexpr (F8) *(GAS unsigned short*)(MIX8 + (size_t)m * DM + 1280 + 128 * h + 2 * l) = (unsigned short)pk4_fp8m(v0 * r * gA, v1 * r * gB, 0.f, 0.f);
;                 else *(GAS unsigned*)(MIX + (size_t)m * DM + 1280 + 128 * h + 2 * l) = pk2(v0 * r * gA, v1 * r * gB); } }
	v_lshlrev_b32_e32 v26, 16, v103
	s_waitcnt vmcnt(21)
	v_lshlrev_b32_e32 v28, 16, v104
	v_and_b32_e32 v27, 0xffff0000, v103
	v_and_b32_e32 v29, 0xffff0000, v104
	v_pk_fma_f32 v[26:27], v[40:41], v[28:29], v[26:27] neg_lo:[1,0,0] neg_hi:[1,0,0]
	s_nop 0
	v_pk_mul_f32 v[28:29], v[26:27], v[26:27]
	s_nop 0
	v_add_f32_e32 v28, v28, v29
	s_nop 1
	v_mov_b32_dpp v29, v28 quad_perm:[1,0,3,2] row_mask:0xf bank_mask:0xf
	s_waitcnt lgkmcnt(0)
	v_add_f32_e32 v28, v28, v29
	s_nop 1
	v_mov_b32_dpp v29, v28 quad_perm:[2,3,0,1] row_mask:0xf bank_mask:0xf
	s_waitcnt lgkmcnt(0)
	v_add_f32_e32 v28, v28, v29
	s_nop 1
	v_mov_b32_dpp v29, v28 row_half_mirror row_mask:0xf bank_mask:0xf
	s_waitcnt lgkmcnt(0)
	v_add_f32_e32 v28, v28, v29
	s_nop 1
	v_mov_b32_dpp v29, v28 row_mirror row_mask:0xf bank_mask:0xf
	s_waitcnt lgkmcnt(0)
	v_add_f32_e32 v28, v28, v29
	v_mov_b32_e32 v29, v28
	s_nop 1
	v_permlane16_swap_b32_e32 v28, v29
	s_waitcnt lgkmcnt(0)
	v_add_f32_e32 v28, v28, v29
	v_mov_b32_e32 v29, v28
	s_nop 1
	v_permlane32_swap_b32_e32 v28, v29
	s_waitcnt lgkmcnt(0)
	v_add_f32_e32 v28, v28, v29
	v_fmamk_f32 v28, v28, 0x3c000000, v210
	v_cmp_gt_f32_e32 vcc, s18, v28
	v_mul_f32_e32 v29, 0x4f800000, v28
	s_nop 0
	v_cndmask_b32_e32 v28, v28, v29, vcc
	v_sqrt_f32_e32 v29, v28
	s_nop 0
	v_add_u32_e32 v30, -1, v29
	v_fma_f32 v31, -v30, v29, v28
	v_cmp_ge_f32_e64 s[2:3], 0, v31
	v_add_u32_e32 v31, 1, v29
	s_nop 0
	v_cndmask_b32_e64 v30, v29, v30, s[2:3]
	v_fma_f32 v29, -v31, v29, v28
	v_cmp_lt_f32_e64 s[2:3], 0, v29
	s_nop 1
	v_cndmask_b32_e64 v29, v30, v31, s[2:3]
	v_mul_f32_e32 v30, 0x37800000, v29
	v_cndmask_b32_e32 v29, v29, v30, vcc
	v_cmp_class_f32_e32 vcc, v28, v211
	s_nop 1
	v_cndmask_b32_e32 v28, v29, v28, vcc
	v_div_scale_f32 v29, s[2:3], v28, v28, 1.0
	v_rcp_f32_e32 v30, v29
	s_nop 0
	v_fma_f32 v31, -v29, v30, 1.0
	v_fmac_f32_e32 v30, v31, v30
	v_div_scale_f32 v31, vcc, 1.0, v28, 1.0
	v_mul_f32_e32 v32, v31, v30
	v_fma_f32 v33, -v29, v32, v31
	v_fmac_f32_e32 v32, v33, v30
	v_fma_f32 v29, -v29, v32, v31
	v_div_fmas_f32 v29, v29, v30, v32
	v_div_fixup_f32 v28, v29, v28, 1.0
	v_pk_mul_f32 v[26:27], v[26:27], v[28:29] op_sel_hi:[1,0]
	s_waitcnt vmcnt(19)
	v_lshlrev_b32_e32 v28, 16, v102
	v_pk_mul_f32 v[26:27], v[58:59], v[26:27]
	v_and_b32_e32 v29, 0xffff0000, v102
	v_cvt_pk_bf16_f32 v26, v26, v27
	global_store_dword v[24:25], v26, off offset:2816
	v_lshlrev_b32_e32 v26, 16, v101
	v_and_b32_e32 v27, 0xffff0000, v101
	v_pk_fma_f32 v[26:27], v[40:41], v[28:29], v[26:27] neg_lo:[1,0,0] neg_hi:[1,0,0]
	s_nop 0
	v_pk_mul_f32 v[28:29], v[26:27], v[26:27]
	s_nop 0
	v_add_f32_e32 v28, v28, v29
	s_nop 1
	v_mov_b32_dpp v29, v28 quad_perm:[1,0,3,2] row_mask:0xf bank_mask:0xf
	s_waitcnt lgkmcnt(0)
	v_add_f32_e32 v28, v28, v29
	s_nop 1
	v_mov_b32_dpp v29, v28 quad_perm:[2,3,0,1] row_mask:0xf bank_mask:0xf
	s_waitcnt lgkmcnt(0)
	v_add_f32_e32 v28, v28, v29
	s_nop 1
	v_mov_b32_dpp v29, v28 row_half_mirror row_mask:0xf bank_mask:0xf
	s_waitcnt lgkmcnt(0)
	v_add_f32_e32 v28, v28, v29
	s_nop 1
	v_mov_b32_dpp v29, v28 row_mirror row_mask:0xf bank_mask:0xf
	s_waitcnt lgkmcnt(0)
	v_add_f32_e32 v28, v28, v29
	v_mov_b32_e32 v29, v28
	s_nop 1
	v_permlane16_swap_b32_e32 v28, v29
	s_waitcnt lgkmcnt(0)
	v_add_f32_e32 v28, v28, v29
	v_mov_b32_e32 v29, v28
	s_nop 1
	v_permlane32_swap_b32_e32 v28, v29
	s_waitcnt lgkmcnt(0)
	v_add_f32_e32 v28, v28, v29
	v_fmamk_f32 v28, v28, 0x3c000000, v210
	v_cmp_gt_f32_e32 vcc, s18, v28
	v_mul_f32_e32 v29, 0x4f800000, v28
	s_nop 0
	v_cndmask_b32_e32 v28, v28, v29, vcc
	v_sqrt_f32_e32 v29, v28
	s_nop 0
	v_add_u32_e32 v30, -1, v29
	v_fma_f32 v31, -v30, v29, v28
	v_cmp_ge_f32_e64 s[2:3], 0, v31
	v_add_u32_e32 v31, 1, v29
	s_nop 0
	v_cndmask_b32_e64 v30, v29, v30, s[2:3]
	v_fma_f32 v29, -v31, v29, v28
	v_cmp_lt_f32_e64 s[2:3], 0, v29
	s_nop 1
	v_cndmask_b32_e64 v29, v30, v31, s[2:3]
	v_mul_f32_e32 v30, 0x37800000, v29
	v_cndmask_b32_e32 v29, v29, v30, vcc
	v_cmp_class_f32_e32 vcc, v28, v211
	s_nop 1
	v_cndmask_b32_e32 v28, v29, v28, vcc
	v_div_scale_f32 v29, s[2:3], v28, v28, 1.0
	v_rcp_f32_e32 v30, v29
	s_nop 0
	v_fma_f32 v31, -v29, v30, 1.0
	v_fmac_f32_e32 v30, v31, v30
	v_div_scale_f32 v31, vcc, 1.0, v28, 1.0
	v_mul_f32_e32 v32, v31, v30
	v_fma_f32 v33, -v29, v32, v31
	v_fmac_f32_e32 v32, v33, v30
	v_fma_f32 v29, -v29, v32, v31
	v_div_fmas_f32 v29, v29, v30, v32
	v_div_fixup_f32 v28, v29, v28, 1.0
	v_pk_mul_f32 v[26:27], v[26:27], v[28:29] op_sel_hi:[1,0]
	s_waitcnt vmcnt(18)
	v_lshlrev_b32_e32 v28, 16, v100
	v_pk_mul_f32 v[26:27], v[58:59], v[26:27]
	v_and_b32_e32 v29, 0xffff0000, v100
	v_cvt_pk_bf16_f32 v26, v26, v27
	global_store_dword v[24:25], v26, off offset:3072
	v_lshlrev_b32_e32 v26, 16, v99
	v_and_b32_e32 v27, 0xffff0000, v99
	v_pk_fma_f32 v[26:27], v[40:41], v[28:29], v[26:27] neg_lo:[1,0,0] neg_hi:[1,0,0]
	s_nop 0
	v_pk_mul_f32 v[28:29], v[26:27], v[26:27]
	s_nop 0
	v_add_f32_e32 v28, v28, v29
	s_nop 1
	v_mov_b32_dpp v29, v28 quad_perm:[1,0,3,2] row_mask:0xf bank_mask:0xf
	s_waitcnt lgkmcnt(0)
	v_add_f32_e32 v28, v28, v29
	s_nop 1
	v_mov_b32_dpp v29, v28 quad_perm:[2,3,0,1] row_mask:0xf bank_mask:0xf
	s_waitcnt lgkmcnt(0)
	v_add_f32_e32 v28, v28, v29
	s_nop 1
	v_mov_b32_dpp v29, v28 row_half_mirror row_mask:0xf bank_mask:0xf
	s_waitcnt lgkmcnt(0)
	v_add_f32_e32 v28, v28, v29
	s_nop 1
	v_mov_b32_dpp v29, v28 row_mirror row_mask:0xf bank_mask:0xf
	s_waitcnt lgkmcnt(0)
	v_add_f32_e32 v28, v28, v29
	v_mov_b32_e32 v29, v28
	s_nop 1
	v_permlane16_swap_b32_e32 v28, v29
	s_waitcnt lgkmcnt(0)
	v_add_f32_e32 v28, v28, v29
	v_mov_b32_e32 v29, v28
	s_nop 1
	v_permlane32_swap_b32_e32 v28, v29
	s_waitcnt lgkmcnt(0)
; #define GAS __attribute__((address_space(1)))
; __device__ __forceinline__ unsigned pk2(float lo, float hi) { f32x2_m v = {lo, hi}; bf16x2_m b = __builtin_convertvector(v, bf16x2_m); return __builtin_bit_cast(unsigned, b); }
; __device__ __forceinline__ float bflo(unsigned w) { return __uint_as_float(w << 16); }
; __device__ __forceinline__ float bfhi(unsigned w) { return __uint_as_float(w & 0xffff0000u); }
; template <bool F8> __device__ __forceinline__ void mix_phase(const Ctx& C, const bf16* YCONV, const bf16* YSWA, const bf16* ODIFF, const float* conv_g, const float* swa_g, const float* lq1, const float* lk1, const float* lq2, const float* lk2, ...
;     ...
; #pragma unroll
;             for (int h = 0; h < 6; ++h) { const unsigned a = oa[q][h], bq = ob[q][h];
;                 const float v0 = bflo(a) - lam * bflo(bq), v1 = bfhi(a) - lam * bfhi(bq);
;                 const float r = 1.0f / sqrtf(wave_sum(v0 * v0 + v1 * v1) * (1.0f / 128.0f) + LN_EPS);
;                 if constexpr (F8) *(GAS unsigned short*)(MIX8 + (size_t)m * DM + 1280 + 128 * h + 2 * l) = (unsigned short)pk4_fp8m(v0 * r * gA, v1 * r * gB, 0.f, 0.f);
;                 else *(GAS unsigned*)(MIX + (size_t)m * DM + 1280 + 128 * h + 2 * l) = pk2(v0 * r * gA, v1 * r * gB); } }
;     }
	v_add_f32_e32 v28, v28, v29
	v_fmamk_f32 v28, v28, 0x3c000000, v210
	v_cmp_gt_f32_e32 vcc, s18, v28
	v_mul_f32_e32 v29, 0x4f800000, v28
	s_nop 0
	v_cndmask_b32_e32 v28, v28, v29, vcc
	v_sqrt_f32_e32 v29, v28
	s_nop 0
	v_add_u32_e32 v30, -1, v29
	v_fma_f32 v31, -v30, v29, v28
	v_cmp_ge_f32_e64 s[2:3], 0, v31
	v_add_u32_e32 v31, 1, v29
	s_nop 0
	v_cndmask_b32_e64 v30, v29, v30, s[2:3]
	v_fma_f32 v29, -v31, v29, v28
	v_cmp_lt_f32_e64 s[2:3], 0, v29
	s_nop 1
	v_cndmask_b32_e64 v29, v30, v31, s[2:3]
	v_mul_f32_e32 v30, 0x37800000, v29
	v_cndmask_b32_e32 v29, v29, v30, vcc
	v_cmp_class_f32_e32 vcc, v28, v211
	s_nop 1
	v_cndmask_b32_e32 v28, v29, v28, vcc
	v_div_scale_f32 v29, s[2:3], v28, v28, 1.0
	v_rcp_f32_e32 v30, v29
	s_nop 0
	v_fma_f32 v31, -v29, v30, 1.0
	v_fmac_f32_e32 v30, v31, v30
	v_div_scale_f32 v31, vcc, 1.0, v28, 1.0
	v_mul_f32_e32 v32, v31, v30
	v_fma_f32 v33, -v29, v32, v31
	v_fmac_f32_e32 v32, v33, v30
	v_fma_f32 v29, -v29, v32, v31
	v_div_fmas_f32 v29, v29, v30, v32
	v_div_fixup_f32 v28, v29, v28, 1.0
	v_pk_mul_f32 v[26:27], v[26:27], v[28:29] op_sel_hi:[1,0]
	s_waitcnt vmcnt(17)
	v_lshlrev_b32_e32 v28, 16, v98
	v_pk_mul_f32 v[26:27], v[58:59], v[26:27]
	v_and_b32_e32 v29, 0xffff0000, v98
	v_cvt_pk_bf16_f32 v26, v26, v27
	global_store_dword v[24:25], v26, off offset:3328
	v_lshlrev_b32_e32 v26, 16, v97
	v_and_b32_e32 v27, 0xffff0000, v97
	v_pk_fma_f32 v[26:27], v[40:41], v[28:29], v[26:27] neg_lo:[1,0,0] neg_hi:[1,0,0]
	s_nop 0
	v_pk_mul_f32 v[28:29], v[26:27], v[26:27]
	s_nop 0
	v_add_f32_e32 v28, v28, v29
	s_nop 1
	v_mov_b32_dpp v29, v28 quad_perm:[1,0,3,2] row_mask:0xf bank_mask:0xf
	s_waitcnt lgkmcnt(0)
	v_add_f32_e32 v28, v28, v29
	s_nop 1
	v_mov_b32_dpp v29, v28 quad_perm:[2,3,0,1] row_mask:0xf bank_mask:0xf
	s_waitcnt lgkmcnt(0)
	v_add_f32_e32 v28, v28, v29
	s_nop 1
	v_mov_b32_dpp v29, v28 row_half_mirror row_mask:0xf bank_mask:0xf
	s_waitcnt lgkmcnt(0)
	v_add_f32_e32 v28, v28, v29
	s_nop 1
	v_mov_b32_dpp v29, v28 row_mirror row_mask:0xf bank_mask:0xf
	s_waitcnt lgkmcnt(0)
	v_add_f32_e32 v28, v28, v29
	v_mov_b32_e32 v29, v28
	s_nop 1
	v_permlane16_swap_b32_e32 v28, v29
	s_waitcnt lgkmcnt(0)
	v_add_f32_e32 v28, v28, v29
	v_mov_b32_e32 v29, v28
	s_nop 1
	v_permlane32_swap_b32_e32 v28, v29
	s_waitcnt lgkmcnt(0)
	v_add_f32_e32 v28, v28, v29
	v_fmamk_f32 v28, v28, 0x3c000000, v210
	v_cmp_gt_f32_e32 vcc, s18, v28
	v_mul_f32_e32 v29, 0x4f800000, v28
	s_nop 0
	v_cndmask_b32_e32 v28, v28, v29, vcc
	v_sqrt_f32_e32 v29, v28
	s_nop 0
	v_add_u32_e32 v30, -1, v29
	v_fma_f32 v31, -v30, v29, v28
	v_cmp_ge_f32_e64 s[2:3], 0, v31
	v_add_u32_e32 v31, 1, v29
	s_nop 0
	v_cndmask_b32_e64 v30, v29, v30, s[2:3]
	v_fma_f32 v29, -v31, v29, v28
	v_cmp_lt_f32_e64 s[2:3], 0, v29
	s_nop 1
	v_cndmask_b32_e64 v29, v30, v31, s[2:3]
	v_mul_f32_e32 v30, 0x37800000, v29
	v_cndmask_b32_e32 v29, v29, v30, vcc
	v_cmp_class_f32_e32 vcc, v28, v211
	s_nop 1
	v_cndmask_b32_e32 v28, v29, v28, vcc
	v_div_scale_f32 v29, s[2:3], v28, v28, 1.0
	v_rcp_f32_e32 v30, v29
	s_nop 0
	v_fma_f32 v31, -v29, v30, 1.0
	v_fmac_f32_e32 v30, v31, v30
	v_div_scale_f32 v31, vcc, 1.0, v28, 1.0
	v_mul_f32_e32 v32, v31, v30
	v_fma_f32 v33, -v29, v32, v31
	v_fmac_f32_e32 v32, v33, v30
	v_fma_f32 v29, -v29, v32, v31
	v_div_fmas_f32 v29, v29, v30, v32
	v_div_fixup_f32 v28, v29, v28, 1.0
	v_pk_mul_f32 v[26:27], v[26:27], v[28:29] op_sel_hi:[1,0]
	s_waitcnt vmcnt(16)
	v_lshlrev_b32_e32 v28, 16, v96
	v_pk_mul_f32 v[26:27], v[58:59], v[26:27]
	v_and_b32_e32 v29, 0xffff0000, v96
	v_cvt_pk_bf16_f32 v26, v26, v27
	global_store_dword v[24:25], v26, off offset:3584
	v_lshlrev_b32_e32 v26, 16, v95
	v_and_b32_e32 v27, 0xffff0000, v95
	v_pk_fma_f32 v[26:27], v[40:41], v[28:29], v[26:27] neg_lo:[1,0,0] neg_hi:[1,0,0]
	s_nop 0
	v_pk_mul_f32 v[28:29], v[26:27], v[26:27]
	s_nop 0
	v_add_f32_e32 v28, v28, v29
	s_nop 1
	v_mov_b32_dpp v29, v28 quad_perm:[1,0,3,2] row_mask:0xf bank_mask:0xf
	s_waitcnt lgkmcnt(0)
	v_add_f32_e32 v28, v28, v29
	s_nop 1
	v_mov_b32_dpp v29, v28 quad_perm:[2,3,0,1] row_mask:0xf bank_mask:0xf
	s_waitcnt lgkmcnt(0)
	v_add_f32_e32 v28, v28, v29
	s_nop 1
	v_mov_b32_dpp v29, v28 row_half_mirror row_mask:0xf bank_mask:0xf
	s_waitcnt lgkmcnt(0)
	v_add_f32_e32 v28, v28, v29
	s_nop 1
	v_mov_b32_dpp v29, v28 row_mirror row_mask:0xf bank_mask:0xf
	s_waitcnt lgkmcnt(0)
	v_add_f32_e32 v28, v28, v29
	v_mov_b32_e32 v29, v28
	s_nop 1
	v_permlane16_swap_b32_e32 v28, v29
	s_waitcnt lgkmcnt(0)
	v_add_f32_e32 v28, v28, v29
	v_mov_b32_e32 v29, v28
	s_nop 1
	v_permlane32_swap_b32_e32 v28, v29
	s_waitcnt lgkmcnt(0)
	v_add_f32_e32 v28, v28, v29
	v_fmamk_f32 v28, v28, 0x3c000000, v210
	v_cmp_gt_f32_e32 vcc, s18, v28
	v_mul_f32_e32 v29, 0x4f800000, v28
	s_nop 0
	v_cndmask_b32_e32 v28, v28, v29, vcc
	v_sqrt_f32_e32 v29, v28
	s_nop 0
	v_add_u32_e32 v30, -1, v29
	v_fma_f32 v31, -v30, v29, v28
	v_cmp_ge_f32_e64 s[2:3], 0, v31
	v_add_u32_e32 v31, 1, v29
	s_nop 0
	v_cndmask_b32_e64 v30, v29, v30, s[2:3]
	v_fma_f32 v29, -v31, v29, v28
	v_cmp_lt_f32_e64 s[2:3], 0, v29
	s_nop 1
	v_cndmask_b32_e64 v29, v30, v31, s[2:3]
	v_mul_f32_e32 v30, 0x37800000, v29
	v_cndmask_b32_e32 v29, v29, v30, vcc
	v_cmp_class_f32_e32 vcc, v28, v211
	s_nop 1
	v_cndmask_b32_e32 v28, v29, v28, vcc
	v_div_scale_f32 v29, s[2:3], v28, v28, 1.0
	v_rcp_f32_e32 v30, v29
	s_nop 0
	v_fma_f32 v31, -v29, v30, 1.0
	v_fmac_f32_e32 v30, v31, v30
	v_div_scale_f32 v31, vcc, 1.0, v28, 1.0
	v_mul_f32_e32 v32, v31, v30
	v_fma_f32 v33, -v29, v32, v31
	v_fmac_f32_e32 v32, v33, v30
	v_fma_f32 v29, -v29, v32, v31
	v_div_fmas_f32 v29, v29, v30, v32
	v_div_fixup_f32 v28, v29, v28, 1.0
	v_pk_mul_f32 v[26:27], v[26:27], v[28:29] op_sel_hi:[1,0]
	s_nop 0
	v_pk_mul_f32 v[26:27], v[58:59], v[26:27]
	s_nop 0
	v_cvt_pk_bf16_f32 v26, v26, v27
	global_store_dword v[24:25], v26, off offset:3840
	s_cbranch_scc1 .LBB0_718

; #define GAS __attribute__((address_space(1)))
; __device__ __forceinline__ float bflo(unsigned w) { return __uint_as_float(w << 16); }
; __device__ __forceinline__ float bfhi(unsigned w) { return __uint_as_float(w & 0xffff0000u); }
; template <bool F8> __device__ __forceinline__ void mix_phase(const Ctx& C, const bf16* YCONV, const bf16* YSWA, const bf16* ODIFF, const float* conv_g, const float* swa_g, const float* lq1, const float* lk1, const float* lq2, const float* lk2, ...
;     bf16* MIX = (bf16*)MIX8; constexpr float SMX_ = F8 ? SMX : 1.0f;
;     const float lam = __expf(wave_sum(lq1[C.lane] * lk1[C.lane])) - __expf(wave_sum(lq2[C.lane] * lk2[C.lane])) + lambda_init;
;     const float osc = 1.0f - lambda_init;
;     const int l = C.lane;
;     const int vh = l >> 5, dd = 2 * (l & 31); const float gA = sub_g[2 * l] * (osc * SMX_), gB = sub_g[2 * l + 1] * (osc * SMX_);
;     const f32x4 cg0 = *(const GAS f32x4*)(conv_g + 8 * l) * SMX_, cg1 = *(const GAS f32x4*)(conv_g + 8 * l + 4) * SMX_;
;     const f32x4 sg0 = *(const GAS f32x4*)(swa_g + 8 * l) * SMX_, sg1 = *(const GAS f32x4*)(swa_g + 8 * l + 4) * SMX_, sg2 = *(const GAS f32x4*)(swa_g + 512 + 4 * l) * SMX_;
;     constexpr int NR = 2;
;     for (int m0 = C.gw; m0 < T; m0 += NR * C.NGW) {
;         v4u yc[NR], ys[NR]; v2u ys2[NR]; unsigned oa[NR][6], ob[NR][6];
; #pragma unroll
;         for (int q = 0; q < NR; ++q) { const int m = m0 + q * C.NGW;
;             yc[q] = *(const GAS v4u*)(YCONV + (size_t)m * 512 + 8 * l); ys[q] = *(const GAS v4u*)(YSWA + (size_t)m * 768 + 8 * l); ys2[q] = *(const GAS v2u*)(YSWA + (size_t)m * 768 + 512 + 4 * l);
; #pragma unroll
;             for (int h = 0; h < 6; ++h) { const bf16* op = ODIFF + (size_t)m * 1536 + 64 * (4 * h + vh) + dd; oa[q][h] = *(const GAS unsigned*)op; ob[q][h] = *(const GAS unsigned*)(op + 128); } }
; #pragma unroll
;         for (int q = 0; q < NR; ++q) { const int m = m0 + q * C.NGW;
;             { const v4u y = yc[q];
;               float f[8] = {bflo(y.x), bfhi(y.x), bflo(y.y), bfhi(y.y), bflo(y.z), bfhi(y.z), bflo(y.w), bfhi(y.w)}; float ss = 0.f;
; #pragma unroll
;               for (int i = 0; i < 8; ++i) ss += f[i] * f[i];
;               const float r = 1.0f / sqrtf(wave_sum(ss) * (1.0f / 512.0f) + RMS_EPS);
.LBB0_723:
	v_lshl_add_u64 v[4:5], s[12:13], 0, v[84:85]
	global_load_dwordx4 v[16:19], v[4:5], off
	v_lshl_add_u64 v[4:5], s[12:13], 0, v[80:81]
	global_load_dwordx4 v[12:15], v[4:5], off
	v_lshl_add_u64 v[4:5], s[12:13], 0, v[82:83]
	global_load_dwordx2 v[88:89], v[4:5], off
	v_lshl_add_u64 v[4:5], s[12:13], 0, v[68:69]
	v_add_co_u32_e32 v4, vcc, s17, v4
	v_lshl_add_u64 v[98:99], s[12:13], 0, v[24:25]
	s_nop 0
	v_addc_co_u32_e32 v5, vcc, 0, v5, vcc
	global_load_dword v120, v[4:5], off
	global_load_dword v121, v[4:5], off offset:256
	v_lshl_add_u64 v[4:5], s[12:13], 0, v[70:71]
	v_add_co_u32_e32 v4, vcc, s17, v4
	v_lshl_add_u64 v[86:87], s[12:13], 0, v[58:59]
	s_nop 0
	v_addc_co_u32_e32 v5, vcc, 0, v5, vcc
	global_load_dword v118, v[4:5], off
	global_load_dword v119, v[4:5], off offset:256
	v_lshl_add_u64 v[4:5], s[12:13], 0, v[72:73]
	v_add_co_u32_e32 v4, vcc, s17, v4
	s_addk_i32 s4, 0x1000
	s_nop 0
	v_addc_co_u32_e32 v5, vcc, 0, v5, vcc
	global_load_dword v116, v[4:5], off
	global_load_dword v117, v[4:5], off offset:256
	v_lshl_add_u64 v[4:5], s[12:13], 0, v[74:75]
	v_add_co_u32_e32 v4, vcc, s17, v4
	v_lshl_add_u64 v[24:25], v[24:25], 0, s[24:25]
	s_nop 0
	v_addc_co_u32_e32 v5, vcc, 0, v5, vcc
	global_load_dword v114, v[4:5], off
	global_load_dword v115, v[4:5], off offset:256
	v_lshl_add_u64 v[4:5], s[12:13], 0, v[76:77]
	v_add_co_u32_e32 v4, vcc, s17, v4
	v_lshl_add_u64 v[58:59], v[58:59], 0, s[26:27]
	s_nop 0
	v_addc_co_u32_e32 v5, vcc, 0, v5, vcc
	global_load_dword v112, v[4:5], off
	global_load_dword v113, v[4:5], off offset:256
	v_lshl_add_u64 v[4:5], s[12:13], 0, v[78:79]
	v_add_co_u32_e32 v4, vcc, s17, v4
	v_lshl_add_u64 v[68:69], v[68:69], 0, s[24:25]
	s_nop 0
	v_addc_co_u32_e32 v5, vcc, 0, v5, vcc
	global_load_dword v110, v[4:5], off
	global_load_dword v111, v[4:5], off offset:256
	v_lshl_add_u64 v[4:5], s[12:13], 0, v[60:61]
	v_add_co_u32_e32 v98, vcc, s17, v98
	global_load_dwordx4 v[8:11], v[4:5], off
	s_nop 0
	v_addc_co_u32_e32 v99, vcc, 0, v99, vcc
	global_load_dwordx2 v[86:87], v[86:87], off
	v_lshl_add_u64 v[4:5], s[12:13], 0, v[56:57]
	global_load_dwordx4 v[4:7], v[4:5], off
	s_nop 0
	global_load_dword v108, v[98:99], off
	global_load_dword v109, v[98:99], off offset:256
	v_lshl_add_u64 v[98:99], s[12:13], 0, v[26:27]
	v_add_co_u32_e32 v98, vcc, s17, v98
	v_lshl_add_u64 v[26:27], v[26:27], 0, s[24:25]
	s_nop 0
	v_addc_co_u32_e32 v99, vcc, 0, v99, vcc
	global_load_dword v106, v[98:99], off
	global_load_dword v107, v[98:99], off offset:256
	v_lshl_add_u64 v[98:99], s[12:13], 0, v[28:29]
	v_add_co_u32_e32 v98, vcc, s17, v98
	v_lshl_add_u64 v[28:29], v[28:29], 0, s[24:25]
	s_nop 0
	v_addc_co_u32_e32 v99, vcc, 0, v99, vcc
	global_load_dword v104, v[98:99], off
	global_load_dword v105, v[98:99], off offset:256
	v_lshl_add_u64 v[98:99], s[12:13], 0, v[30:31]
	v_add_co_u32_e32 v98, vcc, s17, v98
	v_lshl_add_u64 v[30:31], v[30:31], 0, s[24:25]
	s_nop 0
	v_addc_co_u32_e32 v99, vcc, 0, v99, vcc
	global_load_dword v102, v[98:99], off
	global_load_dword v103, v[98:99], off offset:256
	v_lshl_add_u64 v[98:99], s[12:13], 0, v[32:33]
	v_add_co_u32_e32 v98, vcc, s17, v98
	s_waitcnt vmcnt(25)
	v_lshlrev_b32_e32 v124, 16, v18
	v_addc_co_u32_e32 v99, vcc, 0, v99, vcc
	global_load_dword v100, v[98:99], off
	global_load_dword v101, v[98:99], off offset:256
	v_lshl_add_u64 v[98:99], s[12:13], 0, v[34:35]
	v_add_co_u32_e32 v122, vcc, s17, v98
	v_and_b32_e32 v125, 0xffff0000, v18
	s_nop 0
	v_addc_co_u32_e32 v123, vcc, 0, v99, vcc
	global_load_dword v98, v[122:123], off
	global_load_dword v99, v[122:123], off offset:256
	v_lshlrev_b32_e32 v122, 16, v16
	v_and_b32_e32 v16, 0xffff0000, v16
	v_mul_f32_e32 v18, v16, v16
	v_lshlrev_b32_e32 v123, 16, v17
	v_fmac_f32_e32 v18, v122, v122
	v_and_b32_e32 v17, 0xffff0000, v17
	v_fmac_f32_e32 v18, v123, v123
	v_fmac_f32_e32 v18, v17, v17
	v_fmac_f32_e32 v18, v124, v124
	v_lshlrev_b32_e32 v126, 16, v19
	v_fmac_f32_e32 v18, v125, v125
	v_and_b32_e32 v19, 0xffff0000, v19
	v_fmac_f32_e32 v18, v126, v126
	v_fmac_f32_e32 v18, v19, v19
	s_nop 1
	v_mov_b32_dpp v127, v18 quad_perm:[1,0,3,2] row_mask:0xf bank_mask:0xf
	v_lshl_add_u64 v[32:33], v[32:33], 0, s[24:25]
	v_lshl_add_u64 v[34:35], v[34:35], 0, s[24:25]
	v_lshl_add_u64 v[56:57], v[56:57], 0, s[26:27]
	v_lshl_add_u64 v[60:61], v[60:61], 0, s[22:23]
	s_waitcnt lgkmcnt(0)
	v_add_f32_e32 v18, v18, v127
	s_nop 1
	v_mov_b32_dpp v127, v18 quad_perm:[2,3,0,1] row_mask:0xf bank_mask:0xf
	v_lshl_add_u64 v[70:71], v[70:71], 0, s[24:25]
	v_lshl_add_u64 v[72:73], v[72:73], 0, s[24:25]
	v_lshl_add_u64 v[74:75], v[74:75], 0, s[24:25]
	v_lshl_add_u64 v[76:77], v[76:77], 0, s[24:25]
	s_waitcnt lgkmcnt(0)
	v_add_f32_e32 v18, v18, v127
	s_nop 1
	v_mov_b32_dpp v127, v18 row_half_mirror row_mask:0xf bank_mask:0xf
	v_lshl_add_u64 v[78:79], v[78:79], 0, s[24:25]
	v_lshl_add_u64 v[80:81], v[80:81], 0, s[26:27]
	v_lshl_add_u64 v[82:83], v[82:83], 0, s[26:27]
	v_lshl_add_u64 v[84:85], v[84:85], 0, s[22:23]
	s_waitcnt lgkmcnt(0)
	v_add_f32_e32 v18, v18, v127
	s_nop 1
	v_mov_b32_dpp v127, v18 row_mirror row_mask:0xf bank_mask:0xf
	s_cmpk_gt_i32 s4, 0x2fff
	s_waitcnt lgkmcnt(0)
	v_add_f32_e32 v18, v18, v127
	v_mov_b32_e32 v127, v18
	s_nop 1
	v_permlane16_swap_b32_e32 v18, v127
	s_waitcnt lgkmcnt(0)
	v_add_f32_e32 v18, v18, v127
	v_mov_b32_e32 v127, v18
	s_nop 1
	v_permlane32_swap_b32_e32 v18, v127
	s_waitcnt lgkmcnt(0)
; #define GAS __attribute__((address_space(1)))
; __device__ __forceinline__ unsigned pk2(float lo, float hi) { f32x2_m v = {lo, hi}; bf16x2_m b = __builtin_convertvector(v, bf16x2_m); return __builtin_bit_cast(unsigned, b); }
; __device__ __forceinline__ float bflo(unsigned w) { return __uint_as_float(w << 16); }
; template <bool F8> __device__ __forceinline__ void mix_phase(const Ctx& C, const bf16* YCONV, const bf16* YSWA, const bf16* ODIFF, const float* conv_g, const float* swa_g, const float* lq1, const float* lk1, const float* lq2, const float* lk2, ...
;     ...
;             { const v4u y = yc[q];
;               float f[8] = {bflo(y.x), bfhi(y.x), bflo(y.y), bfhi(y.y), bflo(y.z), bfhi(y.z), bflo(y.w), bfhi(y.w)}; float ss = 0.f;
; #pragma unroll
;               for (int i = 0; i < 8; ++i) ss += f[i] * f[i];
;               const float r = 1.0f / sqrtf(wave_sum(ss) * (1.0f / 512.0f) + RMS_EPS);
;               if constexpr (F8) { v2u o; o.x = pk4_fp8m(f[0] * r * cg0.x, f[1] * r * cg0.y, f[2] * r * cg0.z, f[3] * r * cg0.w); o.y = pk4_fp8m(f[4] * r * cg1.x, f[5] * r * cg1.y, f[6] * r * cg1.z, f[7] * r * cg1.w);
;                 *(GAS v2u*)(MIX8 + (size_t)m * DM + 8 * l) = o; }
;               else { v4u o; o.x = pk2(f[0] * r * cg0.x, f[1] * r * cg0.y); o.y = pk2(f[2] * r * cg0.z, f[3] * r * cg0.w); o.z = pk2(f[4] * r * cg1.x, f[5] * r * cg1.y); o.w = pk2(f[6] * r * cg1.z, f[7] * r * cg1.w);
;                 *(GAS v4u*)(MIX + (size_t)m * DM + 8 * l) = o; } }
;             { const v4u y = ys[q]; const v2u y2 = ys2[q];
;               float f[12] = {bflo(y.x), bfhi(y.x), bflo(y.y), bfhi(y.y), bflo(y.z), bfhi(y.z), bflo(y.w), bfhi(y.w), bflo(y2.x), bfhi(y2.x), bflo(y2.y), bfhi(y2.y)}; float ss = 0.f;
; #pragma unroll
;               for (int i = 0; i < 12; ++i) ss += f[i] * f[i];
;               const float r = 1.0f / sqrtf(wave_sum(ss) * (1.0f / 768.0f) + RMS_EPS);
;               if constexpr (F8) { v2u o; o.x = pk4_fp8m(f[0] * r * sg0.x, f[1] * r * sg0.y, f[2] * r * sg0.z, f[3] * r * sg0.w); o.y = pk4_fp8m(f[4] * r * sg1.x, f[5] * r * sg1.y, f[6] * r * sg1.z, f[7] * r * sg1.w);
;                 const unsigned o2 = pk4_fp8m(f[8] * r * sg2.x, f[9] * r * sg2.y, f[10] * r * sg2.z, f[11] * r * sg2.w);
;                 *(GAS v2u*)(MIX8 + (size_t)m * DM + 512 + 8 * l) = o; *(GAS unsigned*)(MIX8 + (size_t)m * DM + 1024 + 4 * l) = o2; }
	v_add_f32_e32 v18, v18, v127
	v_fmamk_f32 v18, v18, 0x3b000000, v212
	v_cmp_gt_f32_e32 vcc, s16, v18
	v_mul_f32_e32 v127, 0x4f800000, v18
	s_nop 0
	v_cndmask_b32_e32 v18, v18, v127, vcc
	v_sqrt_f32_e32 v127, v18
	s_nop 0
	v_add_u32_e32 v128, -1, v127
	v_fma_f32 v129, -v128, v127, v18
	v_cmp_ge_f32_e64 s[2:3], 0, v129
	v_add_u32_e32 v129, 1, v127
	s_nop 0
	v_cndmask_b32_e64 v128, v127, v128, s[2:3]
	v_fma_f32 v127, -v129, v127, v18
	v_cmp_lt_f32_e64 s[2:3], 0, v127
	s_nop 1
	v_cndmask_b32_e64 v127, v128, v129, s[2:3]
	v_mul_f32_e32 v128, 0x37800000, v127
	v_cndmask_b32_e32 v127, v127, v128, vcc
	v_cmp_class_f32_e32 vcc, v18, v211
	s_nop 1
	v_cndmask_b32_e32 v18, v127, v18, vcc
	v_div_scale_f32 v127, s[0:1], v18, v18, 1.0
	v_rcp_f32_e32 v128, v127
	s_nop 0
	v_fma_f32 v129, -v127, v128, 1.0
	v_fmac_f32_e32 v128, v129, v128
	v_div_scale_f32 v129, vcc, 1.0, v18, 1.0
	v_mul_f32_e32 v130, v129, v128
	v_fma_f32 v131, -v127, v130, v129
	v_fmac_f32_e32 v130, v131, v128
	v_fma_f32 v127, -v127, v130, v129
	v_div_fmas_f32 v127, v127, v128, v130
	v_div_fixup_f32 v127, v127, v18, 1.0
	v_mul_f32_e32 v18, v127, v122
	v_mul_f32_e32 v16, v127, v16
	v_mul_f32_e32 v18, v42, v18
	v_mul_f32_e32 v16, v43, v16
	v_mul_f32_e32 v122, v127, v123
	v_med3_f32 v123, v18, s33, v214
	v_med3_f32 v16, v16, s33, v214
	v_mov_b32_e32 v18, v2
	v_cvt_pk_fp8_f32 v18, v123, v16
	v_mul_f32_e32 v17, v127, v17
	v_mul_f32_e32 v122, v40, v122
	v_mul_f32_e32 v17, v41, v17
	v_med3_f32 v122, v122, s33, v214
	v_med3_f32 v17, v17, s33, v214
	v_cvt_pk_fp8_f32 v18, v122, v17 op_sel:[0,0,1]
	v_mul_f32_e32 v16, v127, v124
	v_mul_f32_e32 v17, v127, v125
	v_mul_f32_e32 v19, v127, v19
	v_mul_f32_e32 v16, v38, v16
	v_mul_f32_e32 v17, v39, v17
	v_mul_f32_e32 v19, v37, v19
	v_med3_f32 v16, v16, s33, v214
	v_med3_f32 v17, v17, s33, v214
	v_med3_f32 v123, v19, s33, v214
	v_mov_b32_e32 v19, v2
	v_cvt_pk_fp8_f32 v19, v16, v17
	v_mul_f32_e32 v122, v127, v126
	v_mul_f32_e32 v122, v36, v122
	v_med3_f32 v122, v122, s33, v214
	v_cvt_pk_fp8_f32 v19, v122, v123 op_sel:[0,0,1]
	v_lshl_add_u64 v[16:17], s[12:13], 0, v[66:67]
	v_add_co_u32_e32 v16, vcc, s18, v16
	s_waitcnt vmcnt(28)
	v_lshlrev_b32_e32 v122, 16, v14
	v_addc_co_u32_e32 v17, vcc, 0, v17, vcc
	global_store_dwordx2 v[16:17], v[18:19], off
	v_lshlrev_b32_e32 v18, 16, v12
	v_and_b32_e32 v12, 0xffff0000, v12
	v_mul_f32_e32 v126, v12, v12
	v_lshlrev_b32_e32 v19, 16, v13
	v_fmac_f32_e32 v126, v18, v18
	v_and_b32_e32 v13, 0xffff0000, v13
	v_fmac_f32_e32 v126, v19, v19
	v_fmac_f32_e32 v126, v13, v13
	v_and_b32_e32 v14, 0xffff0000, v14
	v_fmac_f32_e32 v126, v122, v122
	v_lshlrev_b32_e32 v123, 16, v15
	v_fmac_f32_e32 v126, v14, v14
	v_and_b32_e32 v15, 0xffff0000, v15
	v_fmac_f32_e32 v126, v123, v123
	s_waitcnt vmcnt(28)
	v_lshlrev_b32_e32 v124, 16, v88
	v_fmac_f32_e32 v126, v15, v15
	v_and_b32_e32 v88, 0xffff0000, v88
	v_fmac_f32_e32 v126, v124, v124
	v_lshlrev_b32_e32 v125, 16, v89
	v_fmac_f32_e32 v126, v88, v88
	v_and_b32_e32 v89, 0xffff0000, v89
	v_fmac_f32_e32 v126, v125, v125
	v_fmac_f32_e32 v126, v89, v89
	s_nop 1
	v_mov_b32_dpp v127, v126 quad_perm:[1,0,3,2] row_mask:0xf bank_mask:0xf
	v_lshl_add_u64 v[66:67], v[66:67], 0, s[20:21]
	s_waitcnt lgkmcnt(0)
	v_add_f32_e32 v126, v126, v127
	s_nop 1
	v_mov_b32_dpp v127, v126 quad_perm:[2,3,0,1] row_mask:0xf bank_mask:0xf
	s_waitcnt lgkmcnt(0)
	v_add_f32_e32 v126, v126, v127
	s_nop 1
	v_mov_b32_dpp v127, v126 row_half_mirror row_mask:0xf bank_mask:0xf
	s_waitcnt lgkmcnt(0)
	v_add_f32_e32 v126, v126, v127
	s_nop 1
	v_mov_b32_dpp v127, v126 row_mirror row_mask:0xf bank_mask:0xf
	s_waitcnt lgkmcnt(0)
	v_add_f32_e32 v126, v126, v127
	v_mov_b32_e32 v127, v126
	s_nop 1
	v_permlane16_swap_b32_e32 v126, v127
	s_waitcnt lgkmcnt(0)
	v_add_f32_e32 v126, v126, v127
	v_mov_b32_e32 v127, v126
	s_nop 1
	v_permlane32_swap_b32_e32 v126, v127
	s_waitcnt lgkmcnt(0)
	v_add_f32_e32 v126, v126, v127
	v_fmamk_f32 v126, v126, 0x3aaaaaab, v212
	v_cmp_gt_f32_e32 vcc, s16, v126
	v_mul_f32_e32 v127, 0x4f800000, v126
	s_nop 0
	v_cndmask_b32_e32 v126, v126, v127, vcc
	v_sqrt_f32_e32 v127, v126
	s_nop 0
	v_add_u32_e32 v128, -1, v127
	v_fma_f32 v129, -v128, v127, v126
	v_cmp_ge_f32_e64 s[2:3], 0, v129
	v_add_u32_e32 v129, 1, v127
	s_nop 0
	v_cndmask_b32_e64 v128, v127, v128, s[2:3]
	v_fma_f32 v127, -v129, v127, v126
	v_cmp_lt_f32_e64 s[2:3], 0, v127
	s_nop 1
	v_cndmask_b32_e64 v127, v128, v129, s[2:3]
	v_mul_f32_e32 v128, 0x37800000, v127
	v_cndmask_b32_e32 v127, v127, v128, vcc
	v_cmp_class_f32_e32 vcc, v126, v211
	s_nop 1
	v_cndmask_b32_e32 v126, v127, v126, vcc
	v_div_scale_f32 v127, s[0:1], v126, v126, 1.0
	v_rcp_f32_e32 v128, v127
	s_nop 0
	v_fma_f32 v129, -v127, v128, 1.0
	v_fmac_f32_e32 v128, v129, v128
	v_div_scale_f32 v129, vcc, 1.0, v126, 1.0
	v_mul_f32_e32 v130, v129, v128
	v_fma_f32 v131, -v127, v130, v129
	v_fmac_f32_e32 v130, v131, v128
	v_fma_f32 v127, -v127, v130, v129
	v_div_fmas_f32 v127, v127, v128, v130
	v_div_fixup_f32 v126, v127, v126, 1.0
	v_mul_f32_e32 v18, v126, v18
	v_mul_f32_e32 v12, v126, v12
	v_mul_f32_e32 v18, v54, v18
	v_mul_f32_e32 v12, v55, v12
	v_med3_f32 v18, v18, s33, v214
	v_med3_f32 v127, v12, s33, v214
	v_mov_b32_e32 v12, v2
	v_cvt_pk_fp8_f32 v12, v18, v127
	v_mul_f32_e32 v19, v126, v19
	v_mul_f32_e32 v13, v126, v13
	v_mul_f32_e32 v19, v52, v19
	v_mul_f32_e32 v13, v53, v13
	v_med3_f32 v19, v19, s33, v214
	v_med3_f32 v13, v13, s33, v214
	v_cvt_pk_fp8_f32 v12, v19, v13 op_sel:[0,0,1]
	v_mul_f32_e32 v13, v126, v122
	v_mul_f32_e32 v14, v126, v14
	v_mul_f32_e32 v13, v50, v13
	v_mul_f32_e32 v14, v51, v14
	v_med3_f32 v19, v13, s33, v214
	v_med3_f32 v14, v14, s33, v214
	v_mov_b32_e32 v13, v2
	v_cvt_pk_fp8_f32 v13, v19, v14
	v_mul_f32_e32 v18, v126, v123
	v_mul_f32_e32 v15, v126, v15
	v_mul_f32_e32 v18, v48, v18
	v_mul_f32_e32 v15, v49, v15
	v_med3_f32 v18, v18, s33, v214
	v_med3_f32 v15, v15, s33, v214
	v_cvt_pk_fp8_f32 v13, v18, v15 op_sel:[0,0,1]
	v_mul_f32_e32 v14, v126, v124
	v_mul_f32_e32 v15, v126, v88
	v_mul_f32_e32 v14, v46, v14
	v_mul_f32_e32 v15, v47, v15
	v_med3_f32 v14, v14, s33, v214
	v_med3_f32 v15, v15, s33, v214
	v_mov_b32_e32 v88, v2
	v_cvt_pk_fp8_f32 v88, v14, v15
	s_waitcnt vmcnt(27)
; #define GAS __attribute__((address_space(1)))
; __device__ __forceinline__ unsigned pk2(float lo, float hi) { f32x2_m v = {lo, hi}; bf16x2_m b = __builtin_convertvector(v, bf16x2_m); return __builtin_bit_cast(unsigned, b); }
; __device__ __forceinline__ float bflo(unsigned w) { return __uint_as_float(w << 16); }
; __device__ __forceinline__ float bfhi(unsigned w) { return __uint_as_float(w & 0xffff0000u); }
; template <bool F8> __device__ __forceinline__ void mix_phase(const Ctx& C, const bf16* YCONV, const bf16* YSWA, const bf16* ODIFF, const float* conv_g, const float* swa_g, const float* lq1, const float* lk1, const float* lq2, const float* lk2, ...
;     ...
;               if constexpr (F8) { v2u o; o.x = pk4_fp8m(f[0] * r * sg0.x, f[1] * r * sg0.y, f[2] * r * sg0.z, f[3] * r * sg0.w); o.y = pk4_fp8m(f[4] * r * sg1.x, f[5] * r * sg1.y, f[6] * r * sg1.z, f[7] * r * sg1.w);
;                 const unsigned o2 = pk4_fp8m(f[8] * r * sg2.x, f[9] * r * sg2.y, f[10] * r * sg2.z, f[11] * r * sg2.w);
;                 *(GAS v2u*)(MIX8 + (size_t)m * DM + 512 + 8 * l) = o; *(GAS unsigned*)(MIX8 + (size_t)m * DM + 1024 + 4 * l) = o2; }
;               else { v4u o; o.x = pk2(f[0] * r * sg0.x, f[1] * r * sg0.y); o.y = pk2(f[2] * r * sg0.z, f[3] * r * sg0.w); o.z = pk2(f[4] * r * sg1.x, f[5] * r * sg1.y); o.w = pk2(f[6] * r * sg1.z, f[7] * r * sg1.w);
;                 v2u o2; o2.x = pk2(f[8] * r * sg2.x, f[9] * r * sg2.y); o2.y = pk2(f[10] * r * sg2.z, f[11] * r * sg2.w);
;                 *(GAS v4u*)(MIX + (size_t)m * DM + 512 + 8 * l) = o; *(GAS v2u*)(MIX + (size_t)m * DM + 1024 + 4 * l) = o2; } }
; #pragma unroll
;             for (int h = 0; h < 6; ++h) { const unsigned a = oa[q][h], bq = ob[q][h];
;                 const float v0 = bflo(a) - lam * bflo(bq), v1 = bfhi(a) - lam * bfhi(bq);
;                 const float r = 1.0f / sqrtf(wave_sum(v0 * v0 + v1 * v1) * (1.0f / 128.0f) + LN_EPS);
;                 if constexpr (F8) *(GAS unsigned short*)(MIX8 + (size_t)m * DM + 1280 + 128 * h + 2 * l) = (unsigned short)pk4_fp8m(v0 * r * gA, v1 * r * gB, 0.f, 0.f);
;                 else *(GAS unsigned*)(MIX + (size_t)m * DM + 1280 + 128 * h + 2 * l) = pk2(v0 * r * gA, v1 * r * gB); } }
	v_lshlrev_b32_e32 v14, 16, v120
	s_waitcnt vmcnt(26)
	v_lshlrev_b32_e32 v15, 16, v121
	global_store_dwordx2 v[16:17], v[12:13], off offset:512
	v_fma_f32 v14, -v95, v15, v14
	v_and_b32_e32 v15, 0xffff0000, v120
	v_and_b32_e32 v16, 0xffff0000, v121
	v_fma_f32 v15, -v95, v16, v15
	v_mul_f32_e32 v16, v15, v15
	v_fmac_f32_e32 v16, v14, v14
	s_nop 1
	v_mov_b32_dpp v17, v16 quad_perm:[1,0,3,2] row_mask:0xf bank_mask:0xf
	v_mul_f32_e32 v18, v126, v125
	v_mul_f32_e32 v19, v126, v89
	v_mul_f32_e32 v18, v44, v18
	v_mul_f32_e32 v19, v45, v19
	s_waitcnt lgkmcnt(0)
	v_add_f32_e32 v16, v16, v17
	s_nop 1
	v_mov_b32_dpp v17, v16 quad_perm:[2,3,0,1] row_mask:0xf bank_mask:0xf
	v_med3_f32 v18, v18, s33, v214
	v_med3_f32 v19, v19, s33, v214
	v_cvt_pk_fp8_f32 v88, v18, v19 op_sel:[0,0,1]
	v_lshl_add_u64 v[12:13], s[12:13], 0, v[64:65]
	s_waitcnt lgkmcnt(0)
	v_add_f32_e32 v16, v16, v17
	s_nop 1
	v_mov_b32_dpp v17, v16 row_half_mirror row_mask:0xf bank_mask:0xf
	global_store_dword v[12:13], v88, off
	v_lshl_add_u64 v[12:13], s[12:13], 0, v[62:63]
	v_lshl_add_u64 v[62:63], v[62:63], 0, s[20:21]
	v_lshl_add_u64 v[64:65], v[64:65], 0, s[20:21]
	s_waitcnt lgkmcnt(0)
	v_add_f32_e32 v16, v16, v17
	s_nop 1
	v_mov_b32_dpp v17, v16 row_mirror row_mask:0xf bank_mask:0xf
	s_waitcnt lgkmcnt(0)
	v_add_f32_e32 v16, v16, v17
	v_mov_b32_e32 v17, v16
	s_nop 1
	v_permlane16_swap_b32_e32 v16, v17
	s_waitcnt lgkmcnt(0)
	v_add_f32_e32 v16, v16, v17
	v_mov_b32_e32 v17, v16
	s_nop 1
	v_permlane32_swap_b32_e32 v16, v17
	s_waitcnt lgkmcnt(0)
	v_add_f32_e32 v16, v16, v17
	v_fmamk_f32 v16, v16, 0x3c000000, v210
	v_cmp_gt_f32_e32 vcc, s16, v16
	v_mul_f32_e32 v17, 0x4f800000, v16
	s_nop 0
	v_cndmask_b32_e32 v16, v16, v17, vcc
	v_sqrt_f32_e32 v17, v16
	s_nop 0
	v_add_u32_e32 v18, -1, v17
	v_fma_f32 v19, -v18, v17, v16
	v_cmp_ge_f32_e64 s[2:3], 0, v19
	v_add_u32_e32 v19, 1, v17
	s_nop 0
	v_cndmask_b32_e64 v18, v17, v18, s[2:3]
	v_fma_f32 v17, -v19, v17, v16
	v_cmp_lt_f32_e64 s[2:3], 0, v17
	s_nop 1
	v_cndmask_b32_e64 v17, v18, v19, s[2:3]
	v_mul_f32_e32 v18, 0x37800000, v17
	v_cndmask_b32_e32 v17, v17, v18, vcc
	v_cmp_class_f32_e32 vcc, v16, v211
	s_nop 1
	v_cndmask_b32_e32 v16, v17, v16, vcc
	v_div_scale_f32 v17, s[0:1], v16, v16, 1.0
	v_rcp_f32_e32 v18, v17
	s_nop 0
	v_fma_f32 v19, -v17, v18, 1.0
	v_fmac_f32_e32 v18, v19, v18
	v_div_scale_f32 v19, vcc, 1.0, v16, 1.0
	v_mul_f32_e32 v88, v19, v18
	v_fma_f32 v89, -v17, v88, v19
	v_fmac_f32_e32 v88, v89, v18
	v_fma_f32 v17, -v17, v88, v19
	v_div_fmas_f32 v17, v17, v18, v88
	v_div_fixup_f32 v16, v17, v16, 1.0
	v_mul_f32_e32 v14, v14, v16
	v_mul_f32_e32 v15, v15, v16
	v_mul_f32_e32 v14, v96, v14
	v_mul_f32_e32 v15, v97, v15
	v_med3_f32 v14, v14, s33, v214
	v_med3_f32 v15, v15, s33, v214
	v_mov_b32_e32 v16, v2
	v_cvt_pk_fp8_f32 v16, v14, v15
	v_add_co_u32_e32 v12, vcc, s18, v12
	s_waitcnt vmcnt(27)
	v_lshlrev_b32_e32 v14, 16, v118
	v_cvt_pk_fp8_f32 v16, 0, 0 op_sel:[0,0,1]
	v_addc_co_u32_e32 v13, vcc, 0, v13, vcc
	s_waitcnt vmcnt(26)
	v_lshlrev_b32_e32 v15, 16, v119
	global_store_short v[12:13], v16, off offset:1280
	v_fma_f32 v14, -v95, v15, v14
	v_and_b32_e32 v15, 0xffff0000, v118
	v_and_b32_e32 v16, 0xffff0000, v119
	v_fma_f32 v15, -v95, v16, v15
	v_mul_f32_e32 v16, v15, v15
	v_fmac_f32_e32 v16, v14, v14
	s_nop 1
	v_mov_b32_dpp v17, v16 quad_perm:[1,0,3,2] row_mask:0xf bank_mask:0xf
	s_waitcnt lgkmcnt(0)
	v_add_f32_e32 v16, v16, v17
	s_nop 1
	v_mov_b32_dpp v17, v16 quad_perm:[2,3,0,1] row_mask:0xf bank_mask:0xf
	s_waitcnt lgkmcnt(0)
	v_add_f32_e32 v16, v16, v17
	s_nop 1
	v_mov_b32_dpp v17, v16 row_half_mirror row_mask:0xf bank_mask:0xf
	s_waitcnt lgkmcnt(0)
	v_add_f32_e32 v16, v16, v17
	s_nop 1
	v_mov_b32_dpp v17, v16 row_mirror row_mask:0xf bank_mask:0xf
	s_waitcnt lgkmcnt(0)
	v_add_f32_e32 v16, v16, v17
	v_mov_b32_e32 v17, v16
	s_nop 1
	v_permlane16_swap_b32_e32 v16, v17
	s_waitcnt lgkmcnt(0)
	v_add_f32_e32 v16, v16, v17
	v_mov_b32_e32 v17, v16
	s_nop 1
	v_permlane32_swap_b32_e32 v16, v17
	s_waitcnt lgkmcnt(0)
	v_add_f32_e32 v16, v16, v17
	v_fmamk_f32 v16, v16, 0x3c000000, v210
	v_cmp_gt_f32_e32 vcc, s16, v16
	v_mul_f32_e32 v17, 0x4f800000, v16
	s_nop 0
	v_cndmask_b32_e32 v16, v16, v17, vcc
	v_sqrt_f32_e32 v17, v16
	s_nop 0
	v_add_u32_e32 v18, -1, v17
	v_fma_f32 v19, -v18, v17, v16
	v_cmp_ge_f32_e64 s[2:3], 0, v19
	v_add_u32_e32 v19, 1, v17
	s_nop 0
	v_cndmask_b32_e64 v18, v17, v18, s[2:3]
	v_fma_f32 v17, -v19, v17, v16
	v_cmp_lt_f32_e64 s[2:3], 0, v17
	s_nop 1
	v_cndmask_b32_e64 v17, v18, v19, s[2:3]
	v_mul_f32_e32 v18, 0x37800000, v17
	v_cndmask_b32_e32 v17, v17, v18, vcc
	v_cmp_class_f32_e32 vcc, v16, v211
	s_nop 1
	v_cndmask_b32_e32 v16, v17, v16, vcc
	v_div_scale_f32 v17, s[0:1], v16, v16, 1.0
	v_rcp_f32_e32 v18, v17
	s_nop 0
	v_fma_f32 v19, -v17, v18, 1.0
	v_fmac_f32_e32 v18, v19, v18
	v_div_scale_f32 v19, vcc, 1.0, v16, 1.0
	v_mul_f32_e32 v88, v19, v18
	v_fma_f32 v89, -v17, v88, v19
	v_fmac_f32_e32 v88, v89, v18
	v_fma_f32 v17, -v17, v88, v19
	v_div_fmas_f32 v17, v17, v18, v88
	v_div_fixup_f32 v16, v17, v16, 1.0
	v_mul_f32_e32 v14, v14, v16
	v_mul_f32_e32 v15, v15, v16
	v_mul_f32_e32 v14, v96, v14
	v_mul_f32_e32 v15, v97, v15
	v_med3_f32 v14, v14, s33, v214
	v_med3_f32 v15, v15, s33, v214
	v_mov_b32_e32 v16, v2
	v_cvt_pk_fp8_f32 v16, v14, v15
	s_waitcnt vmcnt(26)
	v_lshlrev_b32_e32 v14, 16, v116
	s_waitcnt vmcnt(25)
	v_lshlrev_b32_e32 v15, 16, v117
	v_fma_f32 v14, -v95, v15, v14
	v_cvt_pk_fp8_f32 v16, 0, 0 op_sel:[0,0,1]
	v_and_b32_e32 v15, 0xffff0000, v116
	global_store_short v[12:13], v16, off offset:1408
	v_and_b32_e32 v16, 0xffff0000, v117
	v_fma_f32 v15, -v95, v16, v15
	v_mul_f32_e32 v16, v15, v15
	v_fmac_f32_e32 v16, v14, v14
	s_nop 1
	v_mov_b32_dpp v17, v16 quad_perm:[1,0,3,2] row_mask:0xf bank_mask:0xf
	s_waitcnt lgkmcnt(0)
; #define GAS __attribute__((address_space(1)))
; __device__ __forceinline__ unsigned pk2(float lo, float hi) { f32x2_m v = {lo, hi}; bf16x2_m b = __builtin_convertvector(v, bf16x2_m); return __builtin_bit_cast(unsigned, b); }
; __device__ __forceinline__ float bflo(unsigned w) { return __uint_as_float(w << 16); }
; __device__ __forceinline__ float bfhi(unsigned w) { return __uint_as_float(w & 0xffff0000u); }
; template <bool F8> __device__ __forceinline__ void mix_phase(const Ctx& C, const bf16* YCONV, const bf16* YSWA, const bf16* ODIFF, const float* conv_g, const float* swa_g, const float* lq1, const float* lk1, const float* lq2, const float* lk2, ...
;     ...
; #pragma unroll
;             for (int h = 0; h < 6; ++h) { const unsigned a = oa[q][h], bq = ob[q][h];
;                 const float v0 = bflo(a) - lam * bflo(bq), v1 = bfhi(a) - lam * bfhi(bq);
;                 const float r = 1.0f / sqrtf(wave_sum(v0 * v0 + v1 * v1) * (1.0f / 128.0f) + LN_EPS);
;                 if constexpr (F8) *(GAS unsigned short*)(MIX8 + (size_t)m * DM + 1280 + 128 * h + 2 * l) = (unsigned short)pk4_fp8m(v0 * r * gA, v1 * r * gB, 0.f, 0.f);
;                 else *(GAS unsigned*)(MIX + (size_t)m * DM + 1280 + 128 * h + 2 * l) = pk2(v0 * r * gA, v1 * r * gB); } }
	v_add_f32_e32 v16, v16, v17
	s_nop 1
	v_mov_b32_dpp v17, v16 quad_perm:[2,3,0,1] row_mask:0xf bank_mask:0xf
	s_waitcnt lgkmcnt(0)
	v_add_f32_e32 v16, v16, v17
	s_nop 1
	v_mov_b32_dpp v17, v16 row_half_mirror row_mask:0xf bank_mask:0xf
	s_waitcnt lgkmcnt(0)
	v_add_f32_e32 v16, v16, v17
	s_nop 1
	v_mov_b32_dpp v17, v16 row_mirror row_mask:0xf bank_mask:0xf
	s_waitcnt lgkmcnt(0)
	v_add_f32_e32 v16, v16, v17
	v_mov_b32_e32 v17, v16
	s_nop 1
	v_permlane16_swap_b32_e32 v16, v17
	s_waitcnt lgkmcnt(0)
	v_add_f32_e32 v16, v16, v17
	v_mov_b32_e32 v17, v16
	s_nop 1
	v_permlane32_swap_b32_e32 v16, v17
	s_waitcnt lgkmcnt(0)
	v_add_f32_e32 v16, v16, v17
	v_fmamk_f32 v16, v16, 0x3c000000, v210
	v_cmp_gt_f32_e32 vcc, s16, v16
	v_mul_f32_e32 v17, 0x4f800000, v16
	s_nop 0
	v_cndmask_b32_e32 v16, v16, v17, vcc
	v_sqrt_f32_e32 v17, v16
	s_nop 0
	v_add_u32_e32 v18, -1, v17
	v_fma_f32 v19, -v18, v17, v16
	v_cmp_ge_f32_e64 s[2:3], 0, v19
	v_add_u32_e32 v19, 1, v17
	s_nop 0
	v_cndmask_b32_e64 v18, v17, v18, s[2:3]
	v_fma_f32 v17, -v19, v17, v16
	v_cmp_lt_f32_e64 s[2:3], 0, v17
	s_nop 1
	v_cndmask_b32_e64 v17, v18, v19, s[2:3]
	v_mul_f32_e32 v18, 0x37800000, v17
	v_cndmask_b32_e32 v17, v17, v18, vcc
	v_cmp_class_f32_e32 vcc, v16, v211
	s_nop 1
	v_cndmask_b32_e32 v16, v17, v16, vcc
	v_div_scale_f32 v17, s[0:1], v16, v16, 1.0
	v_rcp_f32_e32 v18, v17
	s_nop 0
	v_fma_f32 v19, -v17, v18, 1.0
	v_fmac_f32_e32 v18, v19, v18
	v_div_scale_f32 v19, vcc, 1.0, v16, 1.0
	v_mul_f32_e32 v88, v19, v18
	v_fma_f32 v89, -v17, v88, v19
	v_fmac_f32_e32 v88, v89, v18
	v_fma_f32 v17, -v17, v88, v19
	v_div_fmas_f32 v17, v17, v18, v88
	v_div_fixup_f32 v16, v17, v16, 1.0
	v_mul_f32_e32 v14, v14, v16
	v_mul_f32_e32 v15, v15, v16
	v_mul_f32_e32 v14, v96, v14
	v_mul_f32_e32 v15, v97, v15
	v_med3_f32 v14, v14, s33, v214
	v_med3_f32 v15, v15, s33, v214
	v_mov_b32_e32 v16, v2
	v_cvt_pk_fp8_f32 v16, v14, v15
	s_waitcnt vmcnt(25)
	v_lshlrev_b32_e32 v14, 16, v114
	s_waitcnt vmcnt(24)
	v_lshlrev_b32_e32 v15, 16, v115
	v_fma_f32 v14, -v95, v15, v14
	v_cvt_pk_fp8_f32 v16, 0, 0 op_sel:[0,0,1]
	v_and_b32_e32 v15, 0xffff0000, v114
	global_store_short v[12:13], v16, off offset:1536
	v_and_b32_e32 v16, 0xffff0000, v115
	v_fma_f32 v15, -v95, v16, v15
	v_mul_f32_e32 v16, v15, v15
	v_fmac_f32_e32 v16, v14, v14
	s_nop 1
	v_mov_b32_dpp v17, v16 quad_perm:[1,0,3,2] row_mask:0xf bank_mask:0xf
	s_waitcnt lgkmcnt(0)
	v_add_f32_e32 v16, v16, v17
	s_nop 1
	v_mov_b32_dpp v17, v16 quad_perm:[2,3,0,1] row_mask:0xf bank_mask:0xf
	s_waitcnt lgkmcnt(0)
	v_add_f32_e32 v16, v16, v17
	s_nop 1
	v_mov_b32_dpp v17, v16 row_half_mirror row_mask:0xf bank_mask:0xf
	s_waitcnt lgkmcnt(0)
	v_add_f32_e32 v16, v16, v17
	s_nop 1
	v_mov_b32_dpp v17, v16 row_mirror row_mask:0xf bank_mask:0xf
	s_waitcnt lgkmcnt(0)
	v_add_f32_e32 v16, v16, v17
	v_mov_b32_e32 v17, v16
	s_nop 1
	v_permlane16_swap_b32_e32 v16, v17
	s_waitcnt lgkmcnt(0)
	v_add_f32_e32 v16, v16, v17
	v_mov_b32_e32 v17, v16
	s_nop 1
	v_permlane32_swap_b32_e32 v16, v17
	s_waitcnt lgkmcnt(0)
	v_add_f32_e32 v16, v16, v17
	v_fmamk_f32 v16, v16, 0x3c000000, v210
	v_cmp_gt_f32_e32 vcc, s16, v16
	v_mul_f32_e32 v17, 0x4f800000, v16
	s_nop 0
	v_cndmask_b32_e32 v16, v16, v17, vcc
	v_sqrt_f32_e32 v17, v16
	s_nop 0
	v_add_u32_e32 v18, -1, v17
	v_fma_f32 v19, -v18, v17, v16
	v_cmp_ge_f32_e64 s[2:3], 0, v19
	v_add_u32_e32 v19, 1, v17
	s_nop 0
	v_cndmask_b32_e64 v18, v17, v18, s[2:3]
	v_fma_f32 v17, -v19, v17, v16
	v_cmp_lt_f32_e64 s[2:3], 0, v17
	s_nop 1
	v_cndmask_b32_e64 v17, v18, v19, s[2:3]
	v_mul_f32_e32 v18, 0x37800000, v17
	v_cndmask_b32_e32 v17, v17, v18, vcc
	v_cmp_class_f32_e32 vcc, v16, v211
	s_nop 1
	v_cndmask_b32_e32 v16, v17, v16, vcc
	v_div_scale_f32 v17, s[0:1], v16, v16, 1.0
	v_rcp_f32_e32 v18, v17
	s_nop 0
	v_fma_f32 v19, -v17, v18, 1.0
	v_fmac_f32_e32 v18, v19, v18
	v_div_scale_f32 v19, vcc, 1.0, v16, 1.0
	v_mul_f32_e32 v88, v19, v18
	v_fma_f32 v89, -v17, v88, v19
	v_fmac_f32_e32 v88, v89, v18
	v_fma_f32 v17, -v17, v88, v19
	v_div_fmas_f32 v17, v17, v18, v88
	v_div_fixup_f32 v16, v17, v16, 1.0
	v_mul_f32_e32 v14, v14, v16
	v_mul_f32_e32 v15, v15, v16
	v_mul_f32_e32 v14, v96, v14
	v_mul_f32_e32 v15, v97, v15
	v_med3_f32 v14, v14, s33, v214
	v_med3_f32 v15, v15, s33, v214
	v_mov_b32_e32 v16, v2
	v_cvt_pk_fp8_f32 v16, v14, v15
	s_waitcnt vmcnt(24)
	v_lshlrev_b32_e32 v14, 16, v112
	s_waitcnt vmcnt(23)
	v_lshlrev_b32_e32 v15, 16, v113
	v_fma_f32 v14, -v95, v15, v14
	v_cvt_pk_fp8_f32 v16, 0, 0 op_sel:[0,0,1]
	v_and_b32_e32 v15, 0xffff0000, v112
	global_store_short v[12:13], v16, off offset:1664
	v_and_b32_e32 v16, 0xffff0000, v113
	v_fma_f32 v15, -v95, v16, v15
	v_mul_f32_e32 v16, v15, v15
	v_fmac_f32_e32 v16, v14, v14
	s_nop 1
	v_mov_b32_dpp v17, v16 quad_perm:[1,0,3,2] row_mask:0xf bank_mask:0xf
	s_waitcnt lgkmcnt(0)
	v_add_f32_e32 v16, v16, v17
	s_nop 1
	v_mov_b32_dpp v17, v16 quad_perm:[2,3,0,1] row_mask:0xf bank_mask:0xf
	s_waitcnt lgkmcnt(0)
	v_add_f32_e32 v16, v16, v17
	s_nop 1
	v_mov_b32_dpp v17, v16 row_half_mirror row_mask:0xf bank_mask:0xf
	s_waitcnt lgkmcnt(0)
	v_add_f32_e32 v16, v16, v17
	s_nop 1
	v_mov_b32_dpp v17, v16 row_mirror row_mask:0xf bank_mask:0xf
	s_waitcnt lgkmcnt(0)
	v_add_f32_e32 v16, v16, v17
	v_mov_b32_e32 v17, v16
	s_nop 1
	v_permlane16_swap_b32_e32 v16, v17
	s_waitcnt lgkmcnt(0)
	v_add_f32_e32 v16, v16, v17
	v_mov_b32_e32 v17, v16
	s_nop 1
	v_permlane32_swap_b32_e32 v16, v17
	s_waitcnt lgkmcnt(0)
; template <bool F8> __device__ __forceinline__ void mix_phase(const Ctx& C, const bf16* YCONV, const bf16* YSWA, const bf16* ODIFF, const float* conv_g, const float* swa_g, const float* lq1, const float* lk1, const float* lq2, const float* lk2, ...
;     ...
;             { const v4u y = yc[q];
;               float f[8] = {bflo(y.x), bfhi(y.x), bflo(y.y), bfhi(y.y), bflo(y.z), bfhi(y.z), bflo(y.w), bfhi(y.w)}; float ss = 0.f;
; #pragma unroll
;               for (int i = 0; i < 8; ++i) ss += f[i] * f[i];
;               const float r = 1.0f / sqrtf(wave_sum(ss) * (1.0f / 512.0f) + RMS_EPS);
;               if constexpr (F8) { v2u o; o.x = pk4_fp8m(f[0] * r * cg0.x, f[1] * r * cg0.y, f[2] * r * cg0.z, f[3] * r * cg0.w); o.y = pk4_fp8m(f[4] * r * cg1.x, f[5] * r * cg1.y, f[6] * r * cg1.z, f[7] * r * cg1.w);
;                 *(GAS v2u*)(MIX8 + (size_t)m * DM + 8 * l) = o; }
;               else { v4u o; o.x = pk2(f[0] * r * cg0.x, f[1] * r * cg0.y); o.y = pk2(f[2] * r * cg0.z, f[3] * r * cg0.w); o.z = pk2(f[4] * r * cg1.x, f[5] * r * cg1.y); o.w = pk2(f[6] * r * cg1.z, f[7] * r * cg1.w);
;                 *(GAS v4u*)(MIX + (size_t)m * DM + 8 * l) = o; } }
;             { const v4u y = ys[q]; const v2u y2 = ys2[q];
;               float f[12] = {bflo(y.x), bfhi(y.x), bflo(y.y), bfhi(y.y), bflo(y.z), bfhi(y.z), bflo(y.w), bfhi(y.w), bflo(y2.x), bfhi(y2.x), bflo(y2.y), bfhi(y2.y)}; float ss = 0.f;
; #pragma unroll
;               for (int i = 0; i < 12; ++i) ss += f[i] * f[i];
;               const float r = 1.0f / sqrtf(wave_sum(ss) * (1.0f / 768.0f) + RMS_EPS);
;               if constexpr (F8) { v2u o; o.x = pk4_fp8m(f[0] * r * sg0.x, f[1] * r * sg0.y, f[2] * r * sg0.z, f[3] * r * sg0.w); o.y = pk4_fp8m(f[4] * r * sg1.x, f[5] * r * sg1.y, f[6] * r * sg1.z, f[7] * r * sg1.w);
;                 const unsigned o2 = pk4_fp8m(f[8] * r * sg2.x, f[9] * r * sg2.y, f[10] * r * sg2.z, f[11] * r * sg2.w);
;                 *(GAS v2u*)(MIX8 + (size_t)m * DM + 512 + 8 * l) = o; *(GAS unsigned*)(MIX8 + (size_t)m * DM + 1024 + 4 * l) = o2; }
;               else { v4u o; o.x = pk2(f[0] * r * sg0.x, f[1] * r * sg0.y); o.y = pk2(f[2] * r * sg0.z, f[3] * r * sg0.w); o.z = pk2(f[4] * r * sg1.x, f[5] * r * sg1.y); o.w = pk2(f[6] * r * sg1.z, f[7] * r * sg1.w);
;                 v2u o2; o2.x = pk2(f[8] * r * sg2.x, f[9] * r * sg2.y); o2.y = pk2(f[10] * r * sg2.z, f[11] * r * sg2.w);
	v_add_f32_e32 v16, v16, v17
	v_fmamk_f32 v16, v16, 0x3c000000, v210
	v_cmp_gt_f32_e32 vcc, s16, v16
	v_mul_f32_e32 v17, 0x4f800000, v16
	s_nop 0
	v_cndmask_b32_e32 v16, v16, v17, vcc
	v_sqrt_f32_e32 v17, v16
	s_nop 0
	v_add_u32_e32 v18, -1, v17
	v_fma_f32 v19, -v18, v17, v16
	v_cmp_ge_f32_e64 s[2:3], 0, v19
	v_add_u32_e32 v19, 1, v17
	s_nop 0
	v_cndmask_b32_e64 v18, v17, v18, s[2:3]
	v_fma_f32 v17, -v19, v17, v16
	v_cmp_lt_f32_e64 s[2:3], 0, v17
	s_nop 1
	v_cndmask_b32_e64 v17, v18, v19, s[2:3]
	v_mul_f32_e32 v18, 0x37800000, v17
	v_cndmask_b32_e32 v17, v17, v18, vcc
	v_cmp_class_f32_e32 vcc, v16, v211
	s_nop 1
	v_cndmask_b32_e32 v16, v17, v16, vcc
	v_div_scale_f32 v17, s[0:1], v16, v16, 1.0
	v_rcp_f32_e32 v18, v17
	s_nop 0
	v_fma_f32 v19, -v17, v18, 1.0
	v_fmac_f32_e32 v18, v19, v18
	v_div_scale_f32 v19, vcc, 1.0, v16, 1.0
	v_mul_f32_e32 v88, v19, v18
	v_fma_f32 v89, -v17, v88, v19
	v_fmac_f32_e32 v88, v89, v18
	v_fma_f32 v17, -v17, v88, v19
	v_div_fmas_f32 v17, v17, v18, v88
	v_div_fixup_f32 v16, v17, v16, 1.0
	v_mul_f32_e32 v14, v14, v16
	v_mul_f32_e32 v15, v15, v16
	v_mul_f32_e32 v14, v96, v14
	v_mul_f32_e32 v15, v97, v15
	v_med3_f32 v14, v14, s33, v214
	v_med3_f32 v15, v15, s33, v214
	v_mov_b32_e32 v16, v2
	v_cvt_pk_fp8_f32 v16, v14, v15
	s_waitcnt vmcnt(23)
	v_lshlrev_b32_e32 v14, 16, v110
	s_waitcnt vmcnt(22)
	v_lshlrev_b32_e32 v15, 16, v111
	v_fma_f32 v14, -v95, v15, v14
	v_cvt_pk_fp8_f32 v16, 0, 0 op_sel:[0,0,1]
	v_and_b32_e32 v15, 0xffff0000, v110
	global_store_short v[12:13], v16, off offset:1792
	v_and_b32_e32 v16, 0xffff0000, v111
	v_fma_f32 v15, -v95, v16, v15
	v_mul_f32_e32 v16, v15, v15
	v_fmac_f32_e32 v16, v14, v14
	s_nop 1
	v_mov_b32_dpp v17, v16 quad_perm:[1,0,3,2] row_mask:0xf bank_mask:0xf
	s_waitcnt lgkmcnt(0)
	v_add_f32_e32 v16, v16, v17
	s_nop 1
	v_mov_b32_dpp v17, v16 quad_perm:[2,3,0,1] row_mask:0xf bank_mask:0xf
	s_waitcnt lgkmcnt(0)
	v_add_f32_e32 v16, v16, v17
	s_nop 1
	v_mov_b32_dpp v17, v16 row_half_mirror row_mask:0xf bank_mask:0xf
	s_waitcnt lgkmcnt(0)
	v_add_f32_e32 v16, v16, v17
	s_nop 1
	v_mov_b32_dpp v17, v16 row_mirror row_mask:0xf bank_mask:0xf
	s_waitcnt lgkmcnt(0)
	v_add_f32_e32 v16, v16, v17
	v_mov_b32_e32 v17, v16
	s_nop 1
	v_permlane16_swap_b32_e32 v16, v17
	s_waitcnt lgkmcnt(0)
	v_add_f32_e32 v16, v16, v17
	v_mov_b32_e32 v17, v16
	s_nop 1
	v_permlane32_swap_b32_e32 v16, v17
	s_waitcnt lgkmcnt(0)
	v_add_f32_e32 v16, v16, v17
	v_fmamk_f32 v16, v16, 0x3c000000, v210
	v_cmp_gt_f32_e32 vcc, s16, v16
	v_mul_f32_e32 v17, 0x4f800000, v16
	s_nop 0
	v_cndmask_b32_e32 v16, v16, v17, vcc
	v_sqrt_f32_e32 v17, v16
	s_nop 0
	v_add_u32_e32 v18, -1, v17
	v_fma_f32 v19, -v18, v17, v16
	v_cmp_ge_f32_e64 s[2:3], 0, v19
	v_add_u32_e32 v19, 1, v17
	s_nop 0
	v_cndmask_b32_e64 v18, v17, v18, s[2:3]
	v_fma_f32 v17, -v19, v17, v16
	v_cmp_lt_f32_e64 s[2:3], 0, v17
	s_nop 1
	v_cndmask_b32_e64 v17, v18, v19, s[2:3]
	v_mul_f32_e32 v18, 0x37800000, v17
	v_cndmask_b32_e32 v17, v17, v18, vcc
	v_cmp_class_f32_e32 vcc, v16, v211
	s_nop 1
	v_cndmask_b32_e32 v16, v17, v16, vcc
	v_div_scale_f32 v17, s[0:1], v16, v16, 1.0
	v_rcp_f32_e32 v18, v17
	s_nop 0
	v_fma_f32 v19, -v17, v18, 1.0
	v_fmac_f32_e32 v18, v19, v18
	v_div_scale_f32 v19, vcc, 1.0, v16, 1.0
	v_mul_f32_e32 v88, v19, v18
	v_fma_f32 v89, -v17, v88, v19
	v_fmac_f32_e32 v88, v89, v18
	v_fma_f32 v17, -v17, v88, v19
	v_div_fmas_f32 v17, v17, v18, v88
	v_div_fixup_f32 v16, v17, v16, 1.0
	v_mul_f32_e32 v14, v14, v16
	v_mul_f32_e32 v15, v15, v16
	v_mul_f32_e32 v14, v96, v14
	v_mul_f32_e32 v15, v97, v15
	v_med3_f32 v14, v14, s33, v214
	v_med3_f32 v15, v15, s33, v214
	v_mov_b32_e32 v16, v2
	v_cvt_pk_fp8_f32 v16, v14, v15
	s_waitcnt vmcnt(22)
	v_lshlrev_b32_e32 v14, 16, v10
	v_and_b32_e32 v10, 0xffff0000, v10
	v_lshlrev_b32_e32 v15, 16, v11
	v_cvt_pk_fp8_f32 v16, 0, 0 op_sel:[0,0,1]
	v_and_b32_e32 v11, 0xffff0000, v11
	global_store_short v[12:13], v16, off offset:1920
	v_lshlrev_b32_e32 v12, 16, v8
	v_and_b32_e32 v8, 0xffff0000, v8
	v_mul_f32_e32 v16, v8, v8
	v_lshlrev_b32_e32 v13, 16, v9
	v_fmac_f32_e32 v16, v12, v12
	v_and_b32_e32 v9, 0xffff0000, v9
	v_fmac_f32_e32 v16, v13, v13
	v_fmac_f32_e32 v16, v9, v9
	v_fmac_f32_e32 v16, v14, v14
	v_fmac_f32_e32 v16, v10, v10
	v_fmac_f32_e32 v16, v15, v15
	v_fmac_f32_e32 v16, v11, v11
	s_nop 1
	v_mov_b32_dpp v17, v16 quad_perm:[1,0,3,2] row_mask:0xf bank_mask:0xf
	s_waitcnt lgkmcnt(0)
	v_add_f32_e32 v16, v16, v17
	s_nop 1
	v_mov_b32_dpp v17, v16 quad_perm:[2,3,0,1] row_mask:0xf bank_mask:0xf
	s_waitcnt lgkmcnt(0)
	v_add_f32_e32 v16, v16, v17
	s_nop 1
	v_mov_b32_dpp v17, v16 row_half_mirror row_mask:0xf bank_mask:0xf
	s_waitcnt lgkmcnt(0)
	v_add_f32_e32 v16, v16, v17
	s_nop 1
	v_mov_b32_dpp v17, v16 row_mirror row_mask:0xf bank_mask:0xf
	s_waitcnt lgkmcnt(0)
	v_add_f32_e32 v16, v16, v17
	v_mov_b32_e32 v17, v16
	s_nop 1
	v_permlane16_swap_b32_e32 v16, v17
	s_waitcnt lgkmcnt(0)
	v_add_f32_e32 v16, v16, v17
	v_mov_b32_e32 v17, v16
	s_nop 1
	v_permlane32_swap_b32_e32 v16, v17
	s_waitcnt lgkmcnt(0)
; #define GAS __attribute__((address_space(1)))
; __device__ __forceinline__ unsigned pk2(float lo, float hi) { f32x2_m v = {lo, hi}; bf16x2_m b = __builtin_convertvector(v, bf16x2_m); return __builtin_bit_cast(unsigned, b); }
; __device__ __forceinline__ float bflo(unsigned w) { return __uint_as_float(w << 16); }
; template <bool F8> __device__ __forceinline__ void mix_phase(const Ctx& C, const bf16* YCONV, const bf16* YSWA, const bf16* ODIFF, const float* conv_g, const float* swa_g, const float* lq1, const float* lk1, const float* lq2, const float* lk2, ...
;     ...
;             { const v4u y = yc[q];
;               float f[8] = {bflo(y.x), bfhi(y.x), bflo(y.y), bfhi(y.y), bflo(y.z), bfhi(y.z), bflo(y.w), bfhi(y.w)}; float ss = 0.f;
; #pragma unroll
;               for (int i = 0; i < 8; ++i) ss += f[i] * f[i];
;               const float r = 1.0f / sqrtf(wave_sum(ss) * (1.0f / 512.0f) + RMS_EPS);
;               if constexpr (F8) { v2u o; o.x = pk4_fp8m(f[0] * r * cg0.x, f[1] * r * cg0.y, f[2] * r * cg0.z, f[3] * r * cg0.w); o.y = pk4_fp8m(f[4] * r * cg1.x, f[5] * r * cg1.y, f[6] * r * cg1.z, f[7] * r * cg1.w);
;                 *(GAS v2u*)(MIX8 + (size_t)m * DM + 8 * l) = o; }
;               else { v4u o; o.x = pk2(f[0] * r * cg0.x, f[1] * r * cg0.y); o.y = pk2(f[2] * r * cg0.z, f[3] * r * cg0.w); o.z = pk2(f[4] * r * cg1.x, f[5] * r * cg1.y); o.w = pk2(f[6] * r * cg1.z, f[7] * r * cg1.w);
;                 *(GAS v4u*)(MIX + (size_t)m * DM + 8 * l) = o; } }
;             { const v4u y = ys[q]; const v2u y2 = ys2[q];
;               float f[12] = {bflo(y.x), bfhi(y.x), bflo(y.y), bfhi(y.y), bflo(y.z), bfhi(y.z), bflo(y.w), bfhi(y.w), bflo(y2.x), bfhi(y2.x), bflo(y2.y), bfhi(y2.y)}; float ss = 0.f;
; #pragma unroll
;               for (int i = 0; i < 12; ++i) ss += f[i] * f[i];
;               const float r = 1.0f / sqrtf(wave_sum(ss) * (1.0f / 768.0f) + RMS_EPS);
;               if constexpr (F8) { v2u o; o.x = pk4_fp8m(f[0] * r * sg0.x, f[1] * r * sg0.y, f[2] * r * sg0.z, f[3] * r * sg0.w); o.y = pk4_fp8m(f[4] * r * sg1.x, f[5] * r * sg1.y, f[6] * r * sg1.z, f[7] * r * sg1.w);
;                 const unsigned o2 = pk4_fp8m(f[8] * r * sg2.x, f[9] * r * sg2.y, f[10] * r * sg2.z, f[11] * r * sg2.w);
;                 *(GAS v2u*)(MIX8 + (size_t)m * DM + 512 + 8 * l) = o; *(GAS unsigned*)(MIX8 + (size_t)m * DM + 1024 + 4 * l) = o2; }
	v_add_f32_e32 v16, v16, v17
	v_fmamk_f32 v16, v16, 0x3b000000, v212
	v_cmp_gt_f32_e32 vcc, s16, v16
	v_mul_f32_e32 v17, 0x4f800000, v16
	s_nop 0
	v_cndmask_b32_e32 v16, v16, v17, vcc
	v_sqrt_f32_e32 v17, v16
	s_nop 0
	v_add_u32_e32 v18, -1, v17
	v_fma_f32 v19, -v18, v17, v16
	v_cmp_ge_f32_e64 s[2:3], 0, v19
	v_add_u32_e32 v19, 1, v17
	s_nop 0
	v_cndmask_b32_e64 v18, v17, v18, s[2:3]
	v_fma_f32 v17, -v19, v17, v16
	v_cmp_lt_f32_e64 s[2:3], 0, v17
	s_nop 1
	v_cndmask_b32_e64 v17, v18, v19, s[2:3]
	v_mul_f32_e32 v18, 0x37800000, v17
	v_cndmask_b32_e32 v17, v17, v18, vcc
	v_cmp_class_f32_e32 vcc, v16, v211
	s_nop 1
	v_cndmask_b32_e32 v16, v17, v16, vcc
	v_div_scale_f32 v17, s[0:1], v16, v16, 1.0
	v_rcp_f32_e32 v18, v17
	s_nop 0
	v_fma_f32 v19, -v17, v18, 1.0
	v_fmac_f32_e32 v18, v19, v18
	v_div_scale_f32 v19, vcc, 1.0, v16, 1.0
	v_mul_f32_e32 v88, v19, v18
	v_fma_f32 v89, -v17, v88, v19
	v_fmac_f32_e32 v88, v89, v18
	v_fma_f32 v17, -v17, v88, v19
	v_div_fmas_f32 v17, v17, v18, v88
	v_div_fixup_f32 v16, v17, v16, 1.0
	v_mul_f32_e32 v12, v16, v12
	v_mul_f32_e32 v8, v16, v8
	v_mul_f32_e32 v12, v42, v12
	v_mul_f32_e32 v8, v43, v8
	v_med3_f32 v12, v12, s33, v214
	v_med3_f32 v17, v8, s33, v214
	v_mov_b32_e32 v8, v2
	v_cvt_pk_fp8_f32 v8, v12, v17
	v_mul_f32_e32 v13, v16, v13
	v_mul_f32_e32 v9, v16, v9
	v_mul_f32_e32 v13, v40, v13
	v_mul_f32_e32 v9, v41, v9
	v_med3_f32 v13, v13, s33, v214
	v_med3_f32 v9, v9, s33, v214
	v_cvt_pk_fp8_f32 v8, v13, v9 op_sel:[0,0,1]
	v_mul_f32_e32 v9, v16, v14
	v_mul_f32_e32 v10, v16, v10
	v_mul_f32_e32 v9, v38, v9
	v_mul_f32_e32 v10, v39, v10
	v_med3_f32 v13, v9, s33, v214
	v_med3_f32 v10, v10, s33, v214
	v_mov_b32_e32 v9, v2
	v_cvt_pk_fp8_f32 v9, v13, v10
	v_mul_f32_e32 v12, v16, v15
	v_mul_f32_e32 v11, v16, v11
	v_mul_f32_e32 v12, v36, v12
	v_mul_f32_e32 v11, v37, v11
	v_med3_f32 v12, v12, s33, v214
	v_med3_f32 v11, v11, s33, v214
	v_cvt_pk_fp8_f32 v9, v12, v11 op_sel:[0,0,1]
	v_lshl_add_u64 v[10:11], s[12:13], 0, v[20:21]
	v_add_co_u32_e32 v10, vcc, s18, v10
	s_waitcnt vmcnt(21)
	v_lshlrev_b32_e32 v12, 16, v6
	v_addc_co_u32_e32 v11, vcc, 0, v11, vcc
	global_store_dwordx2 v[10:11], v[8:9], off
	v_lshlrev_b32_e32 v8, 16, v4
	v_and_b32_e32 v4, 0xffff0000, v4
	v_mul_f32_e32 v18, v4, v4
	v_lshlrev_b32_e32 v9, 16, v5
	v_fmac_f32_e32 v18, v8, v8
	v_and_b32_e32 v5, 0xffff0000, v5
	v_fmac_f32_e32 v18, v9, v9
	v_fmac_f32_e32 v18, v5, v5
	v_and_b32_e32 v6, 0xffff0000, v6
	v_fmac_f32_e32 v18, v12, v12
	v_lshlrev_b32_e32 v13, 16, v7
	v_fmac_f32_e32 v18, v6, v6
	v_and_b32_e32 v7, 0xffff0000, v7
	v_fmac_f32_e32 v18, v13, v13
	v_lshlrev_b32_e32 v14, 16, v86
	v_fmac_f32_e32 v18, v7, v7
	v_and_b32_e32 v15, 0xffff0000, v86
	v_fmac_f32_e32 v18, v14, v14
	v_lshlrev_b32_e32 v16, 16, v87
	v_fmac_f32_e32 v18, v15, v15
	v_and_b32_e32 v17, 0xffff0000, v87
	v_fmac_f32_e32 v18, v16, v16
	v_fmac_f32_e32 v18, v17, v17
	s_nop 1
	v_mov_b32_dpp v19, v18 quad_perm:[1,0,3,2] row_mask:0xf bank_mask:0xf
	v_lshl_add_u64 v[20:21], v[20:21], 0, s[20:21]
	s_waitcnt lgkmcnt(0)
	v_add_f32_e32 v18, v18, v19
	s_nop 1
	v_mov_b32_dpp v19, v18 quad_perm:[2,3,0,1] row_mask:0xf bank_mask:0xf
	s_waitcnt lgkmcnt(0)
	v_add_f32_e32 v18, v18, v19
	s_nop 1
	v_mov_b32_dpp v19, v18 row_half_mirror row_mask:0xf bank_mask:0xf
	s_waitcnt lgkmcnt(0)
	v_add_f32_e32 v18, v18, v19
	s_nop 1
	v_mov_b32_dpp v19, v18 row_mirror row_mask:0xf bank_mask:0xf
	s_waitcnt lgkmcnt(0)
	v_add_f32_e32 v18, v18, v19
	v_mov_b32_e32 v19, v18
	s_nop 1
	v_permlane16_swap_b32_e32 v18, v19
	s_waitcnt lgkmcnt(0)
	v_add_f32_e32 v18, v18, v19
	v_mov_b32_e32 v19, v18
	s_nop 1
	v_permlane32_swap_b32_e32 v18, v19
	s_waitcnt lgkmcnt(0)
	v_add_f32_e32 v18, v18, v19
	v_fmamk_f32 v18, v18, 0x3aaaaaab, v212
	v_cmp_gt_f32_e32 vcc, s16, v18
	v_mul_f32_e32 v19, 0x4f800000, v18
	s_nop 0
	v_cndmask_b32_e32 v18, v18, v19, vcc
	v_sqrt_f32_e32 v19, v18
	s_nop 0
	v_add_u32_e32 v86, -1, v19
	v_fma_f32 v87, -v86, v19, v18
	v_cmp_ge_f32_e64 s[2:3], 0, v87
	v_add_u32_e32 v87, 1, v19
	s_nop 0
	v_cndmask_b32_e64 v86, v19, v86, s[2:3]
	v_fma_f32 v19, -v87, v19, v18
	v_cmp_lt_f32_e64 s[2:3], 0, v19
	s_nop 1
	v_cndmask_b32_e64 v19, v86, v87, s[2:3]
	v_mul_f32_e32 v86, 0x37800000, v19
	v_cndmask_b32_e32 v19, v19, v86, vcc
	v_cmp_class_f32_e32 vcc, v18, v211
	s_nop 1
	v_cndmask_b32_e32 v18, v19, v18, vcc
	v_div_scale_f32 v19, s[0:1], v18, v18, 1.0
	v_rcp_f32_e32 v86, v19
	s_nop 0
	v_fma_f32 v87, -v19, v86, 1.0
	v_fmac_f32_e32 v86, v87, v86
	v_div_scale_f32 v87, vcc, 1.0, v18, 1.0
	v_mul_f32_e32 v88, v87, v86
	v_fma_f32 v89, -v19, v88, v87
	v_fmac_f32_e32 v88, v89, v86
	v_fma_f32 v19, -v19, v88, v87
	v_div_fmas_f32 v19, v19, v86, v88
	v_div_fixup_f32 v18, v19, v18, 1.0
	v_mul_f32_e32 v8, v18, v8
	v_mul_f32_e32 v4, v18, v4
	v_mul_f32_e32 v8, v54, v8
	v_mul_f32_e32 v4, v55, v4
	v_med3_f32 v8, v8, s33, v214
	v_med3_f32 v19, v4, s33, v214
	v_mov_b32_e32 v4, v2
	v_cvt_pk_fp8_f32 v4, v8, v19
	v_mul_f32_e32 v9, v18, v9
	v_mul_f32_e32 v5, v18, v5
	v_mul_f32_e32 v9, v52, v9
	v_mul_f32_e32 v5, v53, v5
	v_med3_f32 v9, v9, s33, v214
	v_med3_f32 v5, v5, s33, v214
	v_cvt_pk_fp8_f32 v4, v9, v5 op_sel:[0,0,1]
	v_mul_f32_e32 v5, v18, v12
	v_mul_f32_e32 v6, v18, v6
	v_mul_f32_e32 v5, v50, v5
	v_mul_f32_e32 v6, v51, v6
	v_med3_f32 v9, v5, s33, v214
	v_med3_f32 v6, v6, s33, v214
	v_mov_b32_e32 v5, v2
	v_cvt_pk_fp8_f32 v5, v9, v6
	v_mul_f32_e32 v8, v18, v13
	v_mul_f32_e32 v7, v18, v7
	v_mul_f32_e32 v8, v48, v8
	v_mul_f32_e32 v7, v49, v7
	v_med3_f32 v8, v8, s33, v214
	v_med3_f32 v7, v7, s33, v214
	v_cvt_pk_fp8_f32 v5, v8, v7 op_sel:[0,0,1]
	v_mul_f32_e32 v6, v18, v14
	v_mul_f32_e32 v7, v18, v15
	v_mul_f32_e32 v6, v46, v6
	v_mul_f32_e32 v7, v47, v7
	v_med3_f32 v6, v6, s33, v214
	v_med3_f32 v7, v7, s33, v214
	v_mov_b32_e32 v12, v2
	v_cvt_pk_fp8_f32 v12, v6, v7
	v_mul_f32_e32 v8, v18, v16
	v_mul_f32_e32 v9, v18, v17
	v_mul_f32_e32 v8, v44, v8
	v_mul_f32_e32 v9, v45, v9
	v_med3_f32 v8, v8, s33, v214
	v_med3_f32 v9, v9, s33, v214
	s_waitcnt vmcnt(21)
; #define GAS __attribute__((address_space(1)))
; __device__ __forceinline__ unsigned pk2(float lo, float hi) { f32x2_m v = {lo, hi}; bf16x2_m b = __builtin_convertvector(v, bf16x2_m); return __builtin_bit_cast(unsigned, b); }
; __device__ __forceinline__ float bflo(unsigned w) { return __uint_as_float(w << 16); }
; __device__ __forceinline__ float bfhi(unsigned w) { return __uint_as_float(w & 0xffff0000u); }
; template <bool F8> __device__ __forceinline__ void mix_phase(const Ctx& C, const bf16* YCONV, const bf16* YSWA, const bf16* ODIFF, const float* conv_g, const float* swa_g, const float* lq1, const float* lk1, const float* lq2, const float* lk2, ...
;     ...
;               if constexpr (F8) { v2u o; o.x = pk4_fp8m(f[0] * r * sg0.x, f[1] * r * sg0.y, f[2] * r * sg0.z, f[3] * r * sg0.w); o.y = pk4_fp8m(f[4] * r * sg1.x, f[5] * r * sg1.y, f[6] * r * sg1.z, f[7] * r * sg1.w);
;                 const unsigned o2 = pk4_fp8m(f[8] * r * sg2.x, f[9] * r * sg2.y, f[10] * r * sg2.z, f[11] * r * sg2.w);
;                 *(GAS v2u*)(MIX8 + (size_t)m * DM + 512 + 8 * l) = o; *(GAS unsigned*)(MIX8 + (size_t)m * DM + 1024 + 4 * l) = o2; }
;               else { v4u o; o.x = pk2(f[0] * r * sg0.x, f[1] * r * sg0.y); o.y = pk2(f[2] * r * sg0.z, f[3] * r * sg0.w); o.z = pk2(f[4] * r * sg1.x, f[5] * r * sg1.y); o.w = pk2(f[6] * r * sg1.z, f[7] * r * sg1.w);
;                 v2u o2; o2.x = pk2(f[8] * r * sg2.x, f[9] * r * sg2.y); o2.y = pk2(f[10] * r * sg2.z, f[11] * r * sg2.w);
;                 *(GAS v4u*)(MIX + (size_t)m * DM + 512 + 8 * l) = o; *(GAS v2u*)(MIX + (size_t)m * DM + 1024 + 4 * l) = o2; } }
; #pragma unroll
;             for (int h = 0; h < 6; ++h) { const unsigned a = oa[q][h], bq = ob[q][h];
;                 const float v0 = bflo(a) - lam * bflo(bq), v1 = bfhi(a) - lam * bfhi(bq);
;                 const float r = 1.0f / sqrtf(wave_sum(v0 * v0 + v1 * v1) * (1.0f / 128.0f) + LN_EPS);
;                 if constexpr (F8) *(GAS unsigned short*)(MIX8 + (size_t)m * DM + 1280 + 128 * h + 2 * l) = (unsigned short)pk4_fp8m(v0 * r * gA, v1 * r * gB, 0.f, 0.f);
;                 else *(GAS unsigned*)(MIX + (size_t)m * DM + 1280 + 128 * h + 2 * l) = pk2(v0 * r * gA, v1 * r * gB); } }
	v_lshlrev_b32_e32 v6, 16, v108
	s_waitcnt vmcnt(20)
	v_lshlrev_b32_e32 v7, 16, v109
	v_cvt_pk_fp8_f32 v12, v8, v9 op_sel:[0,0,1]
	v_fma_f32 v6, -v95, v7, v6
	v_and_b32_e32 v7, 0xffff0000, v108
	v_and_b32_e32 v8, 0xffff0000, v109
	v_fma_f32 v7, -v95, v8, v7
	v_mul_f32_e32 v8, v7, v7
	v_fmac_f32_e32 v8, v6, v6
	s_nop 1
	v_mov_b32_dpp v9, v8 quad_perm:[1,0,3,2] row_mask:0xf bank_mask:0xf
	global_store_dwordx2 v[10:11], v[4:5], off offset:512
	v_lshl_add_u64 v[4:5], s[12:13], 0, v[22:23]
	global_store_dword v[4:5], v12, off
	v_lshl_add_u64 v[4:5], s[12:13], 0, v[0:1]
	s_waitcnt lgkmcnt(0)
	v_add_f32_e32 v8, v8, v9
	s_nop 1
	v_mov_b32_dpp v9, v8 quad_perm:[2,3,0,1] row_mask:0xf bank_mask:0xf
	v_lshl_add_u64 v[0:1], v[0:1], 0, s[20:21]
	v_lshl_add_u64 v[22:23], v[22:23], 0, s[20:21]
	s_waitcnt lgkmcnt(0)
	v_add_f32_e32 v8, v8, v9
	s_nop 1
	v_mov_b32_dpp v9, v8 row_half_mirror row_mask:0xf bank_mask:0xf
	s_waitcnt lgkmcnt(0)
	v_add_f32_e32 v8, v8, v9
	s_nop 1
	v_mov_b32_dpp v9, v8 row_mirror row_mask:0xf bank_mask:0xf
	s_waitcnt lgkmcnt(0)
	v_add_f32_e32 v8, v8, v9
	v_mov_b32_e32 v9, v8
	s_nop 1
	v_permlane16_swap_b32_e32 v8, v9
	s_waitcnt lgkmcnt(0)
	v_add_f32_e32 v8, v8, v9
	v_mov_b32_e32 v9, v8
	s_nop 1
	v_permlane32_swap_b32_e32 v8, v9
	s_waitcnt lgkmcnt(0)
	v_add_f32_e32 v8, v8, v9
	v_fmamk_f32 v8, v8, 0x3c000000, v210
	v_cmp_gt_f32_e32 vcc, s16, v8
	v_mul_f32_e32 v9, 0x4f800000, v8
	s_nop 0
	v_cndmask_b32_e32 v8, v8, v9, vcc
	v_sqrt_f32_e32 v9, v8
	s_nop 0
	v_add_u32_e32 v10, -1, v9
	v_fma_f32 v11, -v10, v9, v8
	v_cmp_ge_f32_e64 s[2:3], 0, v11
	v_add_u32_e32 v11, 1, v9
	s_nop 0
	v_cndmask_b32_e64 v10, v9, v10, s[2:3]
	v_fma_f32 v9, -v11, v9, v8
	v_cmp_lt_f32_e64 s[2:3], 0, v9
	s_nop 1
	v_cndmask_b32_e64 v9, v10, v11, s[2:3]
	v_mul_f32_e32 v10, 0x37800000, v9
	v_cndmask_b32_e32 v9, v9, v10, vcc
	v_cmp_class_f32_e32 vcc, v8, v211
	s_nop 1
	v_cndmask_b32_e32 v8, v9, v8, vcc
	v_div_scale_f32 v9, s[0:1], v8, v8, 1.0
	v_rcp_f32_e32 v10, v9
	s_nop 0
	v_fma_f32 v11, -v9, v10, 1.0
	v_fmac_f32_e32 v10, v11, v10
	v_div_scale_f32 v11, vcc, 1.0, v8, 1.0
	v_mul_f32_e32 v12, v11, v10
	v_fma_f32 v13, -v9, v12, v11
	v_fmac_f32_e32 v12, v13, v10
	v_fma_f32 v9, -v9, v12, v11
	v_div_fmas_f32 v9, v9, v10, v12
	v_div_fixup_f32 v8, v9, v8, 1.0
	v_mul_f32_e32 v6, v6, v8
	v_mul_f32_e32 v7, v7, v8
	v_mul_f32_e32 v6, v96, v6
	v_mul_f32_e32 v7, v97, v7
	v_med3_f32 v6, v6, s33, v214
	v_med3_f32 v7, v7, s33, v214
	v_mov_b32_e32 v8, v2
	v_cvt_pk_fp8_f32 v8, v6, v7
	v_add_co_u32_e32 v4, vcc, s18, v4
	s_waitcnt vmcnt(21)
	v_lshlrev_b32_e32 v6, 16, v106
	v_cvt_pk_fp8_f32 v8, 0, 0 op_sel:[0,0,1]
	v_addc_co_u32_e32 v5, vcc, 0, v5, vcc
	s_waitcnt vmcnt(20)
	v_lshlrev_b32_e32 v7, 16, v107
	global_store_short v[4:5], v8, off offset:1280
	v_fma_f32 v6, -v95, v7, v6
	v_and_b32_e32 v7, 0xffff0000, v106
	v_and_b32_e32 v8, 0xffff0000, v107
	v_fma_f32 v7, -v95, v8, v7
	v_mul_f32_e32 v8, v7, v7
	v_fmac_f32_e32 v8, v6, v6
	s_nop 1
	v_mov_b32_dpp v9, v8 quad_perm:[1,0,3,2] row_mask:0xf bank_mask:0xf
	s_waitcnt lgkmcnt(0)
	v_add_f32_e32 v8, v8, v9
	s_nop 1
	v_mov_b32_dpp v9, v8 quad_perm:[2,3,0,1] row_mask:0xf bank_mask:0xf
	s_waitcnt lgkmcnt(0)
	v_add_f32_e32 v8, v8, v9
	s_nop 1
	v_mov_b32_dpp v9, v8 row_half_mirror row_mask:0xf bank_mask:0xf
	s_waitcnt lgkmcnt(0)
	v_add_f32_e32 v8, v8, v9
	s_nop 1
	v_mov_b32_dpp v9, v8 row_mirror row_mask:0xf bank_mask:0xf
	s_waitcnt lgkmcnt(0)
	v_add_f32_e32 v8, v8, v9
	v_mov_b32_e32 v9, v8
	s_nop 1
	v_permlane16_swap_b32_e32 v8, v9
	s_waitcnt lgkmcnt(0)
	v_add_f32_e32 v8, v8, v9
	v_mov_b32_e32 v9, v8
	s_nop 1
	v_permlane32_swap_b32_e32 v8, v9
	s_waitcnt lgkmcnt(0)
	v_add_f32_e32 v8, v8, v9
	v_fmamk_f32 v8, v8, 0x3c000000, v210
	v_cmp_gt_f32_e32 vcc, s16, v8
	v_mul_f32_e32 v9, 0x4f800000, v8
	s_nop 0
	v_cndmask_b32_e32 v8, v8, v9, vcc
	v_sqrt_f32_e32 v9, v8
	s_nop 0
	v_add_u32_e32 v10, -1, v9
	v_fma_f32 v11, -v10, v9, v8
	v_cmp_ge_f32_e64 s[2:3], 0, v11
	v_add_u32_e32 v11, 1, v9
	s_nop 0
	v_cndmask_b32_e64 v10, v9, v10, s[2:3]
	v_fma_f32 v9, -v11, v9, v8
	v_cmp_lt_f32_e64 s[2:3], 0, v9
	s_nop 1
	v_cndmask_b32_e64 v9, v10, v11, s[2:3]
	v_mul_f32_e32 v10, 0x37800000, v9
	v_cndmask_b32_e32 v9, v9, v10, vcc
	v_cmp_class_f32_e32 vcc, v8, v211
	s_nop 1
	v_cndmask_b32_e32 v8, v9, v8, vcc
	v_div_scale_f32 v9, s[0:1], v8, v8, 1.0
	v_rcp_f32_e32 v10, v9
	s_nop 0
	v_fma_f32 v11, -v9, v10, 1.0
	v_fmac_f32_e32 v10, v11, v10
	v_div_scale_f32 v11, vcc, 1.0, v8, 1.0
	v_mul_f32_e32 v12, v11, v10
	v_fma_f32 v13, -v9, v12, v11
	v_fmac_f32_e32 v12, v13, v10
	v_fma_f32 v9, -v9, v12, v11
	v_div_fmas_f32 v9, v9, v10, v12
	v_div_fixup_f32 v8, v9, v8, 1.0
	v_mul_f32_e32 v6, v6, v8
	v_mul_f32_e32 v7, v7, v8
	v_mul_f32_e32 v6, v96, v6
	v_mul_f32_e32 v7, v97, v7
	v_med3_f32 v6, v6, s33, v214
	v_med3_f32 v7, v7, s33, v214
	v_mov_b32_e32 v8, v2
	v_cvt_pk_fp8_f32 v8, v6, v7
	s_waitcnt vmcnt(20)
	v_lshlrev_b32_e32 v6, 16, v104
	s_waitcnt vmcnt(19)
	v_lshlrev_b32_e32 v7, 16, v105
	v_fma_f32 v6, -v95, v7, v6
	v_cvt_pk_fp8_f32 v8, 0, 0 op_sel:[0,0,1]
	v_and_b32_e32 v7, 0xffff0000, v104
	global_store_short v[4:5], v8, off offset:1408
	v_and_b32_e32 v8, 0xffff0000, v105
	v_fma_f32 v7, -v95, v8, v7
	v_mul_f32_e32 v8, v7, v7
	v_fmac_f32_e32 v8, v6, v6
	s_nop 1
	v_mov_b32_dpp v9, v8 quad_perm:[1,0,3,2] row_mask:0xf bank_mask:0xf
	s_waitcnt lgkmcnt(0)
	v_add_f32_e32 v8, v8, v9
	s_nop 1
	v_mov_b32_dpp v9, v8 quad_perm:[2,3,0,1] row_mask:0xf bank_mask:0xf
	s_waitcnt lgkmcnt(0)
	v_add_f32_e32 v8, v8, v9
	s_nop 1
	v_mov_b32_dpp v9, v8 row_half_mirror row_mask:0xf bank_mask:0xf
	s_waitcnt lgkmcnt(0)
	v_add_f32_e32 v8, v8, v9
	s_nop 1
	v_mov_b32_dpp v9, v8 row_mirror row_mask:0xf bank_mask:0xf
	s_waitcnt lgkmcnt(0)
; #define GAS __attribute__((address_space(1)))
; __device__ __forceinline__ unsigned pk2(float lo, float hi) { f32x2_m v = {lo, hi}; bf16x2_m b = __builtin_convertvector(v, bf16x2_m); return __builtin_bit_cast(unsigned, b); }
; __device__ __forceinline__ float bflo(unsigned w) { return __uint_as_float(w << 16); }
; __device__ __forceinline__ float bfhi(unsigned w) { return __uint_as_float(w & 0xffff0000u); }
; template <bool F8> __device__ __forceinline__ void mix_phase(const Ctx& C, const bf16* YCONV, const bf16* YSWA, const bf16* ODIFF, const float* conv_g, const float* swa_g, const float* lq1, const float* lk1, const float* lq2, const float* lk2, ...
;     ...
; #pragma unroll
;             for (int h = 0; h < 6; ++h) { const unsigned a = oa[q][h], bq = ob[q][h];
;                 const float v0 = bflo(a) - lam * bflo(bq), v1 = bfhi(a) - lam * bfhi(bq);
;                 const float r = 1.0f / sqrtf(wave_sum(v0 * v0 + v1 * v1) * (1.0f / 128.0f) + LN_EPS);
;                 if constexpr (F8) *(GAS unsigned short*)(MIX8 + (size_t)m * DM + 1280 + 128 * h + 2 * l) = (unsigned short)pk4_fp8m(v0 * r * gA, v1 * r * gB, 0.f, 0.f);
;                 else *(GAS unsigned*)(MIX + (size_t)m * DM + 1280 + 128 * h + 2 * l) = pk2(v0 * r * gA, v1 * r * gB); } }
	v_add_f32_e32 v8, v8, v9
	v_mov_b32_e32 v9, v8
	s_nop 1
	v_permlane16_swap_b32_e32 v8, v9
	s_waitcnt lgkmcnt(0)
	v_add_f32_e32 v8, v8, v9
	v_mov_b32_e32 v9, v8
	s_nop 1
	v_permlane32_swap_b32_e32 v8, v9
	s_waitcnt lgkmcnt(0)
	v_add_f32_e32 v8, v8, v9
	v_fmamk_f32 v8, v8, 0x3c000000, v210
	v_cmp_gt_f32_e32 vcc, s16, v8
	v_mul_f32_e32 v9, 0x4f800000, v8
	s_nop 0
	v_cndmask_b32_e32 v8, v8, v9, vcc
	v_sqrt_f32_e32 v9, v8
	s_nop 0
	v_add_u32_e32 v10, -1, v9
	v_fma_f32 v11, -v10, v9, v8
	v_cmp_ge_f32_e64 s[2:3], 0, v11
	v_add_u32_e32 v11, 1, v9
	s_nop 0
	v_cndmask_b32_e64 v10, v9, v10, s[2:3]
	v_fma_f32 v9, -v11, v9, v8
	v_cmp_lt_f32_e64 s[2:3], 0, v9
	s_nop 1
	v_cndmask_b32_e64 v9, v10, v11, s[2:3]
	v_mul_f32_e32 v10, 0x37800000, v9
	v_cndmask_b32_e32 v9, v9, v10, vcc
	v_cmp_class_f32_e32 vcc, v8, v211
	s_nop 1
	v_cndmask_b32_e32 v8, v9, v8, vcc
	v_div_scale_f32 v9, s[0:1], v8, v8, 1.0
	v_rcp_f32_e32 v10, v9
	s_nop 0
	v_fma_f32 v11, -v9, v10, 1.0
	v_fmac_f32_e32 v10, v11, v10
	v_div_scale_f32 v11, vcc, 1.0, v8, 1.0
	v_mul_f32_e32 v12, v11, v10
	v_fma_f32 v13, -v9, v12, v11
	v_fmac_f32_e32 v12, v13, v10
	v_fma_f32 v9, -v9, v12, v11
	v_div_fmas_f32 v9, v9, v10, v12
	v_div_fixup_f32 v8, v9, v8, 1.0
	v_mul_f32_e32 v6, v6, v8
	v_mul_f32_e32 v7, v7, v8
	v_mul_f32_e32 v6, v96, v6
	v_mul_f32_e32 v7, v97, v7
	v_med3_f32 v6, v6, s33, v214
	v_med3_f32 v7, v7, s33, v214
	v_mov_b32_e32 v8, v2
	v_cvt_pk_fp8_f32 v8, v6, v7
	s_waitcnt vmcnt(19)
	v_lshlrev_b32_e32 v6, 16, v102
	s_waitcnt vmcnt(18)
	v_lshlrev_b32_e32 v7, 16, v103
	v_fma_f32 v6, -v95, v7, v6
	v_cvt_pk_fp8_f32 v8, 0, 0 op_sel:[0,0,1]
	v_and_b32_e32 v7, 0xffff0000, v102
	global_store_short v[4:5], v8, off offset:1536
	v_and_b32_e32 v8, 0xffff0000, v103
	v_fma_f32 v7, -v95, v8, v7
	v_mul_f32_e32 v8, v7, v7
	v_fmac_f32_e32 v8, v6, v6
	s_nop 1
	v_mov_b32_dpp v9, v8 quad_perm:[1,0,3,2] row_mask:0xf bank_mask:0xf
	s_waitcnt lgkmcnt(0)
	v_add_f32_e32 v8, v8, v9
	s_nop 1
	v_mov_b32_dpp v9, v8 quad_perm:[2,3,0,1] row_mask:0xf bank_mask:0xf
	s_waitcnt lgkmcnt(0)
	v_add_f32_e32 v8, v8, v9
	s_nop 1
	v_mov_b32_dpp v9, v8 row_half_mirror row_mask:0xf bank_mask:0xf
	s_waitcnt lgkmcnt(0)
	v_add_f32_e32 v8, v8, v9
	s_nop 1
	v_mov_b32_dpp v9, v8 row_mirror row_mask:0xf bank_mask:0xf
	s_waitcnt lgkmcnt(0)
	v_add_f32_e32 v8, v8, v9
	v_mov_b32_e32 v9, v8
	s_nop 1
	v_permlane16_swap_b32_e32 v8, v9
	s_waitcnt lgkmcnt(0)
	v_add_f32_e32 v8, v8, v9
	v_mov_b32_e32 v9, v8
	s_nop 1
	v_permlane32_swap_b32_e32 v8, v9
	s_waitcnt lgkmcnt(0)
	v_add_f32_e32 v8, v8, v9
	v_fmamk_f32 v8, v8, 0x3c000000, v210
	v_cmp_gt_f32_e32 vcc, s16, v8
	v_mul_f32_e32 v9, 0x4f800000, v8
	s_nop 0
	v_cndmask_b32_e32 v8, v8, v9, vcc
	v_sqrt_f32_e32 v9, v8
	s_nop 0
	v_add_u32_e32 v10, -1, v9
	v_fma_f32 v11, -v10, v9, v8
	v_cmp_ge_f32_e64 s[2:3], 0, v11
	v_add_u32_e32 v11, 1, v9
	s_nop 0
	v_cndmask_b32_e64 v10, v9, v10, s[2:3]
	v_fma_f32 v9, -v11, v9, v8
	v_cmp_lt_f32_e64 s[2:3], 0, v9
	s_nop 1
	v_cndmask_b32_e64 v9, v10, v11, s[2:3]
	v_mul_f32_e32 v10, 0x37800000, v9
	v_cndmask_b32_e32 v9, v9, v10, vcc
	v_cmp_class_f32_e32 vcc, v8, v211
	s_nop 1
	v_cndmask_b32_e32 v8, v9, v8, vcc
	v_div_scale_f32 v9, s[0:1], v8, v8, 1.0
	v_rcp_f32_e32 v10, v9
	s_nop 0
	v_fma_f32 v11, -v9, v10, 1.0
	v_fmac_f32_e32 v10, v11, v10
	v_div_scale_f32 v11, vcc, 1.0, v8, 1.0
	v_mul_f32_e32 v12, v11, v10
	v_fma_f32 v13, -v9, v12, v11
	v_fmac_f32_e32 v12, v13, v10
	v_fma_f32 v9, -v9, v12, v11
	v_div_fmas_f32 v9, v9, v10, v12
	v_div_fixup_f32 v8, v9, v8, 1.0
	v_mul_f32_e32 v6, v6, v8
	v_mul_f32_e32 v7, v7, v8
	v_mul_f32_e32 v6, v96, v6
	v_mul_f32_e32 v7, v97, v7
	v_med3_f32 v6, v6, s33, v214
	v_med3_f32 v7, v7, s33, v214
	v_mov_b32_e32 v8, v2
	v_cvt_pk_fp8_f32 v8, v6, v7
	s_waitcnt vmcnt(18)
	v_lshlrev_b32_e32 v6, 16, v100
	s_waitcnt vmcnt(17)
	v_lshlrev_b32_e32 v7, 16, v101
	v_fma_f32 v6, -v95, v7, v6
	v_cvt_pk_fp8_f32 v8, 0, 0 op_sel:[0,0,1]
	v_and_b32_e32 v7, 0xffff0000, v100
	global_store_short v[4:5], v8, off offset:1664
	v_and_b32_e32 v8, 0xffff0000, v101
	v_fma_f32 v7, -v95, v8, v7
	v_mul_f32_e32 v8, v7, v7
	v_fmac_f32_e32 v8, v6, v6
	s_nop 1
	v_mov_b32_dpp v9, v8 quad_perm:[1,0,3,2] row_mask:0xf bank_mask:0xf
	s_waitcnt lgkmcnt(0)
; #define GAS __attribute__((address_space(1)))
; __device__ __forceinline__ unsigned pk2(float lo, float hi) { f32x2_m v = {lo, hi}; bf16x2_m b = __builtin_convertvector(v, bf16x2_m); return __builtin_bit_cast(unsigned, b); }
; __device__ __forceinline__ float bflo(unsigned w) { return __uint_as_float(w << 16); }
; __device__ __forceinline__ float bfhi(unsigned w) { return __uint_as_float(w & 0xffff0000u); }
; __device__ __forceinline__ float wave_sum(float v) {
; #pragma unroll
;     for (int o = 1; o < 64; o <<= 1) v += __shfl_xor(v, o);
;     return v;
; }
; template <bool F8> __device__ __forceinline__ void mix_phase(const Ctx& C, const bf16* YCONV, const bf16* YSWA, const bf16* ODIFF, const float* conv_g, const float* swa_g, const float* lq1, const float* lk1, const float* lq2, const float* lk2, ...
;     ...
;             for (int h = 0; h < 6; ++h) { const unsigned a = oa[q][h], bq = ob[q][h];
;                 const float v0 = bflo(a) - lam * bflo(bq), v1 = bfhi(a) - lam * bfhi(bq);
;                 const float r = 1.0f / sqrtf(wave_sum(v0 * v0 + v1 * v1) * (1.0f / 128.0f) + LN_EPS);
;                 if constexpr (F8) *(GAS unsigned short*)(MIX8 + (size_t)m * DM + 1280 + 128 * h + 2 * l) = (unsigned short)pk4_fp8m(v0 * r * gA, v1 * r * gB, 0.f, 0.f);
;                 else *(GAS unsigned*)(MIX + (size_t)m * DM + 1280 + 128 * h + 2 * l) = pk2(v0 * r * gA, v1 * r * gB); } }
	v_add_f32_e32 v8, v8, v9
	s_nop 1
	v_mov_b32_dpp v9, v8 quad_perm:[2,3,0,1] row_mask:0xf bank_mask:0xf
	s_waitcnt lgkmcnt(0)
	v_add_f32_e32 v8, v8, v9
	s_nop 1
	v_mov_b32_dpp v9, v8 row_half_mirror row_mask:0xf bank_mask:0xf
	s_waitcnt lgkmcnt(0)
	v_add_f32_e32 v8, v8, v9
	s_nop 1
	v_mov_b32_dpp v9, v8 row_mirror row_mask:0xf bank_mask:0xf
	s_waitcnt lgkmcnt(0)
	v_add_f32_e32 v8, v8, v9
	v_mov_b32_e32 v9, v8
	s_nop 1
	v_permlane16_swap_b32_e32 v8, v9
	s_waitcnt lgkmcnt(0)
	v_add_f32_e32 v8, v8, v9
	v_mov_b32_e32 v9, v8
	s_nop 1
	v_permlane32_swap_b32_e32 v8, v9
	s_waitcnt lgkmcnt(0)
	v_add_f32_e32 v8, v8, v9
	v_fmamk_f32 v8, v8, 0x3c000000, v210
	v_cmp_gt_f32_e32 vcc, s16, v8
	v_mul_f32_e32 v9, 0x4f800000, v8
	s_nop 0
	v_cndmask_b32_e32 v8, v8, v9, vcc
	v_sqrt_f32_e32 v9, v8
	s_nop 0
	v_add_u32_e32 v10, -1, v9
	v_fma_f32 v11, -v10, v9, v8
	v_cmp_ge_f32_e64 s[2:3], 0, v11
	v_add_u32_e32 v11, 1, v9
	s_nop 0
	v_cndmask_b32_e64 v10, v9, v10, s[2:3]
	v_fma_f32 v9, -v11, v9, v8
	v_cmp_lt_f32_e64 s[2:3], 0, v9
	s_nop 1
	v_cndmask_b32_e64 v9, v10, v11, s[2:3]
	v_mul_f32_e32 v10, 0x37800000, v9
	v_cndmask_b32_e32 v9, v9, v10, vcc
	v_cmp_class_f32_e32 vcc, v8, v211
	s_nop 1
	v_cndmask_b32_e32 v8, v9, v8, vcc
	v_div_scale_f32 v9, s[0:1], v8, v8, 1.0
	v_rcp_f32_e32 v10, v9
	s_nop 0
	v_fma_f32 v11, -v9, v10, 1.0
	v_fmac_f32_e32 v10, v11, v10
	v_div_scale_f32 v11, vcc, 1.0, v8, 1.0
	v_mul_f32_e32 v12, v11, v10
	v_fma_f32 v13, -v9, v12, v11
	v_fmac_f32_e32 v12, v13, v10
	v_fma_f32 v9, -v9, v12, v11
	v_div_fmas_f32 v9, v9, v10, v12
	v_div_fixup_f32 v8, v9, v8, 1.0
	v_mul_f32_e32 v6, v6, v8
	v_mul_f32_e32 v7, v7, v8
	v_mul_f32_e32 v6, v96, v6
	v_mul_f32_e32 v7, v97, v7
	v_med3_f32 v6, v6, s33, v214
	v_med3_f32 v7, v7, s33, v214
	v_mov_b32_e32 v8, v2
	v_cvt_pk_fp8_f32 v8, v6, v7
	s_waitcnt vmcnt(17)
	v_lshlrev_b32_e32 v6, 16, v98
	s_waitcnt vmcnt(16)
	v_lshlrev_b32_e32 v7, 16, v99
	v_fma_f32 v6, -v95, v7, v6
	v_cvt_pk_fp8_f32 v8, 0, 0 op_sel:[0,0,1]
	v_and_b32_e32 v7, 0xffff0000, v98
	global_store_short v[4:5], v8, off offset:1792
	v_and_b32_e32 v8, 0xffff0000, v99
	v_fma_f32 v7, -v95, v8, v7
	v_mul_f32_e32 v8, v7, v7
	v_fmac_f32_e32 v8, v6, v6
	s_nop 1
	v_mov_b32_dpp v9, v8 quad_perm:[1,0,3,2] row_mask:0xf bank_mask:0xf
	s_waitcnt lgkmcnt(0)
	v_add_f32_e32 v8, v8, v9
	s_nop 1
	v_mov_b32_dpp v9, v8 quad_perm:[2,3,0,1] row_mask:0xf bank_mask:0xf
	s_waitcnt lgkmcnt(0)
	v_add_f32_e32 v8, v8, v9
	s_nop 1
	v_mov_b32_dpp v9, v8 row_half_mirror row_mask:0xf bank_mask:0xf
	s_waitcnt lgkmcnt(0)
	v_add_f32_e32 v8, v8, v9
	s_nop 1
	v_mov_b32_dpp v9, v8 row_mirror row_mask:0xf bank_mask:0xf
	s_waitcnt lgkmcnt(0)
	v_add_f32_e32 v8, v8, v9
	v_mov_b32_e32 v9, v8
	s_nop 1
	v_permlane16_swap_b32_e32 v8, v9
	s_waitcnt lgkmcnt(0)
	v_add_f32_e32 v8, v8, v9
	v_mov_b32_e32 v9, v8
	s_nop 1
	v_permlane32_swap_b32_e32 v8, v9
	s_waitcnt lgkmcnt(0)
	v_add_f32_e32 v8, v8, v9
	v_fmamk_f32 v8, v8, 0x3c000000, v210
	v_cmp_gt_f32_e32 vcc, s16, v8
	v_mul_f32_e32 v9, 0x4f800000, v8
	s_nop 0
	v_cndmask_b32_e32 v8, v8, v9, vcc
	v_sqrt_f32_e32 v9, v8
	s_nop 0
	v_add_u32_e32 v10, -1, v9
	v_fma_f32 v11, -v10, v9, v8
	v_cmp_ge_f32_e64 s[2:3], 0, v11
	v_add_u32_e32 v11, 1, v9
	s_nop 0
	v_cndmask_b32_e64 v10, v9, v10, s[2:3]
	v_fma_f32 v9, -v11, v9, v8
	v_cmp_lt_f32_e64 s[2:3], 0, v9
	s_nop 1
	v_cndmask_b32_e64 v9, v10, v11, s[2:3]
	v_mul_f32_e32 v10, 0x37800000, v9
	v_cndmask_b32_e32 v9, v9, v10, vcc
	v_cmp_class_f32_e32 vcc, v8, v211
	s_nop 1
	v_cndmask_b32_e32 v8, v9, v8, vcc
	v_div_scale_f32 v10, s[0:1], v8, v8, 1.0
	v_rcp_f32_e32 v9, v10
	s_nop 0
	v_fma_f32 v11, -v10, v9, 1.0
	v_fmac_f32_e32 v9, v11, v9
	v_div_scale_f32 v11, vcc, 1.0, v8, 1.0
	v_mul_f32_e32 v12, v11, v9
	v_fma_f32 v13, -v10, v12, v11
	v_fmac_f32_e32 v12, v13, v9
	v_fma_f32 v10, -v10, v12, v11
	v_div_fmas_f32 v9, v10, v9, v12
	v_div_fixup_f32 v8, v9, v8, 1.0
	v_mul_f32_e32 v6, v6, v8
	v_mul_f32_e32 v7, v7, v8
	v_mul_f32_e32 v6, v96, v6
	v_mul_f32_e32 v7, v97, v7
	v_med3_f32 v6, v6, s33, v214
	v_med3_f32 v7, v7, s33, v214
	v_mov_b32_e32 v8, v2
	v_cvt_pk_fp8_f32 v8, v6, v7
	v_cvt_pk_fp8_f32 v8, 0, 0 op_sel:[0,0,1]
	global_store_short v[4:5], v8, off offset:1920
	s_cbranch_scc0 .LBB0_723
